# speedup vs baseline: 1.0119x; 1.0090x over previous
.LBB7_4:
	s_load_dwordx4 s[4:7], s[0:1], 0x60
	s_load_dword s3, s[0:1], 0x70
	s_ashr_i32 s2, s2, 3
	s_add_i32 s2, s16, s2
	s_abs_i32 s16, s2
	s_waitcnt lgkmcnt(0)
	s_abs_i32 s17, s7
	v_cvt_f32_u32_e32 v1, s17
	s_xor_b32 s18, s2, s7
	s_ashr_i32 s19, s18, 31
	s_sub_i32 s18, 0, s17
	v_rcp_iflag_f32_e32 v1, v1
	v_and_b32_e32 v12, 31, v0
	v_mov_b32_e32 v11, 0
	v_mul_f32_e32 v1, 0x4f7ffffe, v1
	v_cvt_u32_f32_e32 v1, v1
	s_nop 2
	v_readfirstlane_b32 s20, v1
	s_mul_i32 s18, s18, s20
	s_mul_hi_u32 s18, s20, s18
	s_add_i32 s20, s20, s18
	s_mul_hi_u32 s18, s16, s20
	s_mul_i32 s20, s18, s17
	s_sub_i32 s16, s16, s20
	s_add_i32 s21, s18, 1
	s_sub_i32 s20, s16, s17
	s_cmp_ge_u32 s16, s17
	s_cselect_b32 s18, s21, s18
	s_cselect_b32 s16, s20, s16
	s_add_i32 s20, s18, 1
	s_cmp_ge_u32 s16, s17
	s_cselect_b32 s16, s20, s18
	s_abs_i32 s18, s3
	v_cvt_f32_u32_e32 v1, s18
	s_xor_b32 s16, s16, s19
	s_sub_i32 s19, s16, s19
	s_mul_i32 s16, s19, s7
	v_rcp_iflag_f32_e32 v1, v1
	s_sub_i32 s17, 0, s18
	s_sub_i32 s2, s2, s16
	s_lshl_b32 s2, s2, 6
	v_mul_f32_e32 v1, 0x4f7ffffe, v1
	v_cvt_u32_f32_e32 v1, v1
	s_abs_i32 s21, s19
	s_ashr_i32 s20, s3, 31
	s_ashr_i32 s7, s19, 31
	v_readfirstlane_b32 s16, v1
	v_lshrrev_b32_e32 v1, 1, v0
	s_mul_i32 s17, s17, s16
	v_and_b32_e32 v1, 32, v1
	s_mul_hi_u32 s17, s16, s17
	v_or_b32_e32 v15, v1, v12
	s_add_i32 s16, s16, s17
	v_or_b32_e32 v2, s2, v15
	s_mul_hi_u32 s22, s21, s16
	v_cmp_gt_i32_e32 vcc, s4, v2
	s_nop 7
	v_mov_b32_e32 v13, 0
	s_and_saveexec_b64 s[16:17], vcc
	s_cbranch_execz .LBB7_6
	s_load_dwordx2 s[24:25], s[0:1], 0x30
	v_ashrrev_i32_e32 v3, 31, v2
	s_waitcnt lgkmcnt(0)
	v_lshl_add_u64 v[2:3], v[2:3], 2, s[24:25]
	global_load_dword v13, v[2:3], off
.LBB7_6:
	s_or_b64 exec, exec, s[16:17]
	s_xor_b32 s7, s7, s20
	s_mul_i32 s20, s22, s18
	s_sub_i32 s20, s21, s20
	s_add_i32 s21, s22, 1
	s_sub_i32 s24, s20, s18
	s_cmp_ge_u32 s20, s18
	s_cselect_b32 s21, s21, s22
	s_cselect_b32 s20, s24, s20
	s_add_i32 s22, s21, 1
	s_cmp_ge_u32 s20, s18
	s_cselect_b32 s18, s22, s21
	s_xor_b32 s18, s18, s7
	s_sub_i32 s7, s18, s7
	s_load_dwordx2 s[16:17], s[0:1], 0x10
	s_load_dword s23, s[0:1], 0x28
	s_mul_i32 s3, s7, s3
	s_sub_i32 s3, s19, s3
	v_lshlrev_b32_e32 v2, 3, v0
	s_mul_i32 s18, s7, s5
	s_lshl_b32 s3, s3, 6
	v_lshrrev_b32_e32 v32, 2, v0
	v_and_b32_e32 v10, 24, v2
	s_ashr_i32 s19, s18, 31
	v_or_b32_e32 v6, s3, v32
	s_ashr_i32 s7, s3, 31
	v_lshl_add_u64 v[2:3], s[18:19], 0, v[10:11]
	s_waitcnt lgkmcnt(0)
	s_mul_i32 s7, s16, s7
	v_mad_u64_u32 v[4:5], s[18:19], s16, v6, v[2:3]
	v_mul_lo_u32 v6, s17, v6
	v_add3_u32 v5, v6, v5, s7
	v_add_u32_e32 v6, s2, v32
	s_add_i32 s7, s4, -1
	v_min_i32_e32 v6, s7, v6
	v_mad_i64_i32 v[6:7], s[16:17], v6, s23, v[2:3]
	v_lshlrev_b64 v[6:7], 1, v[6:7]
	v_lshlrev_b64 v[8:9], 1, v[4:5]
	v_lshl_add_u64 v[4:5], s[12:13], 0, v[6:7]
	global_load_dwordx4 v[70:73], v[4:5], off
	v_lshl_add_u64 v[6:7], s[14:15], 0, v[6:7]
	v_lshl_add_u64 v[2:3], s[8:9], 0, v[8:9]
	global_load_dwordx4 v[74:77], v[6:7], off
	global_load_dwordx4 v[78:81], v[2:3], off
	v_lshl_add_u64 v[8:9], s[10:11], 0, v[8:9]
	global_load_dwordx4 v[82:85], v[8:9], off
	s_load_dwordx2 s[8:9], s[0:1], 0x38
	v_and_b32_e32 v11, 32, v32
	v_mul_u32_u24_e32 v32, 40, v32
	v_lshlrev_b32_e32 v10, 1, v10
	v_bfe_u32 v14, v0, 5, 1
	v_lshl_add_u32 v10, v32, 1, v10
	s_ashr_i32 s7, s5, 31
	s_lshr_b32 s7, s7, 27
	s_add_i32 s5, s5, s7
	s_ashr_i32 s5, s5, 5
	s_add_i32 s7, s5, -1
	s_min_i32 s10, s7, 2
	s_lshl_b32 s10, s10, 5
	s_ashr_i32 s11, s10, 31
	s_lshl_b64 s[10:11], s[10:11], 1
	v_lshl_add_u64 v[16:17], v[2:3], 0, s[10:11]
	global_load_dwordx4 v[18:21], v[2:3], off offset:64
	global_load_dwordx4 v[22:25], v[8:9], off offset:64
	global_load_dwordx4 v[26:29], v[4:5], off offset:64
	global_load_dwordx4 v[34:37], v[6:7], off offset:64
	global_load_dwordx4 v[30:33], v[16:17], off
	v_lshl_add_u64 v[16:17], v[8:9], 0, s[10:11]
	global_load_dwordx4 v[38:41], v[16:17], off
	v_lshl_add_u64 v[16:17], v[4:5], 0, s[10:11]
	global_load_dwordx4 v[42:45], v[16:17], off
	v_lshl_add_u64 v[16:17], v[6:7], 0, s[10:11]
	global_load_dwordx4 v[46:49], v[16:17], off
	v_accvgpr_write_b32 a0, 0
	v_accvgpr_write_b32 a1, 0
	v_accvgpr_write_b32 a2, 0
	v_accvgpr_write_b32 a3, 0
	v_accvgpr_write_b32 a4, 0
	v_accvgpr_write_b32 a5, 0
	v_accvgpr_write_b32 a6, 0
	v_accvgpr_write_b32 a7, 0
	v_accvgpr_write_b32 a8, 0
	v_accvgpr_write_b32 a9, 0
	v_accvgpr_write_b32 a10, 0
	v_accvgpr_write_b32 a11, 0
	v_accvgpr_write_b32 a12, 0
	v_accvgpr_write_b32 a13, 0
	v_accvgpr_write_b32 a14, 0
	v_accvgpr_write_b32 a15, 0
	s_waitcnt vmcnt(11)
	ds_write_b128 v10, v[70:73] offset:10240
	s_waitcnt vmcnt(10)
	ds_write_b128 v10, v[74:77] offset:15360
	s_waitcnt vmcnt(9)
	ds_write_b128 v10, v[78:81]
	s_waitcnt vmcnt(8)
	ds_write_b128 v10, v[82:85] offset:5120
	s_waitcnt lgkmcnt(0)
	s_barrier
	v_lshlrev_b32_e32 v17, 4, v14
	s_movk_i32 s10, 0x50
	v_or_b32_e32 v16, v11, v12
	v_mul_u32_u24_e32 v66, 0x50, v15
	v_mad_u32_u24 v15, v15, s10, v17
	v_mul_u32_u24_e32 v67, 0x50, v16
	v_mad_u32_u24 v16, v16, s10, v17
	ds_read_b128 v[58:61], v15 offset:15360
	ds_read_b128 v[50:53], v15 offset:10240
	ds_read_b128 v[54:57], v16
	ds_read_b128 v[62:65], v16 offset:5120
	s_nop 7
	s_mov_b32 s10, 0
	v_add_u32_e32 v15, v17, v67
	v_add_u32_e32 v16, v17, v66

.LBB7_11:
	s_endpgm
	s_endpgm
	s_endpgm
	s_endpgm
	s_endpgm
	s_endpgm
	s_endpgm
	s_endpgm
	s_endpgm
	s_endpgm
	s_endpgm
	s_endpgm
	s_endpgm
	s_endpgm
	s_endpgm
	s_endpgm
	s_endpgm
	s_endpgm
	s_endpgm
	s_endpgm
	s_endpgm
	s_endpgm
	s_endpgm
	s_endpgm
	s_endpgm
	s_endpgm
	s_endpgm
	s_endpgm
	s_endpgm
	s_endpgm
	s_endpgm
	s_endpgm
	s_endpgm
	s_endpgm
	s_endpgm
	s_endpgm
	s_endpgm
	s_endpgm
	s_endpgm
	s_endpgm
	s_endpgm
	s_endpgm
	s_endpgm
	s_endpgm
	s_endpgm
	s_endpgm
	s_endpgm
	s_endpgm

.LBB8_4:
	s_load_dwordx4 s[32:35], s[0:1], 0x18
	s_load_dword s36, s[0:1], 0x28
	s_load_dwordx4 s[4:7], s[0:1], 0x60
	s_load_dwordx2 s[14:15], s[0:1], 0x10
	s_ashr_i32 s2, s2, 3
	s_add_i32 s2, s3, s2
	s_abs_i32 s3, s2
	s_waitcnt lgkmcnt(0)
	s_abs_i32 s16, s6
	v_cvt_f32_u32_e32 v2, s16
	s_sub_i32 s18, 0, s16
	s_xor_b32 s17, s2, s6
	s_ashr_i32 s17, s17, 31
	v_rcp_iflag_f32_e32 v2, v2
	v_lshrrev_b32_e32 v1, 6, v0
	v_lshrrev_b32_e32 v3, 2, v0
	v_mov_b32_e32 v17, 0
	v_mul_f32_e32 v2, 0x4f7ffffe, v2
	v_cvt_u32_f32_e32 v2, v2
	v_and_b32_e32 v12, 31, v0
	s_nop 1
	v_readfirstlane_b32 s19, v2
	s_mul_i32 s18, s18, s19
	s_mul_hi_u32 s18, s19, s18
	s_add_i32 s19, s19, s18
	s_mul_hi_u32 s18, s3, s19
	s_mul_i32 s19, s18, s16
	s_sub_i32 s3, s3, s19
	s_add_i32 s20, s18, 1
	s_sub_i32 s19, s3, s16
	s_cmp_ge_u32 s3, s16
	s_cselect_b32 s18, s20, s18
	s_cselect_b32 s3, s19, s3
	s_add_i32 s19, s18, 1
	s_cmp_ge_u32 s3, s16
	s_cselect_b32 s3, s19, s18
	s_abs_i32 s16, s7
	v_cvt_f32_u32_e32 v2, s16
	s_xor_b32 s3, s3, s17
	s_sub_i32 s3, s3, s17
	s_mul_i32 s6, s3, s6
	v_rcp_iflag_f32_e32 v2, v2
	s_sub_i32 s19, 0, s16
	s_sub_i32 s18, s2, s6
	s_xor_b32 s17, s3, s7
	v_mul_f32_e32 v2, 0x4f7ffffe, v2
	v_cvt_u32_f32_e32 v2, v2
	s_ashr_i32 s2, s17, 31
	s_abs_i32 s20, s3
	s_nop 0
	v_readfirstlane_b32 s6, v2
	s_mul_i32 s19, s19, s6
	s_mul_hi_u32 s17, s6, s19
	s_add_i32 s6, s6, s17
	s_mul_hi_u32 s6, s20, s6
	s_mul_i32 s17, s6, s16
	s_sub_i32 s17, s20, s17
	s_add_i32 s19, s6, 1
	s_sub_i32 s20, s17, s16
	s_cmp_ge_u32 s17, s16
	s_cselect_b32 s6, s19, s6
	s_cselect_b32 s17, s20, s17
	s_add_i32 s19, s6, 1
	s_cmp_ge_u32 s17, s16
	s_cselect_b32 s6, s19, s6
	s_xor_b32 s6, s6, s2
	s_sub_i32 s2, s6, s2
	s_mul_i32 s6, s2, s7
	s_sub_i32 s3, s3, s6
	v_lshlrev_b32_e32 v2, 3, v0
	s_mul_i32 s6, s2, s4
	s_lshl_b32 s16, s3, 6
	v_and_b32_e32 v16, 24, v2
	s_ashr_i32 s7, s6, 31
	v_or_b32_e32 v6, s16, v3
	s_ashr_i32 s17, s16, 31
	v_lshl_add_u64 v[4:5], s[6:7], 0, v[16:17]
	v_lshlrev_b32_e32 v2, 5, v1
	v_lshl_or_b32 v2, s18, 7, v2
	s_mul_i32 s19, s14, s17
	v_mad_u64_u32 v[4:5], s[2:3], s14, v6, v[4:5]
	v_mul_lo_u32 v6, s15, v6
	v_add3_u32 v5, v6, v5, s19
	v_or_b32_e32 v14, v2, v12
	v_lshlrev_b64 v[6:7], 1, v[4:5]
	v_ashrrev_i32_e32 v15, 31, v14
	v_lshl_add_u64 v[4:5], s[10:11], 0, v[6:7]
	v_lshl_add_u64 v[6:7], s[8:9], 0, v[6:7]
	v_lshl_add_u64 v[14:15], v[14:15], 2, s[12:13]
	global_load_dwordx4 v[78:81], v[6:7], off
	global_load_dwordx4 v[82:85], v[4:5], off
	global_load_dword v13, v[14:15], off
	s_load_dwordx2 s[2:3], s[0:1], 0x38
	s_movk_i32 s9, 0x50
	v_lshlrev_b32_e32 v16, 1, v16
	v_and_b32_e32 v14, 63, v0
	s_nop 7
	v_bfe_u32 v15, v0, 5, 1
	v_mad_u32_u24 v17, v3, s9, v16
	s_mov_b32 s10, s36
	s_lshr_b32 s7, s7, 28
	v_lshl_or_b32 v10, s18, 2, v1
	s_add_i32 s6, s6, s7
	s_ashr_i32 s6, s6, 4
	s_waitcnt lgkmcnt(0)
	s_ashr_i32 s18, s10, 31
	s_lshr_b32 s18, s18, 28
	s_ashr_i32 s8, s4, 31
	s_add_i32 s10, s10, s18
	s_ashr_i32 s7, s6, 31
	s_lshr_b32 s8, s8, 27
	s_ashr_i32 s10, s10, 4
	v_mov_b32_e32 v8, s6
	v_mov_b32_e32 v9, s7
	s_add_i32 s4, s4, s8
	v_mad_i64_i32 v[8:9], s[6:7], v10, s10, v[8:9]
	s_ashr_i32 s4, s4, 5
	v_lshlrev_b64 v[10:11], 10, v[8:9]
	s_add_i32 s8, s4, -1
	v_lshl_or_b32 v10, v14, 4, v10
	s_min_i32 s11, s8, 2
	v_lshl_add_u64 v[8:9], s[32:33], 0, v[10:11]
	global_load_dwordx4 v[30:33], v[6:7], off offset:64
	global_load_dwordx4 v[22:25], v[4:5], off offset:64
	v_lshl_add_u64 v[10:11], s[34:35], 0, v[10:11]
	global_load_dwordx4 v[38:41], v[8:9], off
	global_load_dwordx4 v[18:21], v[8:9], off offset:1024
	global_load_dwordx4 v[54:57], v[10:11], off
	global_load_dwordx4 v[26:29], v[10:11], off offset:1024
	global_load_dwordx4 v[42:45], v[8:9], off offset:2048
	global_load_dwordx4 v[50:53], v[10:11], off offset:2048
	s_lshl_b32 s6, s11, 5
	s_ashr_i32 s7, s6, 31
	s_lshl_b64 s[6:7], s[6:7], 1
	v_lshl_add_u64 v[60:61], v[6:7], 0, s[6:7]
	v_lshl_add_u64 v[58:59], v[4:5], 0, s[6:7]
	global_load_dwordx4 v[46:49], v[60:61], off
	global_load_dwordx4 v[34:37], v[58:59], off
	v_accvgpr_write_b32 a0, 0
	v_accvgpr_write_b32 a1, 0
	v_accvgpr_write_b32 a2, 0
	v_accvgpr_write_b32 a3, 0
	v_accvgpr_write_b32 a4, 0
	v_accvgpr_write_b32 a5, 0
	v_accvgpr_write_b32 a6, 0
	v_accvgpr_write_b32 a7, 0
	v_accvgpr_write_b32 a8, 0
	v_accvgpr_write_b32 a9, 0
	v_accvgpr_write_b32 a10, 0
	v_accvgpr_write_b32 a11, 0
	v_accvgpr_write_b32 a12, 0
	v_accvgpr_write_b32 a13, 0
	v_accvgpr_write_b32 a14, 0
	v_accvgpr_write_b32 a15, 0
	v_accvgpr_write_b32 a16, 0
	v_accvgpr_write_b32 a17, 0
	v_accvgpr_write_b32 a18, 0
	v_accvgpr_write_b32 a19, 0
	v_accvgpr_write_b32 a20, 0
	v_accvgpr_write_b32 a21, 0
	v_accvgpr_write_b32 a22, 0
	v_accvgpr_write_b32 a23, 0
	v_accvgpr_write_b32 a24, 0
	v_accvgpr_write_b32 a25, 0
	v_accvgpr_write_b32 a26, 0
	v_accvgpr_write_b32 a27, 0
	v_accvgpr_write_b32 a28, 0
	v_accvgpr_write_b32 a29, 0
	v_accvgpr_write_b32 a30, 0
	v_accvgpr_write_b32 a31, 0
	s_waitcnt vmcnt(12)
	ds_write_b128 v17, v[78:81]
	s_waitcnt vmcnt(11)
	ds_write_b128 v17, v[82:85] offset:5120
	s_waitcnt lgkmcnt(0)
	s_barrier
	v_mul_u32_u24_e32 v17, 0x50, v3
	v_lshlrev_b32_e32 v3, 4, v15
	v_mad_u32_u24 v70, v12, s9, v3
	ds_read_b128 v[58:61], v70 offset:2560
	ds_read_b128 v[66:69], v70
	ds_read_b128 v[62:65], v70 offset:7680
	ds_read_b128 v[70:73], v70 offset:5120
	v_mul_u32_u24_e32 v74, 0x50, v12
	s_mov_b32 s6, 4
	s_nop 7
	v_add_u32_e32 v3, v3, v74
	v_add_u32_e32 v16, v16, v17

.LBB8_7:
	s_load_dwordx2 s[0:1], s[0:1], 0x40
	s_waitcnt vmcnt(7)
	v_mul_u32_u24_e32 v40, 0x2400, v1
	v_accvgpr_read_b32 v39, a0
	v_accvgpr_read_b32 v38, a1
	v_lshl_or_b32 v1, v12, 2, v40
	s_waitcnt lgkmcnt(0)
	s_mul_hi_u32 s4, s0, s16
	s_mul_i32 s6, s0, s17
	s_add_i32 s4, s4, s6
	s_mul_i32 s6, s1, s16
	s_add_i32 s7, s4, s6
	s_movk_i32 s4, 0x240
	s_waitcnt vmcnt(2)
	v_accvgpr_read_b32 v37, a2
	v_accvgpr_read_b32 v36, a3
	s_waitcnt vmcnt(0)
	v_fma_f32 v12, s5, v39, v13
	v_mad_u32_u24 v1, v15, s4, v1
	v_fma_f32 v15, s5, v38, v13
	v_accvgpr_read_b32 v35, a4
	v_accvgpr_read_b32 v34, a5
	s_barrier
	ds_write2_b32 v1, v12, v15 offset1:36
	v_fma_f32 v12, s5, v37, v13
	v_fma_f32 v15, s5, v36, v13
	v_accvgpr_read_b32 v33, a6
	v_accvgpr_read_b32 v32, a7
	ds_write2_b32 v1, v12, v15 offset0:72 offset1:108
	v_fma_f32 v12, s5, v35, v13
	v_fma_f32 v15, s5, v34, v13
	v_add_u32_e32 v34, 0x400, v1
	v_accvgpr_read_b32 v31, a8
	v_accvgpr_read_b32 v30, a9
	ds_write2_b32 v34, v12, v15 offset0:32 offset1:68
	v_fma_f32 v12, s5, v33, v13
	v_fma_f32 v15, s5, v32, v13
	v_accvgpr_read_b32 v29, a10
	v_accvgpr_read_b32 v28, a11
	ds_write2_b32 v34, v12, v15 offset0:104 offset1:140
	v_fma_f32 v12, s5, v31, v13
	v_fma_f32 v15, s5, v30, v13
	v_add_u32_e32 v30, 0x800, v1
	v_accvgpr_read_b32 v27, a12
	v_accvgpr_read_b32 v26, a13
	ds_write2_b32 v30, v12, v15 offset0:64 offset1:100
	v_fma_f32 v12, s5, v29, v13
	v_fma_f32 v15, s5, v28, v13
	v_accvgpr_read_b32 v25, a14
	v_accvgpr_read_b32 v24, a15
	ds_write2_b32 v30, v12, v15 offset0:136 offset1:172
	v_fma_f32 v12, s5, v27, v13
	v_fma_f32 v15, s5, v26, v13
	v_add_u32_e32 v26, 0xc00, v1
	v_accvgpr_read_b32 v23, a16
	v_accvgpr_read_b32 v22, a17
	ds_write2_b32 v26, v12, v15 offset0:96 offset1:132
	v_fma_f32 v12, s5, v25, v13
	v_fma_f32 v15, s5, v24, v13
	v_accvgpr_read_b32 v21, a18
	v_accvgpr_read_b32 v20, a19
	ds_write2_b32 v26, v12, v15 offset0:168 offset1:204
	v_fma_f32 v12, s5, v23, v13
	v_fma_f32 v15, s5, v22, v13
	v_add_u32_e32 v22, 0x1000, v1
	v_accvgpr_read_b32 v19, a20
	v_accvgpr_read_b32 v18, a21
	ds_write2_b32 v22, v12, v15 offset0:128 offset1:164
	v_fma_f32 v12, s5, v21, v13
	v_fma_f32 v15, s5, v20, v13
	v_accvgpr_read_b32 v17, a22
	v_accvgpr_read_b32 v16, a23
	ds_write2_b32 v22, v12, v15 offset0:200 offset1:236
	v_fma_f32 v12, s5, v19, v13
	v_fma_f32 v15, s5, v18, v13
	v_add_u32_e32 v18, 0x1400, v1
	v_accvgpr_read_b32 v11, a24
	v_accvgpr_read_b32 v10, a25
	v_accvgpr_read_b32 v9, a26
	v_accvgpr_read_b32 v8, a27
	v_accvgpr_read_b32 v7, a28
	v_accvgpr_read_b32 v6, a29
	v_accvgpr_read_b32 v5, a30
	v_accvgpr_read_b32 v4, a31
	s_mul_i32 s6, s0, s16
	ds_write2_b32 v18, v12, v15 offset0:160 offset1:196
	v_fma_f32 v12, s5, v17, v13
	v_fma_f32 v15, s5, v16, v13
	v_add_u32_e32 v16, 0x1600, v1
	ds_write2_b32 v16, v12, v15 offset0:104 offset1:140
	v_fma_f32 v11, s5, v11, v13
	v_fma_f32 v10, s5, v10, v13
	v_add_u32_e32 v12, 0x1800, v1
	v_fma_f32 v9, s5, v9, v13
	v_fma_f32 v8, s5, v8, v13
	v_fma_f32 v7, s5, v7, v13
	v_fma_f32 v6, s5, v6, v13
	v_fma_f32 v5, s5, v5, v13
	v_fmac_f32_e32 v13, s5, v4
	s_lshl_b64 s[4:5], s[6:7], 2
	ds_write2_b32 v12, v11, v10 offset0:192 offset1:228
	v_add_u32_e32 v10, 0x1c00, v1
	s_add_u32 s2, s2, s4
	v_ashrrev_i32_e32 v3, 31, v2
	ds_write2_b32 v10, v9, v8 offset0:8 offset1:44
	v_add_u32_e32 v8, 0x1e00, v1
	v_add_u32_e32 v1, 0x2000, v1
	s_addc_u32 s3, s3, s5
	v_lshlrev_b32_e32 v0, 4, v0
	ds_write2_b32 v1, v5, v13 offset0:40 offset1:76
	v_lshl_add_u64 v[2:3], v[2:3], 2, s[2:3]
	v_and_b32_e32 v0, 0x70, v0
	v_mov_b32_e32 v1, 0
	ds_write2_b32 v8, v7, v6 offset0:96 offset1:132
	v_lshrrev_b32_e32 v12, 3, v14
	v_lshl_add_u64 v[8:9], v[2:3], 0, v[0:1]
	v_or_b32_e32 v0, v40, v0
	s_movk_i32 s2, 0x90
	v_mad_u32_u24 v13, v12, s2, v0
	ds_read_b128 v[0:3], v13
	v_mad_u64_u32 v[4:5], s[2:3], s0, v12, 0
	v_mov_b32_e32 v6, v5
	v_mad_u64_u32 v[6:7], s[2:3], s1, v12, v[6:7]
	v_mov_b32_e32 v5, v6
	v_lshl_add_u64 v[10:11], v[4:5], 2, v[8:9]
	ds_read_b128 v[4:7], v13 offset:1152
	s_waitcnt lgkmcnt(1)
	global_store_dwordx4 v[10:11], v[0:3], off sc1
	s_nop 1
	v_or_b32_e32 v3, 8, v12
	v_mad_u64_u32 v[0:1], s[2:3], s0, v3, 0
	v_mov_b32_e32 v2, v1
	v_mad_u64_u32 v[2:3], s[2:3], s1, v3, v[2:3]
	v_mov_b32_e32 v1, v2
	v_lshl_add_u64 v[0:1], v[0:1], 2, v[8:9]
	s_waitcnt lgkmcnt(0)
	global_store_dwordx4 v[0:1], v[4:7], off sc1
	ds_read_b128 v[0:3], v13 offset:2304
	s_nop 0
	v_or_b32_e32 v7, 16, v12
	v_mad_u64_u32 v[4:5], s[2:3], s0, v7, 0
	v_mov_b32_e32 v6, v5
	v_mad_u64_u32 v[6:7], s[2:3], s1, v7, v[6:7]
	v_mov_b32_e32 v5, v6
	v_lshl_add_u64 v[10:11], v[4:5], 2, v[8:9]
	ds_read_b128 v[4:7], v13 offset:3456
	s_waitcnt lgkmcnt(1)
	global_store_dwordx4 v[10:11], v[0:3], off sc1
	s_nop 1
	v_or_b32_e32 v3, 24, v12
	v_mad_u64_u32 v[0:1], s[2:3], s0, v3, 0
	v_mov_b32_e32 v2, v1
	v_mad_u64_u32 v[2:3], s[2:3], s1, v3, v[2:3]
	v_mov_b32_e32 v1, v2
	v_lshl_add_u64 v[0:1], v[0:1], 2, v[8:9]
	s_waitcnt lgkmcnt(0)
	global_store_dwordx4 v[0:1], v[4:7], off sc1
	ds_read_b128 v[0:3], v13 offset:4608
	s_nop 0
	v_or_b32_e32 v7, 32, v12
	v_mad_u64_u32 v[4:5], s[2:3], s0, v7, 0
	v_mov_b32_e32 v6, v5
	v_mad_u64_u32 v[6:7], s[2:3], s1, v7, v[6:7]
	v_mov_b32_e32 v5, v6
	v_lshl_add_u64 v[10:11], v[4:5], 2, v[8:9]
	ds_read_b128 v[4:7], v13 offset:5760
	s_waitcnt lgkmcnt(1)
	global_store_dwordx4 v[10:11], v[0:3], off sc1
	s_nop 1
	v_or_b32_e32 v3, 40, v12
	v_mad_u64_u32 v[0:1], s[2:3], s0, v3, 0
	v_mov_b32_e32 v2, v1
	v_mad_u64_u32 v[2:3], s[2:3], s1, v3, v[2:3]
	v_mov_b32_e32 v1, v2
	v_lshl_add_u64 v[0:1], v[0:1], 2, v[8:9]
	s_waitcnt lgkmcnt(0)
	global_store_dwordx4 v[0:1], v[4:7], off sc1
	ds_read_b128 v[0:3], v13 offset:6912
	s_nop 0
	v_or_b32_e32 v7, 48, v12
	v_mad_u64_u32 v[4:5], s[2:3], s0, v7, 0
	v_mov_b32_e32 v6, v5
	v_mad_u64_u32 v[6:7], s[2:3], s1, v7, v[6:7]
	v_mov_b32_e32 v5, v6
	v_lshl_add_u64 v[10:11], v[4:5], 2, v[8:9]
	ds_read_b128 v[4:7], v13 offset:8064
	s_waitcnt lgkmcnt(1)
	global_store_dwordx4 v[10:11], v[0:3], off sc1
	s_nop 1
	v_or_b32_e32 v3, 56, v12
	v_mad_u64_u32 v[0:1], s[2:3], s0, v3, 0
	v_mov_b32_e32 v2, v1
	v_mad_u64_u32 v[2:3], s[0:1], s1, v3, v[2:3]
	v_mov_b32_e32 v1, v2
	v_lshl_add_u64 v[0:1], v[0:1], 2, v[8:9]
	s_waitcnt lgkmcnt(0)
	global_store_dwordx4 v[0:1], v[4:7], off sc1
	s_endpgm
	s_endpgm
	s_endpgm
	s_endpgm
	s_endpgm
	s_endpgm
	s_endpgm
	s_endpgm
	s_endpgm
	s_endpgm
	s_endpgm
	s_endpgm
	s_endpgm
	s_endpgm
	s_endpgm
	s_endpgm
	s_endpgm
	s_endpgm
	s_endpgm
	s_endpgm
	s_endpgm
	s_endpgm
	s_endpgm
	s_endpgm
	s_endpgm
	s_endpgm
	s_endpgm
	s_endpgm
	.section	.rodata,"a",@progbits
	.p2align	6, 0x0

.LBB9_4:
	s_load_dwordx4 s[32:35], s[0:1], 0x18
	s_load_dword s36, s[0:1], 0x28
	s_load_dwordx4 s[4:7], s[0:1], 0x60
	s_load_dwordx2 s[12:13], s[0:1], 0x10
	s_ashr_i32 s2, s2, 3
	s_add_i32 s2, s3, s2
	s_abs_i32 s3, s2
	s_waitcnt lgkmcnt(0)
	s_lshl_b32 s26, s7, 7
	s_lshl_b32 s24, s26, 5
	s_mov_b32 s27, 0
	s_cmp_eq_u32 s12, 0x800
	s_cselect_b32 s25, s24, 32
	s_cselect_b32 s26, s26, 1
	s_cselect_b32 s12, 32, s12
	s_abs_i32 s14, s6
	v_cvt_f32_u32_e32 v1, s14
	s_sub_i32 s16, 0, s14
	s_xor_b32 s15, s2, s6
	s_ashr_i32 s15, s15, 31
	v_rcp_iflag_f32_e32 v1, v1
	v_lshlrev_b32_e32 v3, 3, v0
	v_lshrrev_b32_e32 v2, 2, v0
	v_and_b32_e32 v8, 24, v3
	v_mul_f32_e32 v1, 0x4f7ffffe, v1
	v_cvt_u32_f32_e32 v1, v1
	v_mov_b32_e32 v9, 0
	v_lshlrev_b32_e32 v3, 1, v8
	v_lshrrev_b32_e32 v23, 6, v0
	v_readfirstlane_b32 s17, v1
	s_mul_i32 s16, s16, s17
	s_mul_hi_u32 s16, s17, s16
	s_add_i32 s17, s17, s16
	s_mul_hi_u32 s16, s3, s17
	s_mul_i32 s17, s16, s14
	s_sub_i32 s3, s3, s17
	s_add_i32 s18, s16, 1
	s_sub_i32 s17, s3, s14
	s_cmp_ge_u32 s3, s14
	s_cselect_b32 s16, s18, s16
	s_cselect_b32 s3, s17, s3
	s_add_i32 s17, s16, 1
	s_cmp_ge_u32 s3, s14
	s_cselect_b32 s3, s17, s16
	s_abs_i32 s16, s7
	v_cvt_f32_u32_e32 v1, s16
	s_xor_b32 s3, s3, s15
	s_sub_i32 s3, s3, s15
	s_mul_i32 s6, s3, s6
	v_rcp_iflag_f32_e32 v1, v1
	s_sub_i32 s17, 0, s16
	s_sub_i32 s14, s2, s6
	s_xor_b32 s15, s3, s7
	v_mul_f32_e32 v1, 0x4f7ffffe, v1
	v_cvt_u32_f32_e32 v1, v1
	s_ashr_i32 s2, s15, 31
	s_abs_i32 s18, s3
	v_and_b32_e32 v22, 31, v0
	v_readfirstlane_b32 s6, v1
	s_mul_i32 s17, s17, s6
	s_mul_hi_u32 s15, s6, s17
	s_add_i32 s6, s6, s15
	s_mul_hi_u32 s6, s18, s6
	s_mul_i32 s15, s6, s16
	s_sub_i32 s15, s18, s15
	s_add_i32 s17, s6, 1
	s_sub_i32 s18, s15, s16
	s_cmp_ge_u32 s15, s16
	s_cselect_b32 s6, s17, s6
	s_cselect_b32 s15, s18, s15
	s_add_i32 s17, s6, 1
	s_cmp_ge_u32 s15, s16
	s_cselect_b32 s6, s17, s6
	s_xor_b32 s6, s6, s2
	s_sub_i32 s16, s6, s2
	s_mul_i32 s2, s16, s7
	s_sub_i32 s2, s3, s2
	s_lshl_b32 s15, s2, 7
	s_mul_i32 s2, s16, s4
	s_mul_i32 s26, s2, s26
	s_ashr_i32 s3, s2, 31
	v_or_b32_e32 v1, s15, v2
	s_ashr_i32 s17, s15, 31
	v_lshl_add_u64 v[4:5], s[26:27], 0, v[8:9]
	s_mul_i32 s20, s12, s17
	v_mad_u64_u32 v[4:5], s[18:19], s12, v1, v[4:5]
	v_mul_lo_u32 v1, s13, v1
	s_lshl_b64 s[6:7], s[12:13], 6
	v_add3_u32 v5, v1, v5, s20
	v_lshl_add_u64 v[6:7], v[4:5], 0, s[6:7]
	v_lshlrev_b64 v[4:5], 1, v[4:5]
	v_lshl_add_u64 v[12:13], s[10:11], 0, v[4:5]
	v_lshl_add_u64 v[14:15], s[8:9], 0, v[4:5]
	s_lshl_b64 s[6:7], s[12:13], 7
	v_lshl_add_u64 v[10:11], v[6:7], 1, s[8:9]
	v_lshl_add_u64 v[16:17], v[12:13], 0, s[6:7]
	global_load_dwordx4 v[124:127], v[14:15], off
	global_load_dwordx4 v[128:131], v[12:13], off
	global_load_dwordx4 v[132:135], v[10:11], off
	global_load_dwordx4 v[136:139], v[16:17], off
	s_load_dwordx2 s[6:7], s[0:1], 0x38
	s_movk_i32 s9, 0x50
	v_and_b32_e32 v1, 63, v0
	s_nop 7
	v_bfe_u32 v24, v0, 5, 1
	v_mad_u32_u24 v112, v2, s9, v3
	s_mov_b32 s10, s36
	s_lshr_b32 s3, s3, 28
	s_ashr_i32 s8, s4, 31
	s_add_i32 s2, s2, s3
	s_lshr_b32 s8, s8, 27
	s_waitcnt lgkmcnt(0)
	s_ashr_i32 s12, s10, 31
	s_lshr_b32 s12, s12, 28
	s_ashr_i32 s2, s2, 4
	s_add_i32 s4, s4, s8
	s_add_i32 s10, s10, s12
	s_ashr_i32 s3, s2, 31
	s_ashr_i32 s4, s4, 5
	v_lshl_or_b32 v6, s14, 2, v23
	s_ashr_i32 s10, s10, 4
	v_mov_b32_e32 v4, s2
	v_mov_b32_e32 v5, s3
	s_add_i32 s8, s4, -1
	v_mad_i64_i32 v[4:5], s[2:3], v6, s10, v[4:5]
	s_min_i32 s11, s8, 2
	v_lshlrev_b64 v[4:5], 10, v[4:5]
	v_lshl_or_b32 v4, v1, 4, v4
	s_mul_i32 s2, s11, s25
	v_lshl_add_u64 v[18:19], s[32:33], 0, v[4:5]
	s_ashr_i32 s3, s2, 31
	s_lshl_b32 s28, s25, 1
	s_mov_b32 s29, 0
	v_lshl_add_u64 v[116:117], v[14:15], 0, s[28:29]
	v_lshl_add_u64 v[118:119], v[12:13], 0, s[28:29]
	v_lshl_add_u64 v[120:121], v[10:11], 0, s[28:29]
	v_lshl_add_u64 v[122:123], v[16:17], 0, s[28:29]
	global_load_dwordx4 v[44:47], v[116:117], off
	global_load_dwordx4 v[48:51], v[118:119], off
	global_load_dwordx4 v[32:35], v[120:121], off
	global_load_dwordx4 v[28:31], v[122:123], off
	v_lshl_add_u64 v[20:21], s[34:35], 0, v[4:5]
	global_load_dwordx4 v[64:67], v[18:19], off
	global_load_dwordx4 v[36:39], v[18:19], off offset:1024
	global_load_dwordx4 v[80:83], v[20:21], off
	global_load_dwordx4 v[40:43], v[20:21], off offset:1024
	global_load_dwordx4 v[68:71], v[18:19], off offset:2048
	global_load_dwordx4 v[76:79], v[20:21], off offset:2048
	s_lshl_b64 s[2:3], s[2:3], 1
	v_lshl_add_u64 v[26:27], v[14:15], 0, s[2:3]
	v_lshl_add_u64 v[4:5], v[10:11], 0, s[2:3]
	v_lshl_add_u64 v[6:7], v[12:13], 0, s[2:3]
	v_lshl_add_u64 v[8:9], v[16:17], 0, s[2:3]
	global_load_dwordx4 v[60:63], v[26:27], off
	global_load_dwordx4 v[56:59], v[4:5], off
	global_load_dwordx4 v[72:75], v[6:7], off
	global_load_dwordx4 v[52:55], v[8:9], off
	v_accvgpr_write_b32 a48, 0
	v_accvgpr_write_b32 a49, 0
	v_accvgpr_write_b32 a50, 0
	v_accvgpr_write_b32 a51, 0
	v_accvgpr_write_b32 a52, 0
	v_accvgpr_write_b32 a53, 0
	v_accvgpr_write_b32 a54, 0
	v_accvgpr_write_b32 a55, 0
	v_accvgpr_write_b32 a56, 0
	v_accvgpr_write_b32 a57, 0
	v_accvgpr_write_b32 a58, 0
	v_accvgpr_write_b32 a59, 0
	v_accvgpr_write_b32 a60, 0
	v_accvgpr_write_b32 a61, 0
	v_accvgpr_write_b32 a62, 0
	v_accvgpr_write_b32 a63, 0
	v_accvgpr_write_b32 a32, 0
	v_accvgpr_write_b32 a33, 0
	v_accvgpr_write_b32 a34, 0
	v_accvgpr_write_b32 a35, 0
	v_accvgpr_write_b32 a36, 0
	v_accvgpr_write_b32 a37, 0
	v_accvgpr_write_b32 a38, 0
	v_accvgpr_write_b32 a39, 0
	v_accvgpr_write_b32 a40, 0
	v_accvgpr_write_b32 a41, 0
	v_accvgpr_write_b32 a42, 0
	v_accvgpr_write_b32 a43, 0
	v_accvgpr_write_b32 a44, 0
	v_accvgpr_write_b32 a45, 0
	v_accvgpr_write_b32 a46, 0
	v_accvgpr_write_b32 a47, 0
	v_accvgpr_write_b32 a16, 0
	v_accvgpr_write_b32 a17, 0
	v_accvgpr_write_b32 a18, 0
	v_accvgpr_write_b32 a19, 0
	v_accvgpr_write_b32 a20, 0
	v_accvgpr_write_b32 a21, 0
	v_accvgpr_write_b32 a22, 0
	v_accvgpr_write_b32 a23, 0
	v_accvgpr_write_b32 a24, 0
	v_accvgpr_write_b32 a25, 0
	v_accvgpr_write_b32 a26, 0
	v_accvgpr_write_b32 a27, 0
	v_accvgpr_write_b32 a28, 0
	v_accvgpr_write_b32 a29, 0
	v_accvgpr_write_b32 a30, 0
	v_accvgpr_write_b32 a31, 0
	v_accvgpr_write_b32 a0, 0
	v_accvgpr_write_b32 a1, 0
	v_accvgpr_write_b32 a2, 0
	v_accvgpr_write_b32 a3, 0
	v_accvgpr_write_b32 a4, 0
	v_accvgpr_write_b32 a5, 0
	v_accvgpr_write_b32 a6, 0
	v_accvgpr_write_b32 a7, 0
	v_accvgpr_write_b32 a8, 0
	v_accvgpr_write_b32 a9, 0
	v_accvgpr_write_b32 a10, 0
	v_accvgpr_write_b32 a11, 0
	v_accvgpr_write_b32 a12, 0
	v_accvgpr_write_b32 a13, 0
	v_accvgpr_write_b32 a14, 0
	v_accvgpr_write_b32 a15, 0
	s_waitcnt vmcnt(17)
	ds_write_b128 v112, v[124:127]
	s_waitcnt vmcnt(16)
	ds_write_b128 v112, v[128:131] offset:10240
	s_waitcnt vmcnt(15)
	ds_write_b128 v112, v[132:135] offset:5120
	s_waitcnt vmcnt(14)
	ds_write_b128 v112, v[136:139] offset:15360
	s_waitcnt lgkmcnt(0)
	s_barrier
	v_lshlrev_b32_e32 v4, 4, v24
	v_mad_u32_u24 v6, v22, s9, v4
	ds_read_b128 v[84:87], v6 offset:7680
	ds_read_b128 v[92:95], v6 offset:5120
	ds_read_b128 v[88:91], v6 offset:17920
	ds_read_b128 v[96:99], v6 offset:15360
	ds_read_b128 v[100:103], v6 offset:2560
	ds_read_b128 v[104:107], v6
	ds_read_b128 v[108:111], v6 offset:12800
	ds_read_b128 v[112:115], v6 offset:10240
	v_mul_u32_u24_e32 v2, 0x50, v2
	v_mul_u32_u24_e32 v5, 0x50, v22
	s_mov_b32 s2, 4
	s_nop 7
	v_add_u32_e32 v25, v4, v5
	v_add_u32_e32 v26, v3, v2

.LBB9_7:
	s_load_dwordx4 s[0:3], s[0:1], 0x40
	s_ashr_i32 s4, s16, 31
	s_waitcnt vmcnt(1)
	v_lshlrev_b32_e32 v69, 5, v23
	v_lshl_or_b32 v70, s14, 7, v69
	v_mul_u32_u24_e32 v23, 0x2400, v23
	s_waitcnt lgkmcnt(0)
	s_mul_hi_u32 s8, s2, s16
	s_mul_i32 s4, s2, s4
	s_add_i32 s4, s8, s4
	s_mul_i32 s3, s3, s16
	s_add_i32 s3, s4, s3
	s_mul_i32 s2, s2, s16
	s_lshl_b64 s[2:3], s[2:3], 2
	s_add_u32 s4, s6, s2
	s_addc_u32 s6, s7, s3
	s_mul_hi_u32 s2, s0, s15
	s_mul_i32 s3, s0, s17
	s_add_i32 s2, s2, s3
	s_mul_i32 s3, s1, s15
	s_add_i32 s3, s2, s3
	s_mul_i32 s2, s0, s15
	s_lshl_b64 s[2:3], s[2:3], 2
	s_add_u32 s2, s4, s2
	s_addc_u32 s3, s6, s3
	v_ashrrev_i32_e32 v71, 31, v70
	v_lshlrev_b32_e32 v0, 4, v0
	v_accvgpr_read_b32 v68, a0
	v_accvgpr_read_b32 v67, a1
	v_lshl_add_u64 v[70:71], v[70:71], 2, s[2:3]
	v_and_b32_e32 v72, 0x70, v0
	v_mov_b32_e32 v73, 0
	v_lshl_or_b32 v22, v22, 2, v23
	s_movk_i32 s2, 0x240
	v_accvgpr_read_b32 v66, a2
	v_lshrrev_b32_e32 v69, 3, v1
	v_lshl_add_u64 v[0:1], v[70:71], 0, v[72:73]
	v_or_b32_e32 v70, v23, v72
	v_fma_f32 v23, s5, v68, 0
	v_mad_u32_u24 v68, v24, s2, v22
	v_fma_f32 v22, s5, v67, 0
	v_accvgpr_read_b32 v65, a3
	s_barrier
	ds_write_b32 v68, v22 offset:144
	v_fma_f32 v22, s5, v66, 0
	v_accvgpr_read_b32 v64, a4
	ds_write_b32 v68, v22 offset:288
	v_fma_f32 v22, s5, v65, 0
	v_accvgpr_read_b32 v63, a5
	ds_write_b32 v68, v22 offset:432
	v_fma_f32 v22, s5, v64, 0
	v_accvgpr_read_b32 v62, a6
	ds_write_b32 v68, v22 offset:1152
	v_fma_f32 v22, s5, v63, 0
	v_accvgpr_read_b32 v61, a7
	ds_write_b32 v68, v22 offset:1296
	v_fma_f32 v22, s5, v62, 0
	v_accvgpr_read_b32 v60, a8
	ds_write_b32 v68, v22 offset:1440
	v_fma_f32 v22, s5, v61, 0
	v_accvgpr_read_b32 v59, a9
	ds_write_b32 v68, v22 offset:1584
	v_fma_f32 v22, s5, v60, 0
	v_accvgpr_read_b32 v58, a10
	ds_write_b32 v68, v22 offset:2304
	v_fma_f32 v22, s5, v59, 0
	v_accvgpr_read_b32 v57, a11
	ds_write_b32 v68, v22 offset:2448
	v_fma_f32 v22, s5, v58, 0
	v_accvgpr_read_b32 v56, a12
	ds_write_b32 v68, v22 offset:2592
	v_fma_f32 v22, s5, v57, 0
	v_accvgpr_read_b32 v55, a13
	ds_write_b32 v68, v22 offset:2736
	v_fma_f32 v22, s5, v56, 0
	v_accvgpr_read_b32 v54, a14
	ds_write_b32 v68, v22 offset:3456
	v_fma_f32 v22, s5, v55, 0
	v_accvgpr_read_b32 v53, a15
	ds_write_b32 v68, v22 offset:3600
	v_fma_f32 v22, s5, v54, 0
	v_accvgpr_read_b32 v52, a16
	ds_write_b32 v68, v22 offset:3744
	v_fma_f32 v22, s5, v53, 0
	v_accvgpr_read_b32 v51, a17
	ds_write_b32 v68, v22 offset:3888
	v_fma_f32 v22, s5, v52, 0
	v_accvgpr_read_b32 v50, a18
	ds_write_b32 v68, v22 offset:4608
	v_fma_f32 v22, s5, v51, 0
	v_accvgpr_read_b32 v49, a19
	ds_write_b32 v68, v22 offset:4752
	v_fma_f32 v22, s5, v50, 0
	v_accvgpr_read_b32 v48, a20
	ds_write_b32 v68, v22 offset:4896
	v_fma_f32 v22, s5, v49, 0
	v_accvgpr_read_b32 v47, a21
	ds_write_b32 v68, v22 offset:5040
	v_fma_f32 v22, s5, v48, 0
	v_accvgpr_read_b32 v46, a22
	ds_write_b32 v68, v22 offset:5760
	v_fma_f32 v22, s5, v47, 0
	v_accvgpr_read_b32 v45, a23
	ds_write_b32 v68, v22 offset:5904
	v_fma_f32 v22, s5, v46, 0
	v_accvgpr_read_b32 v44, a24
	ds_write_b32 v68, v22 offset:6048
	v_fma_f32 v22, s5, v45, 0
	v_accvgpr_read_b32 v43, a25
	ds_write_b32 v68, v22 offset:6192
	v_fma_f32 v22, s5, v44, 0
	v_accvgpr_read_b32 v42, a26
	ds_write_b32 v68, v22 offset:6912
	v_fma_f32 v22, s5, v43, 0
	v_accvgpr_read_b32 v41, a27
	ds_write_b32 v68, v22 offset:7056
	v_fma_f32 v22, s5, v42, 0
	v_accvgpr_read_b32 v40, a28
	ds_write_b32 v68, v22 offset:7200
	v_fma_f32 v22, s5, v41, 0
	v_accvgpr_read_b32 v39, a29
	ds_write_b32 v68, v22 offset:7344
	v_fma_f32 v22, s5, v40, 0
	v_accvgpr_read_b32 v38, a30
	ds_write_b32 v68, v22 offset:8064
	v_fma_f32 v22, s5, v39, 0
	v_accvgpr_read_b32 v37, a31
	ds_write_b32 v68, v22 offset:8208
	v_fma_f32 v22, s5, v38, 0
	s_movk_i32 s4, 0x90
	ds_write_b32 v68, v22 offset:8352
	v_fma_f32 v22, s5, v37, 0
	v_mad_u32_u24 v71, v69, s4, v70
	ds_write_b32 v68, v23
	ds_write_b32 v68, v22 offset:8496
	ds_read_b128 v[38:41], v71
	v_mad_u64_u32 v[22:23], s[2:3], s0, v69, 0
	v_accvgpr_read_b32 v25, a43
	v_mov_b32_e32 v24, v23
	v_mad_u64_u32 v[42:43], s[2:3], s1, v69, v[24:25]
	v_mov_b32_e32 v23, v42
	v_or_b32_e32 v37, 8, v69
	v_lshl_add_u64 v[22:23], v[22:23], 2, v[0:1]
	v_mad_u32_u24 v46, v37, s4, v70
	ds_read_b128 v[42:45], v46
	s_waitcnt lgkmcnt(1)
	global_store_dwordx4 v[22:23], v[38:41], off sc1
	v_mad_u64_u32 v[22:23], s[2:3], s0, v37, 0
	v_mov_b32_e32 v24, v23
	v_mad_u64_u32 v[38:39], s[2:3], s1, v37, v[24:25]
	v_mov_b32_e32 v23, v38
	v_lshl_add_u64 v[22:23], v[22:23], 2, v[0:1]
	v_or_b32_e32 v37, 16, v69
	ds_read_b128 v[38:41], v46 offset:1152
	s_waitcnt lgkmcnt(1)
	global_store_dwordx4 v[22:23], v[42:45], off sc1
	v_mad_u64_u32 v[22:23], s[2:3], s0, v37, 0
	v_mov_b32_e32 v24, v23
	v_mad_u64_u32 v[42:43], s[2:3], s1, v37, v[24:25]
	v_mov_b32_e32 v23, v42
	v_lshl_add_u64 v[22:23], v[22:23], 2, v[0:1]
	v_or_b32_e32 v37, 24, v69
	ds_read_b128 v[42:45], v46 offset:2304
	s_waitcnt lgkmcnt(1)
	global_store_dwordx4 v[22:23], v[38:41], off sc1
	v_mad_u64_u32 v[22:23], s[2:3], s0, v37, 0
	v_mov_b32_e32 v24, v23
	v_mad_u64_u32 v[38:39], s[2:3], s1, v37, v[24:25]
	v_mov_b32_e32 v23, v38
	v_lshl_add_u64 v[22:23], v[22:23], 2, v[0:1]
	v_or_b32_e32 v37, 32, v69
	ds_read_b128 v[38:41], v46 offset:3456
	s_waitcnt lgkmcnt(1)
	global_store_dwordx4 v[22:23], v[42:45], off sc1
	v_mad_u64_u32 v[22:23], s[2:3], s0, v37, 0
	v_mov_b32_e32 v24, v23
	v_mad_u64_u32 v[42:43], s[2:3], s1, v37, v[24:25]
	v_mov_b32_e32 v23, v42
	v_lshl_add_u64 v[22:23], v[22:23], 2, v[0:1]
	v_or_b32_e32 v37, 40, v69
	ds_read_b128 v[42:45], v46 offset:4608
	s_waitcnt lgkmcnt(1)
	global_store_dwordx4 v[22:23], v[38:41], off sc1
	v_mad_u64_u32 v[22:23], s[2:3], s0, v37, 0
	v_mov_b32_e32 v24, v23
	v_mad_u64_u32 v[38:39], s[2:3], s1, v37, v[24:25]
	v_mov_b32_e32 v23, v38
	v_lshl_add_u64 v[22:23], v[22:23], 2, v[0:1]
	v_or_b32_e32 v37, 48, v69
	ds_read_b128 v[38:41], v46 offset:5760
	s_waitcnt lgkmcnt(1)
	global_store_dwordx4 v[22:23], v[42:45], off sc1
	v_mad_u64_u32 v[22:23], s[2:3], s0, v37, 0
	v_mov_b32_e32 v24, v23
	v_mad_u64_u32 v[42:43], s[2:3], s1, v37, v[24:25]
	v_mov_b32_e32 v23, v42
	v_lshl_add_u64 v[22:23], v[22:23], 2, v[0:1]
	v_or_b32_e32 v37, 56, v69
	ds_read_b128 v[42:45], v46 offset:6912
	s_waitcnt lgkmcnt(1)
	global_store_dwordx4 v[22:23], v[38:41], off sc1
	v_mad_u64_u32 v[22:23], s[2:3], s0, v37, 0
	v_mov_b32_e32 v24, v23
	v_mad_u64_u32 v[38:39], s[2:3], s1, v37, v[24:25]
	v_mov_b32_e32 v23, v38
	v_accvgpr_read_b32 v36, a32
	v_lshl_add_u64 v[22:23], v[22:23], 2, v[0:1]
	v_accvgpr_read_b32 v35, a33
	s_waitcnt lgkmcnt(0)
	global_store_dwordx4 v[22:23], v[42:45], off sc1
	v_fma_f32 v22, s5, v36, 0
	v_accvgpr_read_b32 v34, a34
	ds_write_b32 v68, v22
	v_fma_f32 v22, s5, v35, 0
	v_accvgpr_read_b32 v33, a35
	ds_write_b32 v68, v22 offset:144
	v_fma_f32 v22, s5, v34, 0
	v_accvgpr_read_b32 v32, a36
	ds_write_b32 v68, v22 offset:288
	v_fma_f32 v22, s5, v33, 0
	v_accvgpr_read_b32 v31, a37
	ds_write_b32 v68, v22 offset:432
	v_fma_f32 v22, s5, v32, 0
	v_accvgpr_read_b32 v30, a38
	ds_write_b32 v68, v22 offset:1152
	v_fma_f32 v22, s5, v31, 0
	v_accvgpr_read_b32 v29, a39
	ds_write_b32 v68, v22 offset:1296
	v_fma_f32 v22, s5, v30, 0
	v_accvgpr_read_b32 v28, a40
	ds_write_b32 v68, v22 offset:1440
	v_fma_f32 v22, s5, v29, 0
	v_accvgpr_read_b32 v27, a41
	ds_write_b32 v68, v22 offset:1584
	v_fma_f32 v22, s5, v28, 0
	v_accvgpr_read_b32 v26, a42
	ds_write_b32 v68, v22 offset:2304
	v_fma_f32 v22, s5, v27, 0
	v_accvgpr_read_b32 v17, a48
	v_accvgpr_read_b32 v16, a49
	v_accvgpr_read_b32 v15, a50
	v_accvgpr_read_b32 v14, a51
	v_accvgpr_read_b32 v13, a52
	v_accvgpr_read_b32 v12, a53
	v_accvgpr_read_b32 v11, a54
	v_accvgpr_read_b32 v10, a55
	v_accvgpr_read_b32 v9, a56
	v_accvgpr_read_b32 v8, a57
	v_accvgpr_read_b32 v7, a58
	v_accvgpr_read_b32 v6, a59
	v_accvgpr_read_b32 v5, a60
	v_accvgpr_read_b32 v4, a61
	v_accvgpr_read_b32 v3, a62
	v_accvgpr_read_b32 v2, a63
	v_accvgpr_read_b32 v21, a44
	v_accvgpr_read_b32 v20, a45
	v_accvgpr_read_b32 v19, a46
	v_accvgpr_read_b32 v18, a47
	ds_write_b32 v68, v22 offset:2448
	v_fma_f32 v22, s5, v26, 0
	ds_write_b32 v68, v22 offset:2592
	v_fma_f32 v22, s5, v25, 0
	v_fma_f32 v21, s5, v21, 0
	v_fma_f32 v20, s5, v20, 0
	v_fma_f32 v19, s5, v19, 0
	v_fma_f32 v18, s5, v18, 0
	v_fma_f32 v17, s5, v17, 0
	v_fma_f32 v16, s5, v16, 0
	v_fma_f32 v15, s5, v15, 0
	v_fma_f32 v14, s5, v14, 0
	v_fma_f32 v13, s5, v13, 0
	v_fma_f32 v12, s5, v12, 0
	v_fma_f32 v11, s5, v11, 0
	v_fma_f32 v10, s5, v10, 0
	v_fma_f32 v9, s5, v9, 0
	v_fma_f32 v8, s5, v8, 0
	v_fma_f32 v7, s5, v7, 0
	v_fma_f32 v6, s5, v6, 0
	v_fma_f32 v5, s5, v5, 0
	v_fma_f32 v4, s5, v4, 0
	v_fma_f32 v3, s5, v3, 0
	v_fma_f32 v2, s5, v2, 0
	ds_write_b32 v68, v22 offset:2736
	ds_write_b32 v68, v21 offset:3456
	ds_write_b32 v68, v20 offset:3600
	ds_write_b32 v68, v19 offset:3744
	ds_write_b32 v68, v18 offset:3888
	ds_write_b32 v68, v17 offset:4608
	ds_write_b32 v68, v16 offset:4752
	ds_write_b32 v68, v15 offset:4896
	ds_write_b32 v68, v14 offset:5040
	ds_write_b32 v68, v13 offset:5760
	ds_write_b32 v68, v12 offset:5904
	ds_write_b32 v68, v11 offset:6048
	ds_write_b32 v68, v10 offset:6192
	ds_write_b32 v68, v9 offset:6912
	ds_write_b32 v68, v8 offset:7056
	ds_write_b32 v68, v7 offset:7200
	ds_write_b32 v68, v6 offset:7344
	ds_write_b32 v68, v5 offset:8064
	ds_write_b32 v68, v4 offset:8208
	ds_write_b32 v68, v3 offset:8352
	ds_write_b32 v68, v2 offset:8496
	v_or_b32_e32 v9, 64, v69
	ds_read_b128 v[2:5], v71
	v_mad_u64_u32 v[6:7], s[2:3], s0, v9, 0
	v_mov_b32_e32 v8, v7
	v_mad_u64_u32 v[8:9], s[2:3], s1, v9, v[8:9]
	v_mov_b32_e32 v7, v8
	v_lshl_add_u64 v[10:11], v[6:7], 2, v[0:1]
	ds_read_b128 v[6:9], v46
	s_waitcnt lgkmcnt(1)
	global_store_dwordx4 v[10:11], v[2:5], off sc1
	s_nop 1
	v_or_b32_e32 v5, 0x48, v69
	v_mad_u64_u32 v[2:3], s[2:3], s0, v5, 0
	v_mov_b32_e32 v4, v3
	v_mad_u64_u32 v[4:5], s[2:3], s1, v5, v[4:5]
	v_mov_b32_e32 v3, v4
	v_lshl_add_u64 v[2:3], v[2:3], 2, v[0:1]
	s_waitcnt lgkmcnt(0)
	global_store_dwordx4 v[2:3], v[6:9], off sc1
	ds_read_b128 v[2:5], v46 offset:1152
	s_nop 0
	v_or_b32_e32 v9, 0x50, v69
	v_mad_u64_u32 v[6:7], s[2:3], s0, v9, 0
	v_mov_b32_e32 v8, v7
	v_mad_u64_u32 v[8:9], s[2:3], s1, v9, v[8:9]
	v_mov_b32_e32 v7, v8
	v_lshl_add_u64 v[10:11], v[6:7], 2, v[0:1]
	ds_read_b128 v[6:9], v46 offset:2304
	s_waitcnt lgkmcnt(1)
	global_store_dwordx4 v[10:11], v[2:5], off sc1
	s_nop 1
	v_or_b32_e32 v5, 0x58, v69
	v_mad_u64_u32 v[2:3], s[2:3], s0, v5, 0
	v_mov_b32_e32 v4, v3
	v_mad_u64_u32 v[4:5], s[2:3], s1, v5, v[4:5]
	v_mov_b32_e32 v3, v4
	v_lshl_add_u64 v[2:3], v[2:3], 2, v[0:1]
	s_waitcnt lgkmcnt(0)
	global_store_dwordx4 v[2:3], v[6:9], off sc1
	ds_read_b128 v[2:5], v46 offset:3456
	s_nop 0
	v_or_b32_e32 v9, 0x60, v69
	v_mad_u64_u32 v[6:7], s[2:3], s0, v9, 0
	v_mov_b32_e32 v8, v7
	v_mad_u64_u32 v[8:9], s[2:3], s1, v9, v[8:9]
	v_mov_b32_e32 v7, v8
	v_lshl_add_u64 v[10:11], v[6:7], 2, v[0:1]
	ds_read_b128 v[6:9], v46 offset:4608
	s_waitcnt lgkmcnt(1)
	global_store_dwordx4 v[10:11], v[2:5], off sc1
	s_nop 1
	v_or_b32_e32 v5, 0x68, v69
	v_mad_u64_u32 v[2:3], s[2:3], s0, v5, 0
	v_mov_b32_e32 v4, v3
	v_mad_u64_u32 v[4:5], s[2:3], s1, v5, v[4:5]
	v_mov_b32_e32 v3, v4
	v_lshl_add_u64 v[2:3], v[2:3], 2, v[0:1]
	s_waitcnt lgkmcnt(0)
	global_store_dwordx4 v[2:3], v[6:9], off sc1
	ds_read_b128 v[2:5], v46 offset:5760
	s_nop 0
	v_or_b32_e32 v9, 0x70, v69
	v_mad_u64_u32 v[6:7], s[2:3], s0, v9, 0
	v_mov_b32_e32 v8, v7
	v_mad_u64_u32 v[8:9], s[2:3], s1, v9, v[8:9]
	v_mov_b32_e32 v7, v8
	v_lshl_add_u64 v[10:11], v[6:7], 2, v[0:1]
	ds_read_b128 v[6:9], v46 offset:6912
	s_waitcnt lgkmcnt(1)
	global_store_dwordx4 v[10:11], v[2:5], off sc1
	s_nop 1
	v_or_b32_e32 v5, 0x78, v69
	v_mad_u64_u32 v[2:3], s[2:3], s0, v5, 0
	v_mov_b32_e32 v4, v3
	v_mad_u64_u32 v[4:5], s[0:1], s1, v5, v[4:5]
	v_mov_b32_e32 v3, v4
	v_lshl_add_u64 v[0:1], v[2:3], 2, v[0:1]
	s_waitcnt lgkmcnt(0)
	global_store_dwordx4 v[0:1], v[6:9], off sc1
	s_endpgm
	s_endpgm
	s_endpgm
	s_endpgm
	s_endpgm
	s_endpgm
	s_endpgm
	s_endpgm
	s_endpgm
	s_endpgm
	s_endpgm
	s_endpgm
	s_endpgm
	s_endpgm
	s_endpgm
	s_endpgm
	s_endpgm
	s_endpgm
	s_endpgm
	s_endpgm
	s_endpgm
	s_endpgm
	s_endpgm
	s_endpgm
	s_endpgm
	s_endpgm
	s_endpgm
	s_endpgm
	s_endpgm
	s_endpgm
	s_endpgm
	s_endpgm
	s_endpgm
	s_endpgm
	s_endpgm
	s_endpgm
	s_endpgm
	s_endpgm
	s_endpgm
	s_endpgm
	s_endpgm
	s_endpgm
	s_endpgm
	s_endpgm
	.section	.rodata,"a",@progbits
	.p2align	6, 0x0

.LBB10_4:
	s_load_dwordx4 s[32:35], s[0:1], 0x18
	s_load_dword s36, s[0:1], 0x28
	s_load_dwordx4 s[4:7], s[0:1], 0x60
	s_load_dwordx2 s[12:13], s[0:1], 0x10
	s_ashr_i32 s2, s2, 3
	s_add_i32 s2, s3, s2
	s_abs_i32 s3, s2
	s_waitcnt lgkmcnt(0)
	s_lshl_b32 s26, s7, 6
	s_lshl_b32 s24, s26, 5
	s_mov_b32 s27, 0
	s_cmp_eq_u32 s12, 0x800
	s_cselect_b32 s25, s24, 32
	s_cselect_b32 s26, s26, 1
	s_cselect_b32 s12, 32, s12
	s_abs_i32 s14, s6
	v_cvt_f32_u32_e32 v1, s14
	s_sub_i32 s16, 0, s14
	s_xor_b32 s15, s2, s6
	s_ashr_i32 s15, s15, 31
	v_rcp_iflag_f32_e32 v1, v1
	v_lshlrev_b32_e32 v2, 3, v0
	v_lshrrev_b32_e32 v13, 2, v0
	v_and_b32_e32 v14, 24, v2
	v_mul_f32_e32 v1, 0x4f7ffffe, v1
	v_cvt_u32_f32_e32 v1, v1
	v_mov_b32_e32 v15, 0
	v_lshrrev_b32_e32 v11, 6, v0
	v_and_b32_e32 v10, 31, v0
	v_readfirstlane_b32 s17, v1
	s_mul_i32 s16, s16, s17
	s_mul_hi_u32 s16, s17, s16
	s_add_i32 s17, s17, s16
	s_mul_hi_u32 s16, s3, s17
	s_mul_i32 s17, s16, s14
	s_sub_i32 s3, s3, s17
	s_add_i32 s18, s16, 1
	s_sub_i32 s17, s3, s14
	s_cmp_ge_u32 s3, s14
	s_cselect_b32 s16, s18, s16
	s_cselect_b32 s3, s17, s3
	s_add_i32 s17, s16, 1
	s_cmp_ge_u32 s3, s14
	s_cselect_b32 s3, s17, s16
	s_abs_i32 s16, s7
	v_cvt_f32_u32_e32 v1, s16
	s_xor_b32 s3, s3, s15
	s_sub_i32 s3, s3, s15
	s_mul_i32 s6, s3, s6
	v_rcp_iflag_f32_e32 v1, v1
	s_sub_i32 s17, 0, s16
	s_sub_i32 s14, s2, s6
	s_xor_b32 s15, s3, s7
	v_mul_f32_e32 v1, 0x4f7ffffe, v1
	v_cvt_u32_f32_e32 v1, v1
	s_ashr_i32 s2, s15, 31
	s_abs_i32 s18, s3
	s_nop 0
	v_readfirstlane_b32 s6, v1
	s_mul_i32 s17, s17, s6
	s_mul_hi_u32 s15, s6, s17
	s_add_i32 s6, s6, s15
	s_mul_hi_u32 s6, s18, s6
	s_mul_i32 s15, s6, s16
	s_sub_i32 s15, s18, s15
	s_add_i32 s17, s6, 1
	s_sub_i32 s18, s15, s16
	s_cmp_ge_u32 s15, s16
	s_cselect_b32 s6, s17, s6
	s_cselect_b32 s15, s18, s15
	s_add_i32 s17, s6, 1
	s_cmp_ge_u32 s15, s16
	s_cselect_b32 s6, s17, s6
	s_xor_b32 s6, s6, s2
	s_sub_i32 s16, s6, s2
	s_mul_i32 s2, s16, s7
	s_sub_i32 s2, s3, s2
	s_lshl_b32 s15, s2, 6
	s_mul_i32 s2, s16, s4
	s_mul_i32 s26, s2, s26
	s_ashr_i32 s3, s2, 31
	v_or_b32_e32 v1, s15, v13
	s_ashr_i32 s17, s15, 31
	v_lshl_add_u64 v[2:3], s[26:27], 0, v[14:15]
	s_mul_i32 s18, s12, s17
	v_mad_u64_u32 v[2:3], s[6:7], s12, v1, v[2:3]
	v_mul_lo_u32 v1, s13, v1
	v_add3_u32 v3, v1, v3, s18
	v_lshlrev_b64 v[4:5], 1, v[2:3]
	v_lshl_add_u64 v[2:3], s[10:11], 0, v[4:5]
	v_lshl_add_u64 v[4:5], s[8:9], 0, v[4:5]
	global_load_dwordx4 v[76:79], v[4:5], off
	global_load_dwordx4 v[88:91], v[2:3], off
	s_load_dwordx2 s[6:7], s[0:1], 0x38
	s_movk_i32 s9, 0x50
	v_lshlrev_b32_e32 v14, 1, v14
	v_and_b32_e32 v1, 63, v0
	s_nop 7
	v_bfe_u32 v12, v0, 5, 1
	v_mad_u32_u24 v15, v13, s9, v14
	s_mov_b32 s10, s36
	s_lshr_b32 s3, s3, 28
	s_add_i32 s2, s2, s3
	s_ashr_i32 s2, s2, 4
	s_ashr_i32 s8, s4, 31
	s_waitcnt lgkmcnt(0)
	s_ashr_i32 s12, s10, 31
	s_lshr_b32 s12, s12, 28
	s_add_i32 s10, s10, s12
	s_ashr_i32 s3, s2, 31
	s_lshr_b32 s8, s8, 27
	v_lshl_or_b32 v8, s14, 2, v11
	s_ashr_i32 s10, s10, 4
	v_mov_b32_e32 v6, s2
	v_mov_b32_e32 v7, s3
	s_add_i32 s4, s4, s8
	v_mad_i64_i32 v[6:7], s[2:3], v8, s10, v[6:7]
	s_ashr_i32 s4, s4, 5
	v_lshlrev_b64 v[8:9], 10, v[6:7]
	s_add_i32 s8, s4, -1
	v_lshl_or_b32 v8, v1, 4, v8
	s_min_i32 s11, s8, 2
	v_lshl_add_u64 v[6:7], s[32:33], 0, v[8:9]
	s_lshl_b32 s28, s25, 1
	s_mov_b32 s29, 0
	v_lshl_add_u64 v[72:73], v[4:5], 0, s[28:29]
	v_lshl_add_u64 v[74:75], v[2:3], 0, s[28:29]
	global_load_dwordx4 v[28:31], v[72:73], off
	global_load_dwordx4 v[20:23], v[74:75], off
	v_lshl_add_u64 v[8:9], s[34:35], 0, v[8:9]
	global_load_dwordx4 v[36:39], v[6:7], off
	global_load_dwordx4 v[16:19], v[6:7], off offset:1024
	global_load_dwordx4 v[52:55], v[8:9], off
	global_load_dwordx4 v[24:27], v[8:9], off offset:1024
	global_load_dwordx4 v[40:43], v[6:7], off offset:2048
	global_load_dwordx4 v[48:51], v[8:9], off offset:2048
	s_mul_i32 s2, s11, s25
	s_ashr_i32 s3, s2, 31
	s_lshl_b64 s[2:3], s[2:3], 1
	v_lshl_add_u64 v[58:59], v[4:5], 0, s[2:3]
	v_lshl_add_u64 v[56:57], v[2:3], 0, s[2:3]
	global_load_dwordx4 v[44:47], v[58:59], off
	global_load_dwordx4 v[32:35], v[56:57], off
	v_accvgpr_write_b32 a0, 0
	v_accvgpr_write_b32 a1, 0
	v_accvgpr_write_b32 a2, 0
	v_accvgpr_write_b32 a3, 0
	v_accvgpr_write_b32 a4, 0
	v_accvgpr_write_b32 a5, 0
	v_accvgpr_write_b32 a6, 0
	v_accvgpr_write_b32 a7, 0
	v_accvgpr_write_b32 a8, 0
	v_accvgpr_write_b32 a9, 0
	v_accvgpr_write_b32 a10, 0
	v_accvgpr_write_b32 a11, 0
	v_accvgpr_write_b32 a12, 0
	v_accvgpr_write_b32 a13, 0
	v_accvgpr_write_b32 a14, 0
	v_accvgpr_write_b32 a15, 0
	v_accvgpr_write_b32 a16, 0
	v_accvgpr_write_b32 a17, 0
	v_accvgpr_write_b32 a18, 0
	v_accvgpr_write_b32 a19, 0
	v_accvgpr_write_b32 a20, 0
	v_accvgpr_write_b32 a21, 0
	v_accvgpr_write_b32 a22, 0
	v_accvgpr_write_b32 a23, 0
	v_accvgpr_write_b32 a24, 0
	v_accvgpr_write_b32 a25, 0
	v_accvgpr_write_b32 a26, 0
	v_accvgpr_write_b32 a27, 0
	v_accvgpr_write_b32 a28, 0
	v_accvgpr_write_b32 a29, 0
	v_accvgpr_write_b32 a30, 0
	v_accvgpr_write_b32 a31, 0
	s_waitcnt vmcnt(11)
	ds_write_b128 v15, v[76:79]
	s_waitcnt vmcnt(10)
	ds_write_b128 v15, v[88:91] offset:5120
	s_waitcnt lgkmcnt(0)
	s_barrier
	v_mul_u32_u24_e32 v15, 0x50, v13
	v_lshlrev_b32_e32 v13, 4, v12
	v_mad_u32_u24 v68, v10, s9, v13
	ds_read_b128 v[56:59], v68 offset:2560
	ds_read_b128 v[64:67], v68
	ds_read_b128 v[60:63], v68 offset:7680
	ds_read_b128 v[68:71], v68 offset:5120
	v_mul_u32_u24_e32 v72, 0x50, v10
	s_mov_b32 s2, 4
	s_nop 7
	v_add_u32_e32 v13, v13, v72
	v_add_u32_e32 v14, v14, v15

.LBB10_7:
	s_load_dwordx4 s[0:3], s[0:1], 0x40
	s_ashr_i32 s4, s16, 31
	s_waitcnt vmcnt(7)
	v_lshlrev_b32_e32 v37, 5, v11
	v_lshl_or_b32 v38, s14, 7, v37
	v_mul_u32_u24_e32 v37, 0x2400, v11
	s_waitcnt lgkmcnt(0)
	s_mul_hi_u32 s8, s2, s16
	s_mul_i32 s4, s2, s4
	s_add_i32 s4, s8, s4
	s_mul_i32 s3, s3, s16
	s_add_i32 s3, s4, s3
	s_mul_hi_u32 s4, s0, s15
	s_mul_i32 s8, s0, s17
	s_add_i32 s4, s4, s8
	s_mul_i32 s8, s1, s15
	v_accvgpr_read_b32 v36, a0
	s_waitcnt vmcnt(2)
	v_accvgpr_read_b32 v35, a1
	s_add_i32 s9, s4, s8
	v_lshl_or_b32 v10, v10, 2, v37
	s_movk_i32 s4, 0x240
	v_accvgpr_read_b32 v34, a2
	v_accvgpr_read_b32 v33, a3
	v_fma_f32 v36, s5, v36, 0
	v_mad_u32_u24 v10, v12, s4, v10
	v_fma_f32 v12, s5, v35, 0
	v_accvgpr_read_b32 v32, a4
	v_accvgpr_read_b32 v31, a5
	s_barrier
	ds_write2_b32 v10, v36, v12 offset1:36
	v_fma_f32 v12, s5, v34, 0
	v_fma_f32 v33, s5, v33, 0
	v_accvgpr_read_b32 v30, a6
	v_accvgpr_read_b32 v29, a7
	ds_write2_b32 v10, v12, v33 offset0:72 offset1:108
	v_fma_f32 v12, s5, v32, 0
	v_fma_f32 v31, s5, v31, 0
	v_add_u32_e32 v32, 0x400, v10
	v_accvgpr_read_b32 v28, a8
	v_accvgpr_read_b32 v27, a9
	ds_write2_b32 v32, v12, v31 offset0:32 offset1:68
	v_fma_f32 v12, s5, v30, 0
	v_fma_f32 v29, s5, v29, 0
	v_accvgpr_read_b32 v26, a10
	v_accvgpr_read_b32 v25, a11
	ds_write2_b32 v32, v12, v29 offset0:104 offset1:140
	v_fma_f32 v12, s5, v28, 0
	v_fma_f32 v27, s5, v27, 0
	v_add_u32_e32 v28, 0x800, v10
	v_accvgpr_read_b32 v24, a12
	v_accvgpr_read_b32 v23, a13
	ds_write2_b32 v28, v12, v27 offset0:64 offset1:100
	v_fma_f32 v12, s5, v26, 0
	v_fma_f32 v25, s5, v25, 0
	v_accvgpr_read_b32 v22, a14
	v_accvgpr_read_b32 v21, a15
	ds_write2_b32 v28, v12, v25 offset0:136 offset1:172
	v_fma_f32 v12, s5, v24, 0
	v_fma_f32 v23, s5, v23, 0
	v_add_u32_e32 v24, 0xc00, v10
	v_accvgpr_read_b32 v20, a16
	v_accvgpr_read_b32 v19, a17
	ds_write2_b32 v24, v12, v23 offset0:96 offset1:132
	v_fma_f32 v12, s5, v22, 0
	v_fma_f32 v21, s5, v21, 0
	v_accvgpr_read_b32 v18, a18
	v_accvgpr_read_b32 v17, a19
	ds_write2_b32 v24, v12, v21 offset0:168 offset1:204
	v_fma_f32 v12, s5, v20, 0
	v_fma_f32 v19, s5, v19, 0
	v_add_u32_e32 v20, 0x1000, v10
	v_accvgpr_read_b32 v16, a20
	v_accvgpr_read_b32 v15, a21
	ds_write2_b32 v20, v12, v19 offset0:128 offset1:164
	v_fma_f32 v12, s5, v18, 0
	v_fma_f32 v17, s5, v17, 0
	v_accvgpr_read_b32 v14, a22
	v_accvgpr_read_b32 v13, a23
	s_mul_i32 s2, s2, s16
	ds_write2_b32 v20, v12, v17 offset0:200 offset1:236
	v_fma_f32 v12, s5, v16, 0
	v_fma_f32 v15, s5, v15, 0
	v_add_u32_e32 v16, 0x1400, v10
	v_accvgpr_read_b32 v9, a24
	v_accvgpr_read_b32 v8, a25
	ds_write2_b32 v16, v12, v15 offset0:160 offset1:196
	v_fma_f32 v12, s5, v14, 0
	v_fma_f32 v13, s5, v13, 0
	v_add_u32_e32 v14, 0x1600, v10
	s_lshl_b64 s[2:3], s[2:3], 2
	v_accvgpr_read_b32 v7, a26
	v_accvgpr_read_b32 v6, a27
	v_accvgpr_read_b32 v5, a28
	v_accvgpr_read_b32 v4, a29
	v_accvgpr_read_b32 v3, a30
	v_accvgpr_read_b32 v2, a31
	s_mul_i32 s8, s0, s15
	ds_write2_b32 v14, v12, v13 offset0:104 offset1:140
	v_fma_f32 v9, s5, v9, 0
	v_fma_f32 v8, s5, v8, 0
	v_add_u32_e32 v12, 0x1800, v10
	s_add_u32 s4, s6, s2
	ds_write2_b32 v12, v9, v8 offset0:192 offset1:228
	v_fma_f32 v7, s5, v7, 0
	v_fma_f32 v6, s5, v6, 0
	v_add_u32_e32 v8, 0x1c00, v10
	v_fma_f32 v5, s5, v5, 0
	v_fma_f32 v4, s5, v4, 0
	v_fma_f32 v3, s5, v3, 0
	v_fma_f32 v2, s5, v2, 0
	s_addc_u32 s5, s7, s3
	s_lshl_b64 s[2:3], s[8:9], 2
	ds_write2_b32 v8, v7, v6 offset0:8 offset1:44
	v_add_u32_e32 v6, 0x1e00, v10
	s_add_u32 s2, s4, s2
	v_lshlrev_b32_e32 v0, 4, v0
	v_ashrrev_i32_e32 v39, 31, v38
	ds_write2_b32 v6, v5, v4 offset0:96 offset1:132
	v_add_u32_e32 v4, 0x2000, v10
	s_addc_u32 s3, s5, s3
	v_and_b32_e32 v10, 0x70, v0
	ds_write2_b32 v4, v3, v2 offset0:40 offset1:76
	v_lshrrev_b32_e32 v12, 3, v1
	v_lshl_add_u64 v[2:3], v[38:39], 2, s[2:3]
	v_or_b32_e32 v0, v37, v10
	s_movk_i32 s2, 0x90
	v_mov_b32_e32 v11, 0
	v_mad_u32_u24 v13, v12, s2, v0
	v_lshl_add_u64 v[8:9], v[2:3], 0, v[10:11]
	ds_read_b128 v[0:3], v13
	v_mad_u64_u32 v[4:5], s[2:3], s0, v12, 0
	v_mov_b32_e32 v6, v5
	v_mad_u64_u32 v[6:7], s[2:3], s1, v12, v[6:7]
	v_mov_b32_e32 v5, v6
	v_lshl_add_u64 v[10:11], v[4:5], 2, v[8:9]
	ds_read_b128 v[4:7], v13 offset:1152
	s_waitcnt lgkmcnt(1)
	global_store_dwordx4 v[10:11], v[0:3], off sc1
	s_nop 1
	v_or_b32_e32 v3, 8, v12
	v_mad_u64_u32 v[0:1], s[2:3], s0, v3, 0
	v_mov_b32_e32 v2, v1
	v_mad_u64_u32 v[2:3], s[2:3], s1, v3, v[2:3]
	v_mov_b32_e32 v1, v2
	v_lshl_add_u64 v[0:1], v[0:1], 2, v[8:9]
	s_waitcnt lgkmcnt(0)
	global_store_dwordx4 v[0:1], v[4:7], off sc1
	ds_read_b128 v[0:3], v13 offset:2304
	s_nop 0
	v_or_b32_e32 v7, 16, v12
	v_mad_u64_u32 v[4:5], s[2:3], s0, v7, 0
	v_mov_b32_e32 v6, v5
	v_mad_u64_u32 v[6:7], s[2:3], s1, v7, v[6:7]
	v_mov_b32_e32 v5, v6
	v_lshl_add_u64 v[10:11], v[4:5], 2, v[8:9]
	ds_read_b128 v[4:7], v13 offset:3456
	s_waitcnt lgkmcnt(1)
	global_store_dwordx4 v[10:11], v[0:3], off sc1
	s_nop 1
	v_or_b32_e32 v3, 24, v12
	v_mad_u64_u32 v[0:1], s[2:3], s0, v3, 0
	v_mov_b32_e32 v2, v1
	v_mad_u64_u32 v[2:3], s[2:3], s1, v3, v[2:3]
	v_mov_b32_e32 v1, v2
	v_lshl_add_u64 v[0:1], v[0:1], 2, v[8:9]
	s_waitcnt lgkmcnt(0)
	global_store_dwordx4 v[0:1], v[4:7], off sc1
	ds_read_b128 v[0:3], v13 offset:4608
	s_nop 0
	v_or_b32_e32 v7, 32, v12
	v_mad_u64_u32 v[4:5], s[2:3], s0, v7, 0
	v_mov_b32_e32 v6, v5
	v_mad_u64_u32 v[6:7], s[2:3], s1, v7, v[6:7]
	v_mov_b32_e32 v5, v6
	v_lshl_add_u64 v[10:11], v[4:5], 2, v[8:9]
	ds_read_b128 v[4:7], v13 offset:5760
	s_waitcnt lgkmcnt(1)
	global_store_dwordx4 v[10:11], v[0:3], off sc1
	s_nop 1
	v_or_b32_e32 v3, 40, v12
	v_mad_u64_u32 v[0:1], s[2:3], s0, v3, 0
	v_mov_b32_e32 v2, v1
	v_mad_u64_u32 v[2:3], s[2:3], s1, v3, v[2:3]
	v_mov_b32_e32 v1, v2
	v_lshl_add_u64 v[0:1], v[0:1], 2, v[8:9]
	s_waitcnt lgkmcnt(0)
	global_store_dwordx4 v[0:1], v[4:7], off sc1
	ds_read_b128 v[0:3], v13 offset:6912
	s_nop 0
	v_or_b32_e32 v7, 48, v12
	v_mad_u64_u32 v[4:5], s[2:3], s0, v7, 0
	v_mov_b32_e32 v6, v5
	v_mad_u64_u32 v[6:7], s[2:3], s1, v7, v[6:7]
	v_mov_b32_e32 v5, v6
	v_lshl_add_u64 v[10:11], v[4:5], 2, v[8:9]
	ds_read_b128 v[4:7], v13 offset:8064
	s_waitcnt lgkmcnt(1)
	global_store_dwordx4 v[10:11], v[0:3], off sc1
	s_nop 1
	v_or_b32_e32 v3, 56, v12
	v_mad_u64_u32 v[0:1], s[2:3], s0, v3, 0
	v_mov_b32_e32 v2, v1
	v_mad_u64_u32 v[2:3], s[0:1], s1, v3, v[2:3]
	v_mov_b32_e32 v1, v2
	v_lshl_add_u64 v[0:1], v[0:1], 2, v[8:9]
	s_waitcnt lgkmcnt(0)
	global_store_dwordx4 v[0:1], v[4:7], off sc1
	s_endpgm
	s_endpgm
	s_endpgm
	s_endpgm
	s_endpgm
	s_endpgm
	s_endpgm
	s_endpgm
	s_endpgm
	s_endpgm
	s_endpgm
	s_endpgm
	.section	.rodata,"a",@progbits
	.p2align	6, 0x0

.LBB11_4:
	s_load_dwordx4 s[4:7], s[0:1], 0x60
	s_load_dword s16, s[0:1], 0x70
	s_ashr_i32 s2, s2, 3
	s_add_i32 s18, s3, s2
	s_abs_i32 s2, s18
	s_waitcnt lgkmcnt(0)
	s_abs_i32 s17, s7
	v_cvt_f32_u32_e32 v1, s17
	s_xor_b32 s3, s18, s7
	s_ashr_i32 s19, s3, 31
	s_sub_i32 s3, 0, s17
	v_rcp_iflag_f32_e32 v1, v1
	v_lshrrev_b32_e32 v13, 2, v0
	v_mov_b32_e32 v31, 0
	v_lshrrev_b32_e32 v10, 1, v0
	v_mul_f32_e32 v1, 0x4f7ffffe, v1
	v_cvt_u32_f32_e32 v1, v1
	v_and_b32_e32 v11, 32, v13
	s_nop 1
	v_readfirstlane_b32 s20, v1
	s_mul_i32 s3, s3, s20
	s_mul_hi_u32 s3, s20, s3
	s_add_i32 s20, s20, s3
	s_mul_hi_u32 s3, s2, s20
	s_mul_i32 s20, s3, s17
	s_sub_i32 s2, s2, s20
	s_add_i32 s21, s3, 1
	s_sub_i32 s20, s2, s17
	s_cmp_ge_u32 s2, s17
	s_cselect_b32 s3, s21, s3
	s_cselect_b32 s2, s20, s2
	s_add_i32 s20, s3, 1
	s_cmp_ge_u32 s2, s17
	s_cselect_b32 s17, s20, s3
	s_abs_i32 s20, s16
	v_cvt_f32_u32_e32 v1, s20
	s_xor_b32 s17, s17, s19
	s_sub_i32 s19, s17, s19
	s_mul_i32 s7, s19, s7
	v_rcp_iflag_f32_e32 v1, v1
	s_xor_b32 s17, s19, s16
	s_sub_i32 s22, 0, s20
	s_sub_i32 s18, s18, s7
	v_mul_f32_e32 v1, 0x4f7ffffe, v1
	v_cvt_u32_f32_e32 v1, v1
	s_ashr_i32 s7, s17, 31
	s_abs_i32 s23, s19
	s_load_dwordx2 s[2:3], s[0:1], 0x10
	s_load_dword s21, s[0:1], 0x28
	v_readfirstlane_b32 s17, v1
	s_mul_i32 s22, s22, s17
	s_mul_hi_u32 s22, s17, s22
	s_add_i32 s17, s17, s22
	s_mul_hi_u32 s17, s23, s17
	s_mul_i32 s22, s17, s20
	s_sub_i32 s22, s23, s22
	s_add_i32 s24, s17, 1
	s_sub_i32 s23, s22, s20
	s_cmp_ge_u32 s22, s20
	s_cselect_b32 s17, s24, s17
	s_cselect_b32 s22, s23, s22
	s_add_i32 s23, s17, 1
	s_cmp_ge_u32 s22, s20
	s_cselect_b32 s17, s23, s17
	s_xor_b32 s17, s17, s7
	s_sub_i32 s17, s17, s7
	s_mul_i32 s7, s17, s16
	s_lshl_b32 s16, s18, 6
	v_lshlrev_b32_e32 v1, 3, v0
	s_mul_i32 s18, s17, s5
	s_sub_i32 s7, s19, s7
	v_and_b32_e32 v30, 24, v1
	s_ashr_i32 s19, s18, 31
	s_lshl_b32 s7, s7, 6
	v_lshl_add_u64 v[2:3], s[18:19], 0, v[30:31]
	v_or_b32_e32 v4, s16, v13
	s_add_i32 s18, s4, -1
	v_or_b32_e32 v1, s7, v13
	s_ashr_i32 s20, s7, 31
	v_min_i32_e32 v6, s18, v4
	s_waitcnt lgkmcnt(0)
	s_mul_i32 s20, s2, s20
	v_mad_u64_u32 v[4:5], s[18:19], s2, v1, v[2:3]
	v_mul_lo_u32 v1, s3, v1
	v_mad_i64_i32 v[6:7], s[2:3], v6, s21, v[2:3]
	v_add3_u32 v5, v1, v5, s20
	v_lshlrev_b64 v[6:7], 1, v[6:7]
	v_lshlrev_b64 v[8:9], 1, v[4:5]
	v_lshl_add_u64 v[4:5], s[12:13], 0, v[6:7]
	global_load_dwordx4 v[64:67], v[4:5], off
	v_lshl_add_u64 v[6:7], s[14:15], 0, v[6:7]
	v_lshl_add_u64 v[2:3], s[8:9], 0, v[8:9]
	global_load_dwordx4 v[68:71], v[6:7], off
	global_load_dwordx4 v[72:75], v[2:3], off
	v_lshl_add_u64 v[8:9], s[10:11], 0, v[8:9]
	global_load_dwordx4 v[76:79], v[8:9], off
	s_load_dwordx2 s[8:9], s[0:1], 0x38
	v_mul_u32_u24_e32 v13, 40, v13
	v_lshlrev_b32_e32 v30, 1, v30
	s_mov_b32 s2, 0
	v_and_b32_e32 v1, 31, v0
	s_nop 7
	v_bfe_u32 v12, v0, 5, 1
	v_and_b32_e32 v10, 32, v10
	v_lshl_add_u32 v13, v13, 1, v30
	s_ashr_i32 s3, s5, 31
	s_lshr_b32 s3, s3, 27
	s_add_i32 s3, s5, s3
	s_ashr_i32 s3, s3, 5
	s_add_i32 s5, s3, -1
	s_min_i32 s10, s5, 2
	s_lshl_b32 s10, s10, 5
	s_ashr_i32 s11, s10, 31
	s_lshl_b64 s[10:11], s[10:11], 1
	v_lshl_add_u64 v[14:15], v[2:3], 0, s[10:11]
	global_load_dwordx4 v[16:19], v[2:3], off offset:64
	global_load_dwordx4 v[20:23], v[8:9], off offset:64
	global_load_dwordx4 v[24:27], v[4:5], off offset:64
	global_load_dwordx4 v[32:35], v[6:7], off offset:64
	global_load_dwordx4 v[28:31], v[14:15], off
	v_lshl_add_u64 v[14:15], v[8:9], 0, s[10:11]
	global_load_dwordx4 v[36:39], v[14:15], off
	v_lshl_add_u64 v[14:15], v[4:5], 0, s[10:11]
	global_load_dwordx4 v[40:43], v[14:15], off
	v_lshl_add_u64 v[14:15], v[6:7], 0, s[10:11]
	global_load_dwordx4 v[44:47], v[14:15], off
	v_accvgpr_write_b32 a0, 0
	v_accvgpr_write_b32 a1, 0
	v_accvgpr_write_b32 a2, 0
	v_accvgpr_write_b32 a3, 0
	v_accvgpr_write_b32 a4, 0
	v_accvgpr_write_b32 a5, 0
	v_accvgpr_write_b32 a6, 0
	v_accvgpr_write_b32 a7, 0
	v_accvgpr_write_b32 a8, 0
	v_accvgpr_write_b32 a9, 0
	v_accvgpr_write_b32 a10, 0
	v_accvgpr_write_b32 a11, 0
	v_accvgpr_write_b32 a12, 0
	v_accvgpr_write_b32 a13, 0
	v_accvgpr_write_b32 a14, 0
	v_accvgpr_write_b32 a15, 0
	s_waitcnt vmcnt(11)
	ds_write_b128 v13, v[64:67] offset:10240
	s_waitcnt vmcnt(10)
	ds_write_b128 v13, v[68:71] offset:15360
	s_waitcnt vmcnt(9)
	ds_write_b128 v13, v[72:75]
	s_waitcnt vmcnt(8)
	ds_write_b128 v13, v[76:79] offset:5120
	s_waitcnt lgkmcnt(0)
	s_barrier
	v_or_b32_e32 v15, v10, v1
	v_lshlrev_b32_e32 v64, 4, v12
	s_movk_i32 s10, 0x50
	v_or_b32_e32 v14, v11, v1
	v_mul_u32_u24_e32 v65, 0x50, v15
	v_mad_u32_u24 v15, v15, s10, v64
	v_mul_u32_u24_e32 v66, 0x50, v14
	v_mad_u32_u24 v14, v14, s10, v64
	ds_read_b128 v[56:59], v15 offset:15360
	ds_read_b128 v[48:51], v15 offset:10240
	ds_read_b128 v[52:55], v14
	ds_read_b128 v[60:63], v14 offset:5120
	s_nop 7
	v_add_u32_e32 v14, v64, v66
	v_add_u32_e32 v15, v64, v65

.LBB11_9:
	s_endpgm
	s_endpgm
	s_endpgm
	s_endpgm
	s_endpgm
	s_endpgm
	s_endpgm
	s_endpgm
	s_endpgm
	s_endpgm
	s_endpgm
	s_endpgm
	s_endpgm
	s_endpgm
	s_endpgm
	s_endpgm
	s_endpgm
	s_endpgm
	s_endpgm
	s_endpgm
	s_endpgm
	s_endpgm
	s_endpgm
	s_endpgm
	s_endpgm
	s_endpgm
	s_endpgm
	s_endpgm
	s_endpgm
	s_endpgm
	s_endpgm
	s_endpgm
	s_endpgm
	s_endpgm
	s_endpgm
	s_endpgm
	s_endpgm
	s_endpgm
	s_endpgm
	s_endpgm
	s_endpgm
	s_endpgm
	s_endpgm
	s_endpgm
	s_endpgm
	s_endpgm
	s_endpgm
	s_endpgm
	s_endpgm
	s_endpgm
	s_endpgm
	s_endpgm

.LBB16_4:
	s_load_dwordx4 s[32:35], s[0:1], 0x18
	s_load_dword s36, s[0:1], 0x28
	s_load_dwordx4 s[4:7], s[0:1], 0x60
	s_load_dwordx2 s[14:15], s[0:1], 0x10
	s_ashr_i32 s2, s2, 3
	s_add_i32 s2, s3, s2
	s_abs_i32 s3, s2
	s_waitcnt lgkmcnt(0)
	s_abs_i32 s16, s6
	v_cvt_f32_u32_e32 v1, s16
	s_sub_i32 s18, 0, s16
	s_xor_b32 s17, s2, s6
	s_ashr_i32 s17, s17, 31
	v_rcp_iflag_f32_e32 v1, v1
	v_lshrrev_b32_e32 v11, 6, v0
	v_mov_b32_e32 v9, 0
	v_lshlrev_b32_e32 v6, 5, v11
	v_mul_f32_e32 v1, 0x4f7ffffe, v1
	v_cvt_u32_f32_e32 v1, v1
	v_and_b32_e32 v24, 31, v0
	v_and_b32_e32 v25, 63, v0
	v_bfe_u32 v26, v0, 5, 1
	v_readfirstlane_b32 s19, v1
	s_mul_i32 s18, s18, s19
	s_mul_hi_u32 s18, s19, s18
	s_add_i32 s19, s19, s18
	s_mul_hi_u32 s18, s3, s19
	s_mul_i32 s19, s18, s16
	s_sub_i32 s3, s3, s19
	s_add_i32 s20, s18, 1
	s_sub_i32 s19, s3, s16
	s_cmp_ge_u32 s3, s16
	s_cselect_b32 s18, s20, s18
	s_cselect_b32 s3, s19, s3
	s_add_i32 s19, s18, 1
	s_cmp_ge_u32 s3, s16
	s_cselect_b32 s3, s19, s18
	s_abs_i32 s18, s7
	v_cvt_f32_u32_e32 v2, s18
	s_xor_b32 s3, s3, s17
	s_sub_i32 s3, s3, s17
	s_mul_i32 s6, s3, s6
	v_rcp_iflag_f32_e32 v2, v2
	s_sub_i32 s19, 0, s18
	s_sub_i32 s16, s2, s6
	s_xor_b32 s17, s3, s7
	v_mul_f32_e32 v2, 0x4f7ffffe, v2
	v_cvt_u32_f32_e32 v2, v2
	s_ashr_i32 s2, s17, 31
	s_abs_i32 s20, s3
	v_lshrrev_b32_e32 v1, 2, v0
	v_readfirstlane_b32 s6, v2
	s_mul_i32 s19, s19, s6
	s_mul_hi_u32 s17, s6, s19
	s_add_i32 s6, s6, s17
	s_mul_hi_u32 s6, s20, s6
	s_mul_i32 s17, s6, s18
	s_sub_i32 s17, s20, s17
	s_add_i32 s19, s6, 1
	s_sub_i32 s20, s17, s18
	s_cmp_ge_u32 s17, s18
	s_cselect_b32 s6, s19, s6
	s_cselect_b32 s17, s20, s17
	s_add_i32 s19, s6, 1
	s_cmp_ge_u32 s17, s18
	s_cselect_b32 s6, s19, s6
	s_xor_b32 s6, s6, s2
	s_sub_i32 s2, s6, s2
	s_mul_i32 s6, s2, s7
	s_sub_i32 s3, s3, s6
	v_lshlrev_b32_e32 v2, 3, v0
	s_mul_i32 s2, s2, s4
	s_lshl_b32 s6, s3, 7
	v_and_b32_e32 v8, 24, v2
	s_ashr_i32 s3, s2, 31
	v_or_b32_e32 v4, s6, v1
	s_ashr_i32 s7, s6, 31
	v_lshl_add_u64 v[2:3], s[2:3], 0, v[8:9]
	s_mul_i32 s17, s14, s7
	v_mad_u64_u32 v[2:3], s[20:21], s14, v4, v[2:3]
	v_mul_lo_u32 v4, s15, v4
	v_lshl_or_b32 v10, s16, 7, v6
	s_lshl_b64 s[18:19], s[14:15], 6
	v_add3_u32 v3, v4, v3, s17
	v_or_b32_e32 v6, v10, v24
	v_lshl_add_u64 v[4:5], v[2:3], 0, s[18:19]
	v_lshlrev_b64 v[2:3], 1, v[2:3]
	v_ashrrev_i32_e32 v7, 31, v6
	v_lshl_add_u64 v[12:13], v[4:5], 1, s[10:11]
	v_lshl_add_u64 v[14:15], s[12:13], 0, v[2:3]
	v_lshl_add_u64 v[16:17], s[10:11], 0, v[2:3]
	s_lshl_b64 s[10:11], s[14:15], 7
	v_lshl_add_u64 v[6:7], v[6:7], 2, s[8:9]
	v_lshl_add_u64 v[18:19], v[14:15], 0, s[10:11]
	global_load_dwordx4 v[126:129], v[16:17], off
	global_load_dwordx4 v[130:133], v[14:15], off
	global_load_dwordx4 v[134:137], v[12:13], off
	global_load_dwordx4 v[138:141], v[18:19], off
	global_load_dword v9, v[6:7], off
	v_lshlrev_b32_e32 v0, 1, v8
	s_movk_i32 s9, 0x50
	s_nop 7
	v_mad_u32_u24 v118, v1, s9, v0
	s_mov_b32 s10, s36
	s_lshr_b32 s3, s3, 28
	s_ashr_i32 s8, s4, 31
	v_lshl_or_b32 v4, s16, 2, v11
	s_add_i32 s2, s2, s3
	s_waitcnt lgkmcnt(0)
	s_ashr_i32 s16, s10, 31
	s_lshr_b32 s8, s8, 27
	s_lshr_b32 s16, s16, 28
	s_ashr_i32 s2, s2, 4
	s_add_i32 s4, s4, s8
	s_add_i32 s10, s10, s16
	s_ashr_i32 s3, s2, 31
	s_ashr_i32 s4, s4, 5
	s_ashr_i32 s10, s10, 4
	v_mov_b32_e32 v2, s2
	v_mov_b32_e32 v3, s3
	s_add_i32 s8, s4, -1
	v_mad_i64_i32 v[2:3], s[2:3], v4, s10, v[2:3]
	s_min_i32 s11, s8, 2
	v_lshlrev_b64 v[2:3], 10, v[2:3]
	v_lshl_or_b32 v2, v25, 4, v2
	s_lshl_b32 s2, s11, 5
	v_lshl_add_u64 v[20:21], s[32:33], 0, v[2:3]
	s_ashr_i32 s3, s2, 31
	global_load_dwordx4 v[46:49], v[16:17], off offset:64
	global_load_dwordx4 v[50:53], v[14:15], off offset:64
	global_load_dwordx4 v[34:37], v[12:13], off offset:64
	global_load_dwordx4 v[30:33], v[18:19], off offset:64
	v_lshl_add_u64 v[22:23], s[34:35], 0, v[2:3]
	global_load_dwordx4 v[66:69], v[20:21], off
	global_load_dwordx4 v[38:41], v[20:21], off offset:1024
	global_load_dwordx4 v[82:85], v[22:23], off
	global_load_dwordx4 v[42:45], v[22:23], off offset:1024
	global_load_dwordx4 v[70:73], v[20:21], off offset:2048
	global_load_dwordx4 v[78:81], v[22:23], off offset:2048
	s_lshl_b64 s[2:3], s[2:3], 1
	v_lshl_add_u64 v[28:29], v[16:17], 0, s[2:3]
	v_lshl_add_u64 v[2:3], v[12:13], 0, s[2:3]
	v_lshl_add_u64 v[4:5], v[14:15], 0, s[2:3]
	v_lshl_add_u64 v[6:7], v[18:19], 0, s[2:3]
	global_load_dwordx4 v[62:65], v[28:29], off
	global_load_dwordx4 v[58:61], v[2:3], off
	global_load_dwordx4 v[74:77], v[4:5], off
	global_load_dwordx4 v[54:57], v[6:7], off
	v_accvgpr_write_b32 a48, 0
	v_accvgpr_write_b32 a49, 0
	v_accvgpr_write_b32 a50, 0
	v_accvgpr_write_b32 a51, 0
	v_accvgpr_write_b32 a52, 0
	v_accvgpr_write_b32 a53, 0
	v_accvgpr_write_b32 a54, 0
	v_accvgpr_write_b32 a55, 0
	v_accvgpr_write_b32 a56, 0
	v_accvgpr_write_b32 a57, 0
	v_accvgpr_write_b32 a58, 0
	v_accvgpr_write_b32 a59, 0
	v_accvgpr_write_b32 a60, 0
	v_accvgpr_write_b32 a61, 0
	v_accvgpr_write_b32 a62, 0
	v_accvgpr_write_b32 a63, 0
	v_accvgpr_write_b32 a32, 0
	v_accvgpr_write_b32 a33, 0
	v_accvgpr_write_b32 a34, 0
	v_accvgpr_write_b32 a35, 0
	v_accvgpr_write_b32 a36, 0
	v_accvgpr_write_b32 a37, 0
	v_accvgpr_write_b32 a38, 0
	v_accvgpr_write_b32 a39, 0
	v_accvgpr_write_b32 a40, 0
	v_accvgpr_write_b32 a41, 0
	v_accvgpr_write_b32 a42, 0
	v_accvgpr_write_b32 a43, 0
	v_accvgpr_write_b32 a44, 0
	v_accvgpr_write_b32 a45, 0
	v_accvgpr_write_b32 a46, 0
	v_accvgpr_write_b32 a47, 0
	v_accvgpr_write_b32 a16, 0
	v_accvgpr_write_b32 a17, 0
	v_accvgpr_write_b32 a18, 0
	v_accvgpr_write_b32 a19, 0
	v_accvgpr_write_b32 a20, 0
	v_accvgpr_write_b32 a21, 0
	v_accvgpr_write_b32 a22, 0
	v_accvgpr_write_b32 a23, 0
	v_accvgpr_write_b32 a24, 0
	v_accvgpr_write_b32 a25, 0
	v_accvgpr_write_b32 a26, 0
	v_accvgpr_write_b32 a27, 0
	v_accvgpr_write_b32 a28, 0
	v_accvgpr_write_b32 a29, 0
	v_accvgpr_write_b32 a30, 0
	v_accvgpr_write_b32 a31, 0
	v_accvgpr_write_b32 a0, 0
	v_accvgpr_write_b32 a1, 0
	v_accvgpr_write_b32 a2, 0
	v_accvgpr_write_b32 a3, 0
	v_accvgpr_write_b32 a4, 0
	v_accvgpr_write_b32 a5, 0
	v_accvgpr_write_b32 a6, 0
	v_accvgpr_write_b32 a7, 0
	v_accvgpr_write_b32 a8, 0
	v_accvgpr_write_b32 a9, 0
	v_accvgpr_write_b32 a10, 0
	v_accvgpr_write_b32 a11, 0
	v_accvgpr_write_b32 a12, 0
	v_accvgpr_write_b32 a13, 0
	v_accvgpr_write_b32 a14, 0
	v_accvgpr_write_b32 a15, 0
	s_waitcnt vmcnt(18)
	ds_write_b128 v118, v[126:129]
	s_waitcnt vmcnt(17)
	ds_write_b128 v118, v[130:133] offset:10240
	s_waitcnt vmcnt(16)
	ds_write_b128 v118, v[134:137] offset:5120
	s_waitcnt vmcnt(15)
	ds_write_b128 v118, v[138:141] offset:15360
	s_waitcnt lgkmcnt(0)
	s_barrier
	v_lshlrev_b32_e32 v2, 4, v26
	v_mad_u32_u24 v4, v24, s9, v2
	ds_read_b128 v[86:89], v4 offset:7680
	ds_read_b128 v[94:97], v4 offset:5120
	ds_read_b128 v[90:93], v4 offset:17920
	ds_read_b128 v[98:101], v4 offset:15360
	ds_read_b128 v[102:105], v4 offset:2560
	ds_read_b128 v[106:109], v4
	ds_read_b128 v[110:113], v4 offset:12800
	ds_read_b128 v[114:117], v4 offset:10240
	v_mul_u32_u24_e32 v1, 0x50, v1
	v_mul_u32_u24_e32 v3, 0x50, v24
	s_mov_b32 s2, 4
	s_nop 7
	v_add_u32_e32 v27, v2, v3
	v_add_u32_e32 v28, v0, v1

.LBB16_7:
	s_load_dwordx4 s[8:11], s[0:1], 0x50
	s_waitcnt vmcnt(4)
	v_mul_u32_u24_e32 v76, 0x2800, v11
	s_load_dword s24, s[0:1], 0x6c
	s_load_dwordx2 s[0:1], s[0:1], 0x40
	v_ashrrev_i32_e32 v11, 31, v10
	v_mov_b32_e32 v0, s6
	v_lshrrev_b32_e32 v4, 2, v25
	v_accvgpr_read_b32 v75, a0
	s_waitcnt lgkmcnt(0)
	s_lshl_b32 s24, s24, 7
	s_mov_b32 s0, 32
	s_mov_b32 s1, 0
	v_mul_lo_u32 v10, v10, s24
	v_mov_b32_e32 v11, 0
	s_mul_i32 s2, s1, s6
	s_mul_i32 s3, s0, s7
	s_add_i32 s4, s3, s2
	v_mad_u64_u32 v[0:1], s[2:3], s0, v0, v[10:11]
	v_or_b32_e32 v0, v0, v8
	v_lshl_or_b32 v77, v8, 1, v76
	v_mul_u32_u24_e32 v8, 40, v4
	s_waitcnt vmcnt(0)
	v_lshl_add_u32 v78, v8, 1, v77
	v_fma_f32 v8, s5, v75, v9
	v_max_f32_e32 v8, 0, v8
	s_mov_b32 s2, 0x43800000
	v_mul_u32_u24_e32 v11, 0xa0, v26
	v_fma_mixlo_f16 v10, v8, s2, 0
	v_or_b32_e32 v11, v11, v24
	v_accvgpr_read_b32 v74, a1
	v_fma_mixlo_f16 v8, v8, s2, -v10 op_sel_hi:[0,0,1]
	v_lshl_or_b32 v26, v11, 1, v76
	s_barrier
	ds_write_b16 v26, v10
	ds_write_b16 v26, v8 offset:5120
	v_fma_f32 v8, s5, v74, v9
	v_max_f32_e32 v8, 0, v8
	v_fma_mixlo_f16 v10, v8, s2, 0
	v_accvgpr_read_b32 v73, a2
	v_fma_mixlo_f16 v8, v8, s2, -v10 op_sel_hi:[0,0,1]
	ds_write_b16 v26, v10 offset:80
	ds_write_b16 v26, v8 offset:5200
	v_fma_f32 v8, s5, v73, v9
	v_max_f32_e32 v8, 0, v8
	v_fma_mixlo_f16 v10, v8, s2, 0
	v_accvgpr_read_b32 v72, a3
	v_fma_mixlo_f16 v8, v8, s2, -v10 op_sel_hi:[0,0,1]
	ds_write_b16 v26, v10 offset:160
	ds_write_b16 v26, v8 offset:5280
	v_fma_f32 v8, s5, v72, v9
	v_max_f32_e32 v8, 0, v8
	v_fma_mixlo_f16 v10, v8, s2, 0
	v_accvgpr_read_b32 v71, a4
	v_fma_mixlo_f16 v8, v8, s2, -v10 op_sel_hi:[0,0,1]
	ds_write_b16 v26, v10 offset:240
	ds_write_b16 v26, v8 offset:5360
	v_fma_f32 v8, s5, v71, v9
	v_max_f32_e32 v8, 0, v8
	v_fma_mixlo_f16 v10, v8, s2, 0
	v_accvgpr_read_b32 v70, a5
	v_fma_mixlo_f16 v8, v8, s2, -v10 op_sel_hi:[0,0,1]
	ds_write_b16 v26, v10 offset:640
	ds_write_b16 v26, v8 offset:5760
	v_fma_f32 v8, s5, v70, v9
	v_max_f32_e32 v8, 0, v8
	v_fma_mixlo_f16 v10, v8, s2, 0
	v_accvgpr_read_b32 v69, a6
	v_fma_mixlo_f16 v8, v8, s2, -v10 op_sel_hi:[0,0,1]
	ds_write_b16 v26, v10 offset:720
	ds_write_b16 v26, v8 offset:5840
	v_fma_f32 v8, s5, v69, v9
	v_max_f32_e32 v8, 0, v8
	v_fma_mixlo_f16 v10, v8, s2, 0
	v_accvgpr_read_b32 v68, a7
	v_fma_mixlo_f16 v8, v8, s2, -v10 op_sel_hi:[0,0,1]
	ds_write_b16 v26, v10 offset:800
	ds_write_b16 v26, v8 offset:5920
	v_fma_f32 v8, s5, v68, v9
	v_max_f32_e32 v8, 0, v8
	v_fma_mixlo_f16 v10, v8, s2, 0
	v_accvgpr_read_b32 v67, a8
	v_fma_mixlo_f16 v8, v8, s2, -v10 op_sel_hi:[0,0,1]
	ds_write_b16 v26, v10 offset:880
	ds_write_b16 v26, v8 offset:6000
	v_fma_f32 v8, s5, v67, v9
	v_max_f32_e32 v8, 0, v8
	v_fma_mixlo_f16 v10, v8, s2, 0
	v_accvgpr_read_b32 v66, a9
	v_fma_mixlo_f16 v8, v8, s2, -v10 op_sel_hi:[0,0,1]
	ds_write_b16 v26, v10 offset:1280
	ds_write_b16 v26, v8 offset:6400
	v_fma_f32 v8, s5, v66, v9
	v_max_f32_e32 v8, 0, v8
	v_fma_mixlo_f16 v10, v8, s2, 0
	v_accvgpr_read_b32 v65, a10
	v_fma_mixlo_f16 v8, v8, s2, -v10 op_sel_hi:[0,0,1]
	ds_write_b16 v26, v10 offset:1360
	ds_write_b16 v26, v8 offset:6480
	v_fma_f32 v8, s5, v65, v9
	v_max_f32_e32 v8, 0, v8
	v_fma_mixlo_f16 v10, v8, s2, 0
	v_accvgpr_read_b32 v64, a11
	v_fma_mixlo_f16 v8, v8, s2, -v10 op_sel_hi:[0,0,1]
	ds_write_b16 v26, v10 offset:1440
	ds_write_b16 v26, v8 offset:6560
	v_fma_f32 v8, s5, v64, v9
	v_max_f32_e32 v8, 0, v8
	v_fma_mixlo_f16 v10, v8, s2, 0
	v_accvgpr_read_b32 v63, a12
	v_fma_mixlo_f16 v8, v8, s2, -v10 op_sel_hi:[0,0,1]
	ds_write_b16 v26, v10 offset:1520
	ds_write_b16 v26, v8 offset:6640
	v_fma_f32 v8, s5, v63, v9
	v_max_f32_e32 v8, 0, v8
	v_fma_mixlo_f16 v10, v8, s2, 0
	v_accvgpr_read_b32 v62, a13
	v_fma_mixlo_f16 v8, v8, s2, -v10 op_sel_hi:[0,0,1]
	ds_write_b16 v26, v10 offset:1920
	ds_write_b16 v26, v8 offset:7040
	v_fma_f32 v8, s5, v62, v9
	v_max_f32_e32 v8, 0, v8
	v_fma_mixlo_f16 v10, v8, s2, 0
	v_accvgpr_read_b32 v61, a14
	v_fma_mixlo_f16 v8, v8, s2, -v10 op_sel_hi:[0,0,1]
	ds_write_b16 v26, v10 offset:2000
	ds_write_b16 v26, v8 offset:7120
	v_fma_f32 v8, s5, v61, v9
	v_max_f32_e32 v8, 0, v8
	v_fma_mixlo_f16 v10, v8, s2, 0
	v_accvgpr_read_b32 v60, a15
	v_fma_mixlo_f16 v8, v8, s2, -v10 op_sel_hi:[0,0,1]
	ds_write_b16 v26, v10 offset:2080
	ds_write_b16 v26, v8 offset:7200
	v_fma_f32 v8, s5, v60, v9
	v_max_f32_e32 v8, 0, v8
	v_fma_mixlo_f16 v10, v8, s2, 0
	v_accvgpr_read_b32 v59, a16
	v_fma_mixlo_f16 v8, v8, s2, -v10 op_sel_hi:[0,0,1]
	ds_write_b16 v26, v10 offset:2160
	ds_write_b16 v26, v8 offset:7280
	v_fma_f32 v8, s5, v59, v9
	v_max_f32_e32 v8, 0, v8
	v_fma_mixlo_f16 v10, v8, s2, 0
	v_accvgpr_read_b32 v58, a17
	v_fma_mixlo_f16 v8, v8, s2, -v10 op_sel_hi:[0,0,1]
	ds_write_b16 v26, v10 offset:2560
	ds_write_b16 v26, v8 offset:7680
	v_fma_f32 v8, s5, v58, v9
	v_max_f32_e32 v8, 0, v8
	v_fma_mixlo_f16 v10, v8, s2, 0
	v_accvgpr_read_b32 v57, a18
	v_fma_mixlo_f16 v8, v8, s2, -v10 op_sel_hi:[0,0,1]
	ds_write_b16 v26, v10 offset:2640
	ds_write_b16 v26, v8 offset:7760
	v_fma_f32 v8, s5, v57, v9
	v_max_f32_e32 v8, 0, v8
	v_fma_mixlo_f16 v10, v8, s2, 0
	v_accvgpr_read_b32 v56, a19
	v_fma_mixlo_f16 v8, v8, s2, -v10 op_sel_hi:[0,0,1]
	ds_write_b16 v26, v10 offset:2720
	ds_write_b16 v26, v8 offset:7840
	v_fma_f32 v8, s5, v56, v9
	v_max_f32_e32 v8, 0, v8
	v_fma_mixlo_f16 v10, v8, s2, 0
	v_accvgpr_read_b32 v55, a20
	v_fma_mixlo_f16 v8, v8, s2, -v10 op_sel_hi:[0,0,1]
	ds_write_b16 v26, v10 offset:2800
	ds_write_b16 v26, v8 offset:7920
	v_fma_f32 v8, s5, v55, v9
	v_max_f32_e32 v8, 0, v8
	v_fma_mixlo_f16 v10, v8, s2, 0
	v_accvgpr_read_b32 v54, a21
	v_fma_mixlo_f16 v8, v8, s2, -v10 op_sel_hi:[0,0,1]
	ds_write_b16 v26, v10 offset:3200
	ds_write_b16 v26, v8 offset:8320
	v_fma_f32 v8, s5, v54, v9
	v_max_f32_e32 v8, 0, v8
	v_fma_mixlo_f16 v10, v8, s2, 0
	v_accvgpr_read_b32 v53, a22
	v_fma_mixlo_f16 v8, v8, s2, -v10 op_sel_hi:[0,0,1]
	ds_write_b16 v26, v10 offset:3280
	ds_write_b16 v26, v8 offset:8400
	v_fma_f32 v8, s5, v53, v9
	v_max_f32_e32 v8, 0, v8
	v_fma_mixlo_f16 v10, v8, s2, 0
	v_accvgpr_read_b32 v52, a23
	v_fma_mixlo_f16 v8, v8, s2, -v10 op_sel_hi:[0,0,1]
	ds_write_b16 v26, v10 offset:3360
	ds_write_b16 v26, v8 offset:8480
	v_fma_f32 v8, s5, v52, v9
	v_max_f32_e32 v8, 0, v8
	v_fma_mixlo_f16 v10, v8, s2, 0
	v_accvgpr_read_b32 v51, a24
	v_fma_mixlo_f16 v8, v8, s2, -v10 op_sel_hi:[0,0,1]
	ds_write_b16 v26, v10 offset:3440
	ds_write_b16 v26, v8 offset:8560
	v_fma_f32 v8, s5, v51, v9
	v_max_f32_e32 v8, 0, v8
	v_fma_mixlo_f16 v10, v8, s2, 0
	v_accvgpr_read_b32 v50, a25
	v_fma_mixlo_f16 v8, v8, s2, -v10 op_sel_hi:[0,0,1]
	ds_write_b16 v26, v10 offset:3840
	ds_write_b16 v26, v8 offset:8960
	v_fma_f32 v8, s5, v50, v9
	v_max_f32_e32 v8, 0, v8
	v_fma_mixlo_f16 v10, v8, s2, 0
	v_accvgpr_read_b32 v49, a26
	v_fma_mixlo_f16 v8, v8, s2, -v10 op_sel_hi:[0,0,1]
	ds_write_b16 v26, v10 offset:3920
	ds_write_b16 v26, v8 offset:9040
	v_fma_f32 v8, s5, v49, v9
	v_max_f32_e32 v8, 0, v8
	v_fma_mixlo_f16 v10, v8, s2, 0
	v_accvgpr_read_b32 v48, a27
	v_fma_mixlo_f16 v8, v8, s2, -v10 op_sel_hi:[0,0,1]
	ds_write_b16 v26, v10 offset:4000
	ds_write_b16 v26, v8 offset:9120
	v_fma_f32 v8, s5, v48, v9
	v_max_f32_e32 v8, 0, v8
	v_fma_mixlo_f16 v10, v8, s2, 0
	v_accvgpr_read_b32 v47, a28
	v_fma_mixlo_f16 v8, v8, s2, -v10 op_sel_hi:[0,0,1]
	ds_write_b16 v26, v10 offset:4080
	ds_write_b16 v26, v8 offset:9200
	v_fma_f32 v8, s5, v47, v9
	v_max_f32_e32 v8, 0, v8
	v_fma_mixlo_f16 v10, v8, s2, 0
	v_accvgpr_read_b32 v46, a29
	v_fma_mixlo_f16 v8, v8, s2, -v10 op_sel_hi:[0,0,1]
	ds_write_b16 v26, v10 offset:4480
	ds_write_b16 v26, v8 offset:9600
	v_fma_f32 v8, s5, v46, v9
	v_max_f32_e32 v8, 0, v8
	v_fma_mixlo_f16 v10, v8, s2, 0
	v_accvgpr_read_b32 v45, a30
	v_fma_mixlo_f16 v8, v8, s2, -v10 op_sel_hi:[0,0,1]
	ds_write_b16 v26, v10 offset:4560
	ds_write_b16 v26, v8 offset:9680
	v_fma_f32 v8, s5, v45, v9
	v_max_f32_e32 v8, 0, v8
	v_fma_mixlo_f16 v10, v8, s2, 0
	v_accvgpr_read_b32 v44, a31
	v_fma_mixlo_f16 v8, v8, s2, -v10 op_sel_hi:[0,0,1]
	ds_write_b16 v26, v10 offset:4640
	ds_write_b16 v26, v8 offset:9760
	v_fma_f32 v8, s5, v44, v9
	v_max_f32_e32 v8, 0, v8
	v_fma_mixlo_f16 v10, v8, s2, 0
	v_fma_mixlo_f16 v8, v8, s2, -v10 op_sel_hi:[0,0,1]
	ds_write_b16 v26, v10 offset:4720
	ds_write_b16 v26, v8 offset:9840
	v_mad_u64_u32 v[10:11], s[6:7], s0, v4, 0
	v_mov_b32_e32 v8, v11
	v_add_u32_e32 v1, s4, v1
	ds_read_b128 v[44:47], v78
	ds_read_b128 v[48:51], v78 offset:5120
	v_mad_u64_u32 v[24:25], s[6:7], s1, v4, v[8:9]
	v_lshlrev_b64 v[0:1], 1, v[0:1]
	v_mov_b32_e32 v11, v24
	v_lshl_add_u64 v[2:3], s[8:9], 0, v[0:1]
	v_lshlrev_b64 v[10:11], 1, v[10:11]
	v_lshl_add_u64 v[0:1], s[10:11], 0, v[0:1]
	v_lshl_add_u64 v[24:25], v[2:3], 0, v[10:11]
	s_waitcnt lgkmcnt(1)
	global_store_dwordx4 v[24:25], v[44:47], off sc1
	v_lshl_add_u64 v[10:11], v[0:1], 0, v[10:11]
	v_or_b32_e32 v24, 16, v4
	s_waitcnt lgkmcnt(0)
	global_store_dwordx4 v[10:11], v[48:51], off sc1
	v_mul_u32_u24_e32 v8, 40, v24
	v_mad_u64_u32 v[10:11], s[6:7], s0, v24, 0
	v_lshl_add_u32 v56, v8, 1, v77
	v_mov_b32_e32 v8, v11
	ds_read_b128 v[44:47], v56
	ds_read_b128 v[48:51], v56 offset:5120
	v_mad_u64_u32 v[24:25], s[6:7], s1, v24, v[8:9]
	v_mov_b32_e32 v11, v24
	v_lshlrev_b64 v[10:11], 1, v[10:11]
	v_lshl_add_u64 v[24:25], v[2:3], 0, v[10:11]
	s_waitcnt lgkmcnt(1)
	global_store_dwordx4 v[24:25], v[44:47], off sc1
	v_lshl_add_u64 v[10:11], v[0:1], 0, v[10:11]
	v_or_b32_e32 v24, 32, v4
	s_waitcnt lgkmcnt(0)
	global_store_dwordx4 v[10:11], v[48:51], off sc1
	v_mad_u64_u32 v[10:11], s[6:7], s0, v24, 0
	ds_read_b128 v[52:55], v56 offset:1280
	ds_read_b128 v[44:47], v56 offset:2560
	v_mov_b32_e32 v8, v11
	ds_read_b128 v[48:51], v56 offset:6400
	v_mad_u64_u32 v[24:25], s[6:7], s1, v24, v[8:9]
	v_mov_b32_e32 v11, v24
	v_lshlrev_b64 v[10:11], 1, v[10:11]
	v_lshl_add_u64 v[24:25], v[2:3], 0, v[10:11]
	s_waitcnt lgkmcnt(2)
	global_store_dwordx4 v[24:25], v[52:55], off sc1
	v_lshl_add_u64 v[10:11], v[0:1], 0, v[10:11]
	v_or_b32_e32 v24, 48, v4
	ds_read_b128 v[52:55], v56 offset:7680
	s_waitcnt lgkmcnt(1)
	global_store_dwordx4 v[10:11], v[48:51], off sc1
	v_mad_u64_u32 v[10:11], s[6:7], s0, v24, 0
	v_mov_b32_e32 v8, v11
	v_mad_u64_u32 v[24:25], s[6:7], s1, v24, v[8:9]
	v_accvgpr_read_b32 v43, a32
	v_mov_b32_e32 v11, v24
	v_lshlrev_b64 v[10:11], 1, v[10:11]
	v_fma_f32 v8, s5, v43, v9
	v_lshl_add_u64 v[24:25], v[2:3], 0, v[10:11]
	v_lshl_add_u64 v[10:11], v[0:1], 0, v[10:11]
	v_max_f32_e32 v8, 0, v8
	s_waitcnt lgkmcnt(0)
	global_store_dwordx4 v[10:11], v[52:55], off sc1
	v_fma_mixlo_f16 v10, v8, s2, 0
	v_accvgpr_read_b32 v42, a33
	v_fma_mixlo_f16 v8, v8, s2, -v10 op_sel_hi:[0,0,1]
	global_store_dwordx4 v[24:25], v[44:47], off sc1
	ds_write_b16 v26, v10
	ds_write_b16 v26, v8 offset:5120
	v_fma_f32 v8, s5, v42, v9
	v_max_f32_e32 v8, 0, v8
	v_fma_mixlo_f16 v10, v8, s2, 0
	v_accvgpr_read_b32 v41, a34
	v_fma_mixlo_f16 v8, v8, s2, -v10 op_sel_hi:[0,0,1]
	ds_write_b16 v26, v10 offset:80
	ds_write_b16 v26, v8 offset:5200
	v_fma_f32 v8, s5, v41, v9
	v_max_f32_e32 v8, 0, v8
	v_fma_mixlo_f16 v10, v8, s2, 0
	v_accvgpr_read_b32 v40, a35
	v_fma_mixlo_f16 v8, v8, s2, -v10 op_sel_hi:[0,0,1]
	ds_write_b16 v26, v10 offset:160
	ds_write_b16 v26, v8 offset:5280
	v_fma_f32 v8, s5, v40, v9
	v_max_f32_e32 v8, 0, v8
	v_fma_mixlo_f16 v10, v8, s2, 0
	v_accvgpr_read_b32 v39, a36
	v_fma_mixlo_f16 v8, v8, s2, -v10 op_sel_hi:[0,0,1]
	ds_write_b16 v26, v10 offset:240
	ds_write_b16 v26, v8 offset:5360
	v_fma_f32 v8, s5, v39, v9
	v_max_f32_e32 v8, 0, v8
	v_fma_mixlo_f16 v10, v8, s2, 0
	v_accvgpr_read_b32 v38, a37
	v_fma_mixlo_f16 v8, v8, s2, -v10 op_sel_hi:[0,0,1]
	ds_write_b16 v26, v10 offset:640
	ds_write_b16 v26, v8 offset:5760
	v_fma_f32 v8, s5, v38, v9
	v_max_f32_e32 v8, 0, v8
	v_fma_mixlo_f16 v10, v8, s2, 0
	v_accvgpr_read_b32 v37, a38
	v_fma_mixlo_f16 v8, v8, s2, -v10 op_sel_hi:[0,0,1]
	ds_write_b16 v26, v10 offset:720
	ds_write_b16 v26, v8 offset:5840
	v_fma_f32 v8, s5, v37, v9
	v_max_f32_e32 v8, 0, v8
	v_fma_mixlo_f16 v10, v8, s2, 0
	v_accvgpr_read_b32 v36, a39
	v_fma_mixlo_f16 v8, v8, s2, -v10 op_sel_hi:[0,0,1]
	ds_write_b16 v26, v10 offset:800
	ds_write_b16 v26, v8 offset:5920
	v_fma_f32 v8, s5, v36, v9
	v_max_f32_e32 v8, 0, v8
	v_fma_mixlo_f16 v10, v8, s2, 0
	v_accvgpr_read_b32 v35, a40
	v_fma_mixlo_f16 v8, v8, s2, -v10 op_sel_hi:[0,0,1]
	ds_write_b16 v26, v10 offset:880
	ds_write_b16 v26, v8 offset:6000
	v_fma_f32 v8, s5, v35, v9
	v_max_f32_e32 v8, 0, v8
	v_fma_mixlo_f16 v10, v8, s2, 0
	v_accvgpr_read_b32 v34, a41
	v_fma_mixlo_f16 v8, v8, s2, -v10 op_sel_hi:[0,0,1]
	ds_write_b16 v26, v10 offset:1280
	ds_write_b16 v26, v8 offset:6400
	v_fma_f32 v8, s5, v34, v9
	v_max_f32_e32 v8, 0, v8
	v_fma_mixlo_f16 v10, v8, s2, 0
	v_accvgpr_read_b32 v33, a42
	v_fma_mixlo_f16 v8, v8, s2, -v10 op_sel_hi:[0,0,1]
	ds_write_b16 v26, v10 offset:1360
	ds_write_b16 v26, v8 offset:6480
	v_fma_f32 v8, s5, v33, v9
	v_max_f32_e32 v8, 0, v8
	v_fma_mixlo_f16 v10, v8, s2, 0
	v_accvgpr_read_b32 v32, a43
	v_fma_mixlo_f16 v8, v8, s2, -v10 op_sel_hi:[0,0,1]
	ds_write_b16 v26, v10 offset:1440
	ds_write_b16 v26, v8 offset:6560
	v_fma_f32 v8, s5, v32, v9
	v_max_f32_e32 v8, 0, v8
	v_fma_mixlo_f16 v10, v8, s2, 0
	v_accvgpr_read_b32 v31, a44
	v_fma_mixlo_f16 v8, v8, s2, -v10 op_sel_hi:[0,0,1]
	ds_write_b16 v26, v10 offset:1520
	ds_write_b16 v26, v8 offset:6640
	v_fma_f32 v8, s5, v31, v9
	v_max_f32_e32 v8, 0, v8
	v_fma_mixlo_f16 v10, v8, s2, 0
	v_accvgpr_read_b32 v30, a45
	v_fma_mixlo_f16 v8, v8, s2, -v10 op_sel_hi:[0,0,1]
	ds_write_b16 v26, v10 offset:1920
	ds_write_b16 v26, v8 offset:7040
	v_fma_f32 v8, s5, v30, v9
	v_max_f32_e32 v8, 0, v8
	v_fma_mixlo_f16 v10, v8, s2, 0
	v_accvgpr_read_b32 v29, a46
	v_fma_mixlo_f16 v8, v8, s2, -v10 op_sel_hi:[0,0,1]
	ds_write_b16 v26, v10 offset:2000
	ds_write_b16 v26, v8 offset:7120
	v_fma_f32 v8, s5, v29, v9
	v_max_f32_e32 v8, 0, v8
	v_fma_mixlo_f16 v10, v8, s2, 0
	v_accvgpr_read_b32 v28, a47
	v_fma_mixlo_f16 v8, v8, s2, -v10 op_sel_hi:[0,0,1]
	ds_write_b16 v26, v10 offset:2080
	ds_write_b16 v26, v8 offset:7200
	v_fma_f32 v8, s5, v28, v9
	v_max_f32_e32 v8, 0, v8
	v_fma_mixlo_f16 v10, v8, s2, 0
	v_accvgpr_read_b32 v27, a48
	v_fma_mixlo_f16 v8, v8, s2, -v10 op_sel_hi:[0,0,1]
	ds_write_b16 v26, v10 offset:2160
	ds_write_b16 v26, v8 offset:7280
	v_fma_f32 v8, s5, v27, v9
	v_max_f32_e32 v8, 0, v8
	v_fma_mixlo_f16 v10, v8, s2, 0
	v_accvgpr_read_b32 v23, a49
	v_fma_mixlo_f16 v8, v8, s2, -v10 op_sel_hi:[0,0,1]
	ds_write_b16 v26, v10 offset:2560
	ds_write_b16 v26, v8 offset:7680
	v_fma_f32 v8, s5, v23, v9
	v_max_f32_e32 v8, 0, v8
	v_fma_mixlo_f16 v10, v8, s2, 0
	v_accvgpr_read_b32 v22, a50
	v_fma_mixlo_f16 v8, v8, s2, -v10 op_sel_hi:[0,0,1]
	ds_write_b16 v26, v10 offset:2640
	ds_write_b16 v26, v8 offset:7760
	v_fma_f32 v8, s5, v22, v9
	v_max_f32_e32 v8, 0, v8
	v_fma_mixlo_f16 v10, v8, s2, 0
	v_accvgpr_read_b32 v21, a51
	v_fma_mixlo_f16 v8, v8, s2, -v10 op_sel_hi:[0,0,1]
	ds_write_b16 v26, v10 offset:2720
	ds_write_b16 v26, v8 offset:7840
	v_fma_f32 v8, s5, v21, v9
	v_max_f32_e32 v8, 0, v8
	v_fma_mixlo_f16 v10, v8, s2, 0
	v_accvgpr_read_b32 v20, a52
	v_fma_mixlo_f16 v8, v8, s2, -v10 op_sel_hi:[0,0,1]
	ds_write_b16 v26, v10 offset:2800
	ds_write_b16 v26, v8 offset:7920
	v_fma_f32 v8, s5, v20, v9
	v_max_f32_e32 v8, 0, v8
	v_fma_mixlo_f16 v10, v8, s2, 0
	v_accvgpr_read_b32 v19, a53
	v_fma_mixlo_f16 v8, v8, s2, -v10 op_sel_hi:[0,0,1]
	ds_write_b16 v26, v10 offset:3200
	ds_write_b16 v26, v8 offset:8320
	v_fma_f32 v8, s5, v19, v9
	v_max_f32_e32 v8, 0, v8
	v_fma_mixlo_f16 v10, v8, s2, 0
	v_accvgpr_read_b32 v18, a54
	v_fma_mixlo_f16 v8, v8, s2, -v10 op_sel_hi:[0,0,1]
	ds_write_b16 v26, v10 offset:3280
	ds_write_b16 v26, v8 offset:8400
	v_fma_f32 v8, s5, v18, v9
	v_max_f32_e32 v8, 0, v8
	v_fma_mixlo_f16 v10, v8, s2, 0
	v_accvgpr_read_b32 v17, a55
	v_fma_mixlo_f16 v8, v8, s2, -v10 op_sel_hi:[0,0,1]
	ds_write_b16 v26, v10 offset:3360
	ds_write_b16 v26, v8 offset:8480
	v_fma_f32 v8, s5, v17, v9
	v_max_f32_e32 v8, 0, v8
	v_fma_mixlo_f16 v10, v8, s2, 0
	v_accvgpr_read_b32 v16, a56
	v_fma_mixlo_f16 v8, v8, s2, -v10 op_sel_hi:[0,0,1]
	ds_write_b16 v26, v10 offset:3440
	ds_write_b16 v26, v8 offset:8560
	v_fma_f32 v8, s5, v16, v9
	v_max_f32_e32 v8, 0, v8
	v_fma_mixlo_f16 v10, v8, s2, 0
	v_accvgpr_read_b32 v15, a57
	v_fma_mixlo_f16 v8, v8, s2, -v10 op_sel_hi:[0,0,1]
	ds_write_b16 v26, v10 offset:3840
	ds_write_b16 v26, v8 offset:8960
	v_fma_f32 v8, s5, v15, v9
	v_max_f32_e32 v8, 0, v8
	v_fma_mixlo_f16 v10, v8, s2, 0
	v_accvgpr_read_b32 v14, a58
	v_fma_mixlo_f16 v8, v8, s2, -v10 op_sel_hi:[0,0,1]
	ds_write_b16 v26, v10 offset:3920
	ds_write_b16 v26, v8 offset:9040
	v_fma_f32 v8, s5, v14, v9
	v_max_f32_e32 v8, 0, v8
	v_fma_mixlo_f16 v10, v8, s2, 0
	v_accvgpr_read_b32 v13, a59
	v_fma_mixlo_f16 v8, v8, s2, -v10 op_sel_hi:[0,0,1]
	ds_write_b16 v26, v10 offset:4000
	ds_write_b16 v26, v8 offset:9120
	v_fma_f32 v8, s5, v13, v9
	v_max_f32_e32 v8, 0, v8
	v_fma_mixlo_f16 v10, v8, s2, 0
	v_accvgpr_read_b32 v12, a60
	v_fma_mixlo_f16 v8, v8, s2, -v10 op_sel_hi:[0,0,1]
	ds_write_b16 v26, v10 offset:4080
	ds_write_b16 v26, v8 offset:9200
	v_fma_f32 v8, s5, v12, v9
	v_accvgpr_read_b32 v7, a61
	v_max_f32_e32 v8, 0, v8
	v_fma_mixlo_f16 v10, v8, s2, 0
	v_fma_f32 v7, s5, v7, v9
	v_accvgpr_read_b32 v6, a62
	v_fma_mixlo_f16 v8, v8, s2, -v10 op_sel_hi:[0,0,1]
	v_max_f32_e32 v7, 0, v7
	ds_write_b16 v26, v10 offset:4480
	ds_write_b16 v26, v8 offset:9600
	v_fma_mixlo_f16 v8, v7, s2, 0
	v_fma_f32 v6, s5, v6, v9
	v_accvgpr_read_b32 v5, a63
	v_fma_mixlo_f16 v7, v7, s2, -v8 op_sel_hi:[0,0,1]
	v_max_f32_e32 v6, 0, v6
	ds_write_b16 v26, v8 offset:4560
	ds_write_b16 v26, v7 offset:9680
	v_fma_mixlo_f16 v7, v6, s2, 0
	v_fmac_f32_e32 v9, s5, v5
	v_fma_mixlo_f16 v6, v6, s2, -v7 op_sel_hi:[0,0,1]
	v_max_f32_e32 v5, 0, v9
	ds_write_b16 v26, v7 offset:4640
	ds_write_b16 v26, v6 offset:9760
	v_fma_mixlo_f16 v6, v5, s2, 0
	v_fma_mixlo_f16 v5, v5, s2, -v6 op_sel_hi:[0,0,1]
	ds_write_b16 v26, v6 offset:4720
	ds_write_b16 v26, v5 offset:9840
	v_or_b32_e32 v5, 64, v4
	v_mad_u64_u32 v[14:15], s[2:3], s0, v5, 0
	v_mov_b32_e32 v16, v15
	ds_read_b128 v[6:9], v78
	ds_read_b128 v[10:13], v78 offset:5120
	v_mad_u64_u32 v[16:17], s[2:3], s1, v5, v[16:17]
	v_mov_b32_e32 v15, v16
	v_lshlrev_b64 v[14:15], 1, v[14:15]
	v_lshl_add_u64 v[16:17], v[2:3], 0, v[14:15]
	s_waitcnt lgkmcnt(1)
	global_store_dwordx4 v[16:17], v[6:9], off sc1
	v_or_b32_e32 v5, 0x50, v4
	s_nop 0
	v_lshl_add_u64 v[6:7], v[0:1], 0, v[14:15]
	s_waitcnt lgkmcnt(0)
	global_store_dwordx4 v[6:7], v[10:13], off sc1
	v_mad_u64_u32 v[14:15], s[2:3], s0, v5, 0
	ds_read_b128 v[6:9], v56
	ds_read_b128 v[10:13], v56 offset:5120
	v_mov_b32_e32 v16, v15
	v_mad_u64_u32 v[16:17], s[2:3], s1, v5, v[16:17]
	v_mov_b32_e32 v15, v16
	v_lshlrev_b64 v[18:19], 1, v[14:15]
	v_lshl_add_u64 v[20:21], v[2:3], 0, v[18:19]
	v_lshl_add_u64 v[18:19], v[0:1], 0, v[18:19]
	v_or_b32_e32 v5, 0x60, v4
	s_waitcnt lgkmcnt(0)
	global_store_dwordx4 v[18:19], v[10:13], off sc1
	v_mad_u64_u32 v[18:19], s[2:3], s0, v5, 0
	ds_read_b128 v[14:17], v56 offset:1280
	global_store_dwordx4 v[20:21], v[6:9], off sc1
	ds_read_b128 v[10:13], v56 offset:6400
	v_mov_b32_e32 v20, v19
	v_mad_u64_u32 v[20:21], s[2:3], s1, v5, v[20:21]
	v_mov_b32_e32 v19, v20
	v_lshlrev_b64 v[18:19], 1, v[18:19]
	v_lshl_add_u64 v[20:21], v[2:3], 0, v[18:19]
	v_lshl_add_u64 v[18:19], v[0:1], 0, v[18:19]
	ds_read_b128 v[6:9], v56 offset:2560
	s_waitcnt lgkmcnt(2)
	global_store_dwordx4 v[20:21], v[14:17], off sc1
	ds_read_b128 v[14:17], v56 offset:7680
	s_waitcnt lgkmcnt(2)
	global_store_dwordx4 v[18:19], v[10:13], off sc1
	s_nop 1
	v_or_b32_e32 v11, 0x70, v4
	v_mad_u64_u32 v[4:5], s[2:3], s0, v11, 0
	v_mov_b32_e32 v10, v5
	v_mad_u64_u32 v[10:11], s[0:1], s1, v11, v[10:11]
	v_mov_b32_e32 v5, v10
	v_lshlrev_b64 v[4:5], 1, v[4:5]
	v_lshl_add_u64 v[2:3], v[2:3], 0, v[4:5]
	v_lshl_add_u64 v[0:1], v[0:1], 0, v[4:5]
	s_waitcnt lgkmcnt(1)
	global_store_dwordx4 v[2:3], v[6:9], off sc1
	s_waitcnt lgkmcnt(0)
	global_store_dwordx4 v[0:1], v[14:17], off sc1
	s_endpgm
	s_endpgm
	s_endpgm
	s_endpgm
	s_endpgm
	s_endpgm
	s_endpgm
	s_endpgm
	s_endpgm
	s_endpgm
	s_endpgm
	s_endpgm
	s_endpgm
	s_endpgm
	s_endpgm
	s_endpgm
	s_endpgm
	s_endpgm
	s_endpgm
	s_endpgm
	s_endpgm
	s_endpgm
	s_endpgm
	s_endpgm
	s_endpgm
	s_endpgm
	s_endpgm
	s_endpgm
	s_endpgm
	s_endpgm
	s_endpgm
	s_endpgm
	s_endpgm
	s_endpgm
	s_endpgm
	s_endpgm
	s_endpgm
	s_endpgm
	s_endpgm
	s_endpgm
	s_endpgm
	s_endpgm
	s_endpgm
	.section	.rodata,"a",@progbits
	.p2align	6, 0x0

.LBB17_4:
	s_load_dwordx4 s[4:7], s[0:1], 0x60
	s_load_dwordx2 s[14:15], s[0:1], 0x10
	s_ashr_i32 s2, s2, 3
	s_add_i32 s2, s3, s2
	s_abs_i32 s3, s2
	s_waitcnt lgkmcnt(0)
	s_abs_i32 s16, s6
	v_cvt_f32_u32_e32 v1, s16
	s_sub_i32 s18, 0, s16
	s_xor_b32 s17, s2, s6
	s_ashr_i32 s17, s17, 31
	v_rcp_iflag_f32_e32 v1, v1
	v_lshrrev_b32_e32 v5, 6, v0
	v_lshrrev_b32_e32 v15, 2, v0
	v_mov_b32_e32 v3, 0
	v_mul_f32_e32 v1, 0x4f7ffffe, v1
	v_cvt_u32_f32_e32 v1, v1
	v_and_b32_e32 v13, 31, v0
	s_nop 1
	v_readfirstlane_b32 s19, v1
	s_mul_i32 s18, s18, s19
	s_mul_hi_u32 s18, s19, s18
	s_add_i32 s19, s19, s18
	s_mul_hi_u32 s18, s3, s19
	s_mul_i32 s19, s18, s16
	s_sub_i32 s3, s3, s19
	s_add_i32 s20, s18, 1
	s_sub_i32 s19, s3, s16
	s_cmp_ge_u32 s3, s16
	s_cselect_b32 s18, s20, s18
	s_cselect_b32 s3, s19, s3
	s_add_i32 s19, s18, 1
	s_cmp_ge_u32 s3, s16
	s_cselect_b32 s3, s19, s18
	s_abs_i32 s18, s7
	v_cvt_f32_u32_e32 v1, s18
	s_xor_b32 s3, s3, s17
	s_sub_i32 s3, s3, s17
	s_mul_i32 s6, s3, s6
	v_rcp_iflag_f32_e32 v1, v1
	s_sub_i32 s19, 0, s18
	s_sub_i32 s16, s2, s6
	s_xor_b32 s17, s3, s7
	v_mul_f32_e32 v1, 0x4f7ffffe, v1
	v_cvt_u32_f32_e32 v1, v1
	s_ashr_i32 s2, s17, 31
	s_abs_i32 s20, s3
	s_nop 0
	v_readfirstlane_b32 s6, v1
	s_mul_i32 s19, s19, s6
	s_mul_hi_u32 s17, s6, s19
	s_add_i32 s6, s6, s17
	s_mul_hi_u32 s6, s20, s6
	s_mul_i32 s17, s6, s18
	s_sub_i32 s17, s20, s17
	s_add_i32 s19, s6, 1
	s_sub_i32 s20, s17, s18
	s_cmp_ge_u32 s17, s18
	s_cselect_b32 s6, s19, s6
	s_cselect_b32 s17, s20, s17
	s_add_i32 s19, s6, 1
	s_cmp_ge_u32 s17, s18
	s_cselect_b32 s6, s19, s6
	s_xor_b32 s6, s6, s2
	s_sub_i32 s2, s6, s2
	s_mul_i32 s6, s2, s7
	s_sub_i32 s3, s3, s6
	v_lshlrev_b32_e32 v1, 3, v0
	s_mul_i32 s2, s2, s4
	s_lshl_b32 s6, s3, 6
	v_and_b32_e32 v2, 24, v1
	s_ashr_i32 s3, s2, 31
	v_or_b32_e32 v1, s6, v15
	s_ashr_i32 s7, s6, 31
	v_lshl_add_u64 v[6:7], s[2:3], 0, v[2:3]
	v_lshlrev_b32_e32 v3, 5, v5
	v_lshl_or_b32 v4, s16, 7, v3
	s_mul_i32 s17, s14, s7
	v_mad_u64_u32 v[6:7], s[18:19], s14, v1, v[6:7]
	v_mul_lo_u32 v1, s15, v1
	v_add3_u32 v7, v1, v7, s17
	v_or_b32_e32 v10, v4, v13
	v_lshlrev_b64 v[8:9], 1, v[6:7]
	v_ashrrev_i32_e32 v11, 31, v10
	v_lshl_add_u64 v[6:7], s[10:11], 0, v[8:9]
	v_lshl_add_u64 v[8:9], s[8:9], 0, v[8:9]
	v_lshl_add_u64 v[10:11], v[10:11], 2, s[12:13]
	global_load_dwordx4 v[18:21], v[8:9], off
	global_load_dwordx4 v[22:25], v[6:7], off
	global_load_dword v12, v[10:11], off
	s_movk_i32 s9, 0x50
	v_lshlrev_b32_e32 v16, 1, v2
	v_and_b32_e32 v3, 63, v0
	s_nop 7
	v_bfe_u32 v14, v0, 5, 1
	v_mad_u32_u24 v0, v15, s9, v16
	s_cmp_lt_i32 s4, 32
	v_accvgpr_write_b32 a0, 0
	v_accvgpr_write_b32 a1, 0
	v_accvgpr_write_b32 a2, 0
	v_accvgpr_write_b32 a3, 0
	v_accvgpr_write_b32 a4, 0
	v_accvgpr_write_b32 a5, 0
	v_accvgpr_write_b32 a6, 0
	v_accvgpr_write_b32 a7, 0
	v_accvgpr_write_b32 a8, 0
	v_accvgpr_write_b32 a9, 0
	v_accvgpr_write_b32 a10, 0
	v_accvgpr_write_b32 a11, 0
	v_accvgpr_write_b32 a12, 0
	v_accvgpr_write_b32 a13, 0
	v_accvgpr_write_b32 a14, 0
	v_accvgpr_write_b32 a15, 0
	v_accvgpr_write_b32 a16, 0
	v_accvgpr_write_b32 a17, 0
	v_accvgpr_write_b32 a18, 0
	v_accvgpr_write_b32 a19, 0
	v_accvgpr_write_b32 a20, 0
	v_accvgpr_write_b32 a21, 0
	v_accvgpr_write_b32 a22, 0
	v_accvgpr_write_b32 a23, 0
	v_accvgpr_write_b32 a24, 0
	v_accvgpr_write_b32 a25, 0
	v_accvgpr_write_b32 a26, 0
	v_accvgpr_write_b32 a27, 0
	v_accvgpr_write_b32 a28, 0
	v_accvgpr_write_b32 a29, 0
	v_accvgpr_write_b32 a30, 0
	v_accvgpr_write_b32 a31, 0
	s_waitcnt vmcnt(2)
	ds_write_b128 v0, v[18:21]
	s_waitcnt vmcnt(1)
	ds_write_b128 v0, v[22:25] offset:5120
	s_waitcnt lgkmcnt(0)
	s_barrier
	s_cbranch_scc1 .LBB17_7
	s_load_dwordx4 s[12:15], s[0:1], 0x18
	s_load_dword s10, s[0:1], 0x28
	s_lshr_b32 s3, s3, 28
	v_lshl_or_b32 v10, s16, 2, v5
	s_add_i32 s2, s2, s3
	s_ashr_i32 s2, s2, 4
	s_waitcnt lgkmcnt(0)
	s_ashr_i32 s16, s10, 31
	s_lshr_b32 s16, s16, 28
	s_ashr_i32 s8, s4, 31
	s_add_i32 s10, s10, s16
	s_ashr_i32 s3, s2, 31
	s_lshr_b32 s8, s8, 27
	s_ashr_i32 s10, s10, 4
	v_mov_b32_e32 v0, s2
	v_mov_b32_e32 v1, s3
	s_add_i32 s4, s4, s8
	v_mad_i64_i32 v[0:1], s[2:3], v10, s10, v[0:1]
	s_ashr_i32 s4, s4, 5
	v_lshlrev_b64 v[10:11], 10, v[0:1]
	s_add_i32 s8, s4, -1
	v_lshl_or_b32 v10, v3, 4, v10
	s_min_i32 s11, s8, 2
	v_lshl_add_u64 v[0:1], s[12:13], 0, v[10:11]
	global_load_dwordx4 v[30:33], v[8:9], off offset:64
	global_load_dwordx4 v[22:25], v[6:7], off offset:64
	v_lshl_add_u64 v[10:11], s[14:15], 0, v[10:11]
	global_load_dwordx4 v[38:41], v[0:1], off
	global_load_dwordx4 v[18:21], v[0:1], off offset:1024
	global_load_dwordx4 v[54:57], v[10:11], off
	global_load_dwordx4 v[26:29], v[10:11], off offset:1024
	global_load_dwordx4 v[42:45], v[0:1], off offset:2048
	global_load_dwordx4 v[50:53], v[10:11], off offset:2048
	s_lshl_b32 s2, s11, 5
	s_ashr_i32 s3, s2, 31
	s_lshl_b64 s[2:3], s[2:3], 1
	v_lshl_add_u64 v[60:61], v[8:9], 0, s[2:3]
	v_lshl_add_u64 v[58:59], v[6:7], 0, s[2:3]
	global_load_dwordx4 v[46:49], v[60:61], off
	global_load_dwordx4 v[34:37], v[58:59], off
	v_mul_u32_u24_e32 v17, 0x50, v15
	v_lshlrev_b32_e32 v15, 4, v14
	v_mad_u32_u24 v70, v13, s9, v15
	ds_read_b128 v[58:61], v70 offset:2560
	ds_read_b128 v[66:69], v70
	ds_read_b128 v[62:65], v70 offset:7680
	ds_read_b128 v[70:73], v70 offset:5120
	v_mul_u32_u24_e32 v74, 0x50, v13
	s_mov_b32 s2, 4
	s_nop 7
	v_add_u32_e32 v15, v15, v74
	v_add_u32_e32 v16, v16, v17

.LBB17_7:
	s_load_dwordx4 s[8:11], s[0:1], 0x50
	s_waitcnt vmcnt(7)
	v_accvgpr_read_b32 v39, a1
	s_load_dwordx2 s[0:1], s[0:1], 0x40
	v_mul_u32_u24_e32 v41, 0x2800, v5
	v_ashrrev_i32_e32 v5, 31, v4
	v_mov_b32_e32 v0, s6
	v_mul_u32_u24_e32 v14, 0xa0, v14
	s_waitcnt lgkmcnt(0)
	s_mul_i32 s2, s1, s6
	s_mul_i32 s3, s0, s7
	v_accvgpr_read_b32 v40, a0
	s_add_i32 s4, s3, s2
	v_mad_u64_u32 v[0:1], s[2:3], s0, v0, v[4:5]
	v_or_b32_e32 v13, v14, v13
	s_waitcnt vmcnt(0)
	v_fma_f32 v14, s5, v39, v12
	v_fma_f32 v40, s5, v40, v12
	s_mov_b32 s2, 0x43800000
	v_max_f32_e32 v14, 0, v14
	v_max_f32_e32 v40, 0, v40
	v_fma_mixlo_f16 v39, v14, s2, 0
	v_accvgpr_read_b32 v38, a2
	v_fma_mixlo_f16 v42, v40, s2, 0
	v_lshl_or_b32 v13, v13, 1, v41
	v_fma_mixlo_f16 v14, v14, s2, -v39 op_sel_hi:[0,0,1]
	s_barrier
	v_fma_mixlo_f16 v40, v40, s2, -v42 op_sel_hi:[0,0,1]
	ds_write_b16 v13, v42
	ds_write_b16 v13, v40 offset:5120
	ds_write_b16 v13, v39 offset:80
	ds_write_b16 v13, v14 offset:5200
	v_fma_f32 v14, s5, v38, v12
	v_max_f32_e32 v14, 0, v14
	v_fma_mixlo_f16 v38, v14, s2, 0
	v_accvgpr_read_b32 v37, a3
	v_fma_mixlo_f16 v14, v14, s2, -v38 op_sel_hi:[0,0,1]
	ds_write_b16 v13, v38 offset:160
	ds_write_b16 v13, v14 offset:5280
	v_fma_f32 v14, s5, v37, v12
	v_max_f32_e32 v14, 0, v14
	v_fma_mixlo_f16 v37, v14, s2, 0
	v_accvgpr_read_b32 v36, a4
	v_fma_mixlo_f16 v14, v14, s2, -v37 op_sel_hi:[0,0,1]
	ds_write_b16 v13, v37 offset:240
	ds_write_b16 v13, v14 offset:5360
	v_fma_f32 v14, s5, v36, v12
	v_max_f32_e32 v14, 0, v14
	v_fma_mixlo_f16 v36, v14, s2, 0
	v_accvgpr_read_b32 v35, a5
	v_fma_mixlo_f16 v14, v14, s2, -v36 op_sel_hi:[0,0,1]
	ds_write_b16 v13, v36 offset:640
	ds_write_b16 v13, v14 offset:5760
	v_fma_f32 v14, s5, v35, v12
	v_max_f32_e32 v14, 0, v14
	v_fma_mixlo_f16 v35, v14, s2, 0
	v_accvgpr_read_b32 v34, a6
	v_fma_mixlo_f16 v14, v14, s2, -v35 op_sel_hi:[0,0,1]
	ds_write_b16 v13, v35 offset:720
	ds_write_b16 v13, v14 offset:5840
	v_fma_f32 v14, s5, v34, v12
	v_max_f32_e32 v14, 0, v14
	v_fma_mixlo_f16 v34, v14, s2, 0
	v_accvgpr_read_b32 v33, a7
	v_fma_mixlo_f16 v14, v14, s2, -v34 op_sel_hi:[0,0,1]
	ds_write_b16 v13, v34 offset:800
	ds_write_b16 v13, v14 offset:5920
	v_fma_f32 v14, s5, v33, v12
	v_max_f32_e32 v14, 0, v14
	v_fma_mixlo_f16 v33, v14, s2, 0
	v_accvgpr_read_b32 v32, a8
	v_fma_mixlo_f16 v14, v14, s2, -v33 op_sel_hi:[0,0,1]
	ds_write_b16 v13, v33 offset:880
	ds_write_b16 v13, v14 offset:6000
	v_fma_f32 v14, s5, v32, v12
	v_max_f32_e32 v14, 0, v14
	v_fma_mixlo_f16 v32, v14, s2, 0
	v_accvgpr_read_b32 v31, a9
	v_fma_mixlo_f16 v14, v14, s2, -v32 op_sel_hi:[0,0,1]
	ds_write_b16 v13, v32 offset:1280
	ds_write_b16 v13, v14 offset:6400
	v_fma_f32 v14, s5, v31, v12
	v_max_f32_e32 v14, 0, v14
	v_fma_mixlo_f16 v31, v14, s2, 0
	v_accvgpr_read_b32 v30, a10
	v_fma_mixlo_f16 v14, v14, s2, -v31 op_sel_hi:[0,0,1]
	ds_write_b16 v13, v31 offset:1360
	ds_write_b16 v13, v14 offset:6480
	v_fma_f32 v14, s5, v30, v12
	v_max_f32_e32 v14, 0, v14
	v_fma_mixlo_f16 v30, v14, s2, 0
	v_accvgpr_read_b32 v29, a11
	v_fma_mixlo_f16 v14, v14, s2, -v30 op_sel_hi:[0,0,1]
	ds_write_b16 v13, v30 offset:1440
	ds_write_b16 v13, v14 offset:6560
	v_fma_f32 v14, s5, v29, v12
	v_max_f32_e32 v14, 0, v14
	v_fma_mixlo_f16 v29, v14, s2, 0
	v_accvgpr_read_b32 v28, a12
	v_fma_mixlo_f16 v14, v14, s2, -v29 op_sel_hi:[0,0,1]
	ds_write_b16 v13, v29 offset:1520
	ds_write_b16 v13, v14 offset:6640
	v_fma_f32 v14, s5, v28, v12
	v_max_f32_e32 v14, 0, v14
	v_fma_mixlo_f16 v28, v14, s2, 0
	v_accvgpr_read_b32 v27, a13
	v_fma_mixlo_f16 v14, v14, s2, -v28 op_sel_hi:[0,0,1]
	ds_write_b16 v13, v28 offset:1920
	ds_write_b16 v13, v14 offset:7040
	v_fma_f32 v14, s5, v27, v12
	v_max_f32_e32 v14, 0, v14
	v_fma_mixlo_f16 v27, v14, s2, 0
	v_accvgpr_read_b32 v26, a14
	v_fma_mixlo_f16 v14, v14, s2, -v27 op_sel_hi:[0,0,1]
	ds_write_b16 v13, v27 offset:2000
	ds_write_b16 v13, v14 offset:7120
	v_fma_f32 v14, s5, v26, v12
	v_max_f32_e32 v14, 0, v14
	v_fma_mixlo_f16 v26, v14, s2, 0
	v_accvgpr_read_b32 v25, a15
	v_fma_mixlo_f16 v14, v14, s2, -v26 op_sel_hi:[0,0,1]
	ds_write_b16 v13, v26 offset:2080
	ds_write_b16 v13, v14 offset:7200
	v_fma_f32 v14, s5, v25, v12
	v_max_f32_e32 v14, 0, v14
	v_fma_mixlo_f16 v25, v14, s2, 0
	v_accvgpr_read_b32 v24, a16
	v_fma_mixlo_f16 v14, v14, s2, -v25 op_sel_hi:[0,0,1]
	ds_write_b16 v13, v25 offset:2160
	ds_write_b16 v13, v14 offset:7280
	v_fma_f32 v14, s5, v24, v12
	v_max_f32_e32 v14, 0, v14
	v_fma_mixlo_f16 v24, v14, s2, 0
	v_accvgpr_read_b32 v23, a17
	v_fma_mixlo_f16 v14, v14, s2, -v24 op_sel_hi:[0,0,1]
	ds_write_b16 v13, v24 offset:2560
	ds_write_b16 v13, v14 offset:7680
	v_fma_f32 v14, s5, v23, v12
	v_max_f32_e32 v14, 0, v14
	v_fma_mixlo_f16 v23, v14, s2, 0
	v_accvgpr_read_b32 v22, a18
	v_fma_mixlo_f16 v14, v14, s2, -v23 op_sel_hi:[0,0,1]
	ds_write_b16 v13, v23 offset:2640
	ds_write_b16 v13, v14 offset:7760
	v_fma_f32 v14, s5, v22, v12
	v_max_f32_e32 v14, 0, v14
	v_fma_mixlo_f16 v22, v14, s2, 0
	v_accvgpr_read_b32 v21, a19
	v_fma_mixlo_f16 v14, v14, s2, -v22 op_sel_hi:[0,0,1]
	ds_write_b16 v13, v22 offset:2720
	ds_write_b16 v13, v14 offset:7840
	v_fma_f32 v14, s5, v21, v12
	v_max_f32_e32 v14, 0, v14
	v_fma_mixlo_f16 v21, v14, s2, 0
	v_accvgpr_read_b32 v20, a20
	v_fma_mixlo_f16 v14, v14, s2, -v21 op_sel_hi:[0,0,1]
	ds_write_b16 v13, v21 offset:2800
	ds_write_b16 v13, v14 offset:7920
	v_fma_f32 v14, s5, v20, v12
	v_max_f32_e32 v14, 0, v14
	v_fma_mixlo_f16 v20, v14, s2, 0
	v_accvgpr_read_b32 v19, a21
	v_fma_mixlo_f16 v14, v14, s2, -v20 op_sel_hi:[0,0,1]
	ds_write_b16 v13, v20 offset:3200
	ds_write_b16 v13, v14 offset:8320
	v_fma_f32 v14, s5, v19, v12
	v_max_f32_e32 v14, 0, v14
	v_fma_mixlo_f16 v19, v14, s2, 0
	v_accvgpr_read_b32 v18, a22
	v_fma_mixlo_f16 v14, v14, s2, -v19 op_sel_hi:[0,0,1]
	ds_write_b16 v13, v19 offset:3280
	ds_write_b16 v13, v14 offset:8400
	v_fma_f32 v14, s5, v18, v12
	v_max_f32_e32 v14, 0, v14
	v_fma_mixlo_f16 v18, v14, s2, 0
	v_accvgpr_read_b32 v17, a23
	v_fma_mixlo_f16 v14, v14, s2, -v18 op_sel_hi:[0,0,1]
	ds_write_b16 v13, v18 offset:3360
	ds_write_b16 v13, v14 offset:8480
	v_fma_f32 v14, s5, v17, v12
	v_max_f32_e32 v14, 0, v14
	v_fma_mixlo_f16 v17, v14, s2, 0
	v_accvgpr_read_b32 v16, a24
	v_fma_mixlo_f16 v14, v14, s2, -v17 op_sel_hi:[0,0,1]
	ds_write_b16 v13, v17 offset:3440
	ds_write_b16 v13, v14 offset:8560
	v_fma_f32 v14, s5, v16, v12
	v_max_f32_e32 v14, 0, v14
	v_fma_mixlo_f16 v16, v14, s2, 0
	v_accvgpr_read_b32 v15, a25
	v_fma_mixlo_f16 v14, v14, s2, -v16 op_sel_hi:[0,0,1]
	ds_write_b16 v13, v16 offset:3840
	ds_write_b16 v13, v14 offset:8960
	v_fma_f32 v14, s5, v15, v12
	v_accvgpr_read_b32 v11, a26
	v_max_f32_e32 v14, 0, v14
	v_fma_mixlo_f16 v15, v14, s2, 0
	v_fma_f32 v11, s5, v11, v12
	v_accvgpr_read_b32 v10, a27
	v_fma_mixlo_f16 v14, v14, s2, -v15 op_sel_hi:[0,0,1]
	v_max_f32_e32 v11, 0, v11
	ds_write_b16 v13, v15 offset:3920
	ds_write_b16 v13, v14 offset:9040
	v_fma_mixlo_f16 v14, v11, s2, 0
	v_fma_f32 v10, s5, v10, v12
	v_accvgpr_read_b32 v9, a28
	v_fma_mixlo_f16 v11, v11, s2, -v14 op_sel_hi:[0,0,1]
	v_max_f32_e32 v10, 0, v10
	ds_write_b16 v13, v14 offset:4000
	ds_write_b16 v13, v11 offset:9120
	v_fma_mixlo_f16 v11, v10, s2, 0
	v_fma_f32 v9, s5, v9, v12
	v_accvgpr_read_b32 v8, a29
	v_fma_mixlo_f16 v10, v10, s2, -v11 op_sel_hi:[0,0,1]
	v_max_f32_e32 v9, 0, v9
	ds_write_b16 v13, v11 offset:4080
	ds_write_b16 v13, v10 offset:9200
	v_fma_mixlo_f16 v10, v9, s2, 0
	v_fma_f32 v8, s5, v8, v12
	v_accvgpr_read_b32 v7, a30
	v_fma_mixlo_f16 v9, v9, s2, -v10 op_sel_hi:[0,0,1]
	v_max_f32_e32 v8, 0, v8
	ds_write_b16 v13, v10 offset:4480
	ds_write_b16 v13, v9 offset:9600
	v_fma_mixlo_f16 v9, v8, s2, 0
	v_fma_f32 v7, s5, v7, v12
	v_accvgpr_read_b32 v6, a31
	v_fma_mixlo_f16 v8, v8, s2, -v9 op_sel_hi:[0,0,1]
	v_max_f32_e32 v7, 0, v7
	ds_write_b16 v13, v9 offset:4560
	ds_write_b16 v13, v8 offset:9680
	v_fma_mixlo_f16 v8, v7, s2, 0
	v_fmac_f32_e32 v12, s5, v6
	v_fma_mixlo_f16 v7, v7, s2, -v8 op_sel_hi:[0,0,1]
	v_max_f32_e32 v6, 0, v12
	v_lshrrev_b32_e32 v20, 2, v3
	v_add_u32_e32 v1, s4, v1
	v_or_b32_e32 v0, v0, v2
	v_lshl_or_b32 v2, v2, 1, v41
	ds_write_b16 v13, v8 offset:4640
	ds_write_b16 v13, v7 offset:9760
	v_fma_mixlo_f16 v7, v6, s2, 0
	v_mul_u32_u24_e32 v3, 40, v20
	v_lshlrev_b64 v[4:5], 1, v[0:1]
	v_fma_mixlo_f16 v6, v6, s2, -v7 op_sel_hi:[0,0,1]
	ds_write_b16 v13, v7 offset:4720
	ds_write_b16 v13, v6 offset:9840
	v_lshl_add_u32 v21, v3, 1, v2
	v_mad_u64_u32 v[10:11], s[2:3], s0, v20, 0
	v_lshl_add_u64 v[0:1], s[8:9], 0, v[4:5]
	v_lshl_add_u64 v[14:15], s[10:11], 0, v[4:5]
	ds_read_b128 v[2:5], v21
	ds_read_b128 v[6:9], v21 offset:5120
	v_mov_b32_e32 v12, v11
	v_mad_u64_u32 v[12:13], s[2:3], s1, v20, v[12:13]
	v_mov_b32_e32 v11, v12
	v_lshlrev_b64 v[16:17], 1, v[10:11]
	v_lshl_add_u64 v[18:19], v[0:1], 0, v[16:17]
	v_lshl_add_u64 v[16:17], v[14:15], 0, v[16:17]
	s_waitcnt lgkmcnt(0)
	global_store_dwordx4 v[16:17], v[6:9], off sc1
	ds_read_b128 v[10:13], v21 offset:1280
	global_store_dwordx4 v[18:19], v[2:5], off sc1
	v_or_b32_e32 v9, 16, v20
	v_mad_u64_u32 v[6:7], s[2:3], s0, v9, 0
	v_mov_b32_e32 v8, v7
	ds_read_b128 v[2:5], v21 offset:6400
	v_mad_u64_u32 v[8:9], s[2:3], s1, v9, v[8:9]
	v_mov_b32_e32 v7, v8
	v_lshlrev_b64 v[6:7], 1, v[6:7]
	v_lshl_add_u64 v[8:9], v[0:1], 0, v[6:7]
	s_waitcnt lgkmcnt(1)
	global_store_dwordx4 v[8:9], v[10:13], off sc1
	v_lshl_add_u64 v[6:7], v[14:15], 0, v[6:7]
	s_waitcnt lgkmcnt(0)
	global_store_dwordx4 v[6:7], v[2:5], off sc1
	v_or_b32_e32 v13, 32, v20
	v_mad_u64_u32 v[10:11], s[2:3], s0, v13, 0
	ds_read_b128 v[2:5], v21 offset:2560
	ds_read_b128 v[6:9], v21 offset:7680
	v_mov_b32_e32 v12, v11
	v_mad_u64_u32 v[12:13], s[2:3], s1, v13, v[12:13]
	v_mov_b32_e32 v11, v12
	v_lshlrev_b64 v[16:17], 1, v[10:11]
	v_lshl_add_u64 v[18:19], v[0:1], 0, v[16:17]
	v_lshl_add_u64 v[16:17], v[14:15], 0, v[16:17]
	s_waitcnt lgkmcnt(0)
	global_store_dwordx4 v[16:17], v[6:9], off sc1
	ds_read_b128 v[10:13], v21 offset:3840
	global_store_dwordx4 v[18:19], v[2:5], off sc1
	v_or_b32_e32 v9, 48, v20
	v_mad_u64_u32 v[6:7], s[2:3], s0, v9, 0
	v_mov_b32_e32 v8, v7
	ds_read_b128 v[2:5], v21 offset:8960
	v_mad_u64_u32 v[8:9], s[0:1], s1, v9, v[8:9]
	v_mov_b32_e32 v7, v8
	v_lshlrev_b64 v[6:7], 1, v[6:7]
	v_lshl_add_u64 v[0:1], v[0:1], 0, v[6:7]
	s_waitcnt lgkmcnt(1)
	global_store_dwordx4 v[0:1], v[10:13], off sc1
	v_lshl_add_u64 v[0:1], v[14:15], 0, v[6:7]
	s_waitcnt lgkmcnt(0)
	global_store_dwordx4 v[0:1], v[2:5], off sc1
	s_endpgm
	s_endpgm
	s_endpgm
	s_endpgm
	s_endpgm
	s_endpgm
	s_endpgm
	s_endpgm
	s_endpgm
	s_endpgm
	s_endpgm
	s_endpgm
	s_endpgm
	.section	.rodata,"a",@progbits
	.p2align	6, 0x0

.LBB18_4:
	s_load_dwordx4 s[4:7], s[0:1], 0x60
	s_load_dword s16, s[0:1], 0x70
	s_ashr_i32 s2, s2, 3
	s_add_i32 s2, s3, s2
	s_abs_i32 s3, s2
	s_waitcnt lgkmcnt(0)
	s_abs_i32 s17, s7
	v_cvt_f32_u32_e32 v1, s17
	s_sub_i32 s19, 0, s17
	s_xor_b32 s18, s2, s7
	s_ashr_i32 s18, s18, 31
	v_rcp_iflag_f32_e32 v1, v1
	v_and_b32_e32 v13, 31, v0
	v_mov_b32_e32 v3, 0
	v_mul_f32_e32 v1, 0x4f7ffffe, v1
	v_cvt_u32_f32_e32 v1, v1
	s_nop 2
	v_readfirstlane_b32 s20, v1
	s_mul_i32 s19, s19, s20
	s_mul_hi_u32 s19, s20, s19
	s_add_i32 s20, s20, s19
	s_mul_hi_u32 s19, s3, s20
	s_mul_i32 s20, s19, s17
	s_sub_i32 s3, s3, s20
	s_add_i32 s21, s19, 1
	s_sub_i32 s20, s3, s17
	s_cmp_ge_u32 s3, s17
	s_cselect_b32 s19, s21, s19
	s_cselect_b32 s3, s20, s3
	s_add_i32 s20, s19, 1
	s_cmp_ge_u32 s3, s17
	s_cselect_b32 s3, s20, s19
	s_abs_i32 s17, s16
	v_cvt_f32_u32_e32 v1, s17
	s_xor_b32 s3, s3, s18
	s_sub_i32 s18, s3, s18
	s_mul_i32 s3, s18, s7
	v_rcp_iflag_f32_e32 v1, v1
	s_sub_i32 s2, s2, s3
	s_sub_i32 s22, 0, s17
	s_lshl_b32 s7, s2, 6
	v_mul_f32_e32 v1, 0x4f7ffffe, v1
	v_cvt_u32_f32_e32 v1, v1
	s_abs_i32 s21, s18
	s_ashr_i32 s19, s16, 31
	s_ashr_i32 s20, s18, 31
	v_readfirstlane_b32 s2, v1
	v_lshrrev_b32_e32 v1, 1, v0
	s_mul_i32 s22, s22, s2
	v_and_b32_e32 v1, 32, v1
	s_mul_hi_u32 s3, s2, s22
	v_or_b32_e32 v16, v1, v13
	s_add_i32 s2, s2, s3
	v_or_b32_e32 v4, s7, v16
	s_mul_hi_u32 s22, s21, s2
	v_cmp_gt_i32_e32 vcc, s4, v4
	s_nop 7
	v_mov_b32_e32 v12, 0
	s_and_saveexec_b64 s[2:3], vcc
	s_cbranch_execz .LBB18_6
	s_load_dwordx2 s[24:25], s[0:1], 0x30
	v_ashrrev_i32_e32 v5, 31, v4
	s_waitcnt lgkmcnt(0)
	v_lshl_add_u64 v[4:5], v[4:5], 2, s[24:25]
	global_load_dword v12, v[4:5], off
.LBB18_6:
	s_or_b64 exec, exec, s[2:3]
	s_xor_b32 s2, s20, s19
	s_mul_i32 s19, s22, s17
	s_sub_i32 s19, s21, s19
	s_add_i32 s20, s22, 1
	s_sub_i32 s21, s19, s17
	s_cmp_ge_u32 s19, s17
	s_cselect_b32 s20, s20, s22
	s_cselect_b32 s19, s21, s19
	s_add_i32 s21, s20, 1
	s_cmp_ge_u32 s19, s17
	s_cselect_b32 s17, s21, s20
	s_xor_b32 s17, s17, s2
	s_sub_i32 s17, s17, s2
	s_load_dwordx2 s[24:25], s[0:1], 0x10
	s_load_dword s3, s[0:1], 0x28
	s_mul_i32 s2, s17, s16
	s_sub_i32 s2, s18, s2
	v_lshlrev_b32_e32 v2, 3, v0
	s_mul_i32 s16, s17, s5
	s_lshl_b32 s2, s2, 6
	v_lshrrev_b32_e32 v15, 2, v0
	v_and_b32_e32 v2, 24, v2
	s_ashr_i32 s17, s16, 31
	v_or_b32_e32 v8, s2, v15
	s_ashr_i32 s18, s2, 31
	v_lshl_add_u64 v[4:5], s[16:17], 0, v[2:3]
	s_waitcnt lgkmcnt(0)
	s_mul_i32 s18, s24, s18
	v_mad_u64_u32 v[6:7], s[16:17], s24, v8, v[4:5]
	v_mul_lo_u32 v3, s25, v8
	v_add3_u32 v7, v3, v7, s18
	v_add_u32_e32 v3, s7, v15
	s_add_i32 s4, s4, -1
	v_min_i32_e32 v3, s4, v3
	v_mad_i64_i32 v[8:9], s[16:17], v3, s3, v[4:5]
	v_lshlrev_b64 v[8:9], 1, v[8:9]
	v_lshlrev_b64 v[10:11], 1, v[6:7]
	v_lshl_add_u64 v[6:7], s[12:13], 0, v[8:9]
	global_load_dwordx4 v[70:73], v[6:7], off
	v_lshl_add_u64 v[8:9], s[14:15], 0, v[8:9]
	v_lshl_add_u64 v[4:5], s[8:9], 0, v[10:11]
	global_load_dwordx4 v[74:77], v[8:9], off
	global_load_dwordx4 v[78:81], v[4:5], off
	v_lshl_add_u64 v[10:11], s[10:11], 0, v[10:11]
	global_load_dwordx4 v[82:85], v[10:11], off
	v_and_b32_e32 v3, 32, v15
	v_mul_u32_u24_e32 v15, 40, v15
	v_lshlrev_b32_e32 v17, 1, v2
	v_bfe_u32 v14, v0, 5, 1
	v_lshl_add_u32 v15, v15, 1, v17
	s_ashr_i32 s3, s5, 31
	s_lshr_b32 s3, s3, 27
	s_add_i32 s3, s5, s3
	s_ashr_i32 s3, s3, 5
	s_add_i32 s4, s3, -1
	s_min_i32 s5, s4, 2
	s_lshl_b32 s8, s5, 5
	s_ashr_i32 s9, s8, 31
	global_load_dwordx4 v[18:21], v[4:5], off offset:64
	global_load_dwordx4 v[22:25], v[10:11], off offset:64
	global_load_dwordx4 v[26:29], v[6:7], off offset:64
	global_load_dwordx4 v[34:37], v[8:9], off offset:64
	s_lshl_b64 s[8:9], s[8:9], 1
	v_lshl_add_u64 v[30:31], v[4:5], 0, s[8:9]
	v_lshl_add_u64 v[38:39], v[10:11], 0, s[8:9]
	v_lshl_add_u64 v[42:43], v[6:7], 0, s[8:9]
	v_lshl_add_u64 v[46:47], v[8:9], 0, s[8:9]
	global_load_dwordx4 v[30:33], v[30:31], off
	v_lshlrev_b32_e32 v66, 4, v14
	global_load_dwordx4 v[38:41], v[38:39], off
	s_movk_i32 s5, 0x50
	global_load_dwordx4 v[42:45], v[42:43], off
	v_or_b32_e32 v17, v3, v13
	global_load_dwordx4 v[46:49], v[46:47], off
	v_accvgpr_write_b32 a0, 0
	v_accvgpr_write_b32 a1, 0
	v_accvgpr_write_b32 a2, 0
	v_accvgpr_write_b32 a3, 0
	v_accvgpr_write_b32 a4, 0
	v_accvgpr_write_b32 a5, 0
	v_accvgpr_write_b32 a6, 0
	v_accvgpr_write_b32 a7, 0
	v_accvgpr_write_b32 a8, 0
	v_accvgpr_write_b32 a9, 0
	v_accvgpr_write_b32 a10, 0
	v_accvgpr_write_b32 a11, 0
	v_accvgpr_write_b32 a12, 0
	v_accvgpr_write_b32 a13, 0
	v_accvgpr_write_b32 a14, 0
	v_accvgpr_write_b32 a15, 0
	s_waitcnt vmcnt(11)
	ds_write_b128 v15, v[70:73] offset:10240
	s_waitcnt vmcnt(10)
	ds_write_b128 v15, v[74:77] offset:15360
	s_waitcnt vmcnt(9)
	ds_write_b128 v15, v[78:81]
	s_waitcnt vmcnt(8)
	ds_write_b128 v15, v[82:85] offset:5120
	s_waitcnt lgkmcnt(0)
	s_barrier
	v_mul_u32_u24_e32 v67, 0x50, v16
	v_mad_u32_u24 v16, v16, s5, v66
	v_mul_u32_u24_e32 v68, 0x50, v17
	v_mad_u32_u24 v17, v17, s5, v66
	ds_read_b128 v[58:61], v16 offset:15360
	ds_read_b128 v[50:53], v16 offset:10240
	ds_read_b128 v[54:57], v17
	ds_read_b128 v[62:65], v17 offset:5120
	s_nop 7
	s_mov_b32 s5, 0
	v_add_u32_e32 v16, v66, v68
	v_add_u32_e32 v17, v66, v67

.LBB18_9:
	s_waitcnt vmcnt(7)
	s_nop 7
	v_accvgpr_read_b32 v21, a1
	v_mul_u32_u24_e32 v14, 0xa0, v14
	s_waitcnt vmcnt(6)
	v_accvgpr_read_b32 v22, a0
	v_or_b32_e32 v13, v14, v13
	v_fma_f32 v14, s6, v21, v12
	v_lshrrev_b32_e32 v23, 6, v0
	v_fma_f32 v22, s6, v22, v12
	s_mov_b32 s3, 0x43800000
	v_max_f32_e32 v14, 0, v14
	v_mul_u32_u24_e32 v23, 0x1400, v23
	v_max_f32_e32 v22, 0, v22
	v_fma_mixlo_f16 v21, v14, s3, 0
	v_accvgpr_read_b32 v20, a2
	v_fma_mixlo_f16 v24, v22, s3, 0
	v_lshl_or_b32 v13, v13, 1, v23
	v_fma_mixlo_f16 v14, v14, s3, -v21 op_sel_hi:[0,0,1]
	s_load_dwordx4 s[8:11], s[0:1], 0x50
	v_fma_mixlo_f16 v22, v22, s3, -v24 op_sel_hi:[0,0,1]
	s_load_dwordx2 s[0:1], s[0:1], 0x40
	s_waitcnt lgkmcnt(0)
	s_barrier
	ds_write_b16 v13, v24
	ds_write_b16 v13, v22 offset:2560
	ds_write_b16 v13, v21 offset:80
	ds_write_b16 v13, v14 offset:2640
	v_fma_f32 v14, s6, v20, v12
	v_max_f32_e32 v14, 0, v14
	v_fma_mixlo_f16 v20, v14, s3, 0
	v_accvgpr_read_b32 v19, a3
	v_fma_mixlo_f16 v14, v14, s3, -v20 op_sel_hi:[0,0,1]
	ds_write_b16 v13, v20 offset:160
	ds_write_b16 v13, v14 offset:2720
	v_fma_f32 v14, s6, v19, v12
	v_max_f32_e32 v14, 0, v14
	v_fma_mixlo_f16 v19, v14, s3, 0
	v_accvgpr_read_b32 v18, a4
	v_fma_mixlo_f16 v14, v14, s3, -v19 op_sel_hi:[0,0,1]
	ds_write_b16 v13, v19 offset:240
	ds_write_b16 v13, v14 offset:2800
	v_fma_f32 v14, s6, v18, v12
	v_max_f32_e32 v14, 0, v14
	v_fma_mixlo_f16 v18, v14, s3, 0
	v_accvgpr_read_b32 v17, a5
	v_fma_mixlo_f16 v14, v14, s3, -v18 op_sel_hi:[0,0,1]
	ds_write_b16 v13, v18 offset:640
	ds_write_b16 v13, v14 offset:3200
	v_fma_f32 v14, s6, v17, v12
	v_max_f32_e32 v14, 0, v14
	v_fma_mixlo_f16 v17, v14, s3, 0
	v_accvgpr_read_b32 v16, a6
	v_fma_mixlo_f16 v14, v14, s3, -v17 op_sel_hi:[0,0,1]
	ds_write_b16 v13, v17 offset:720
	ds_write_b16 v13, v14 offset:3280
	v_fma_f32 v14, s6, v16, v12
	v_max_f32_e32 v14, 0, v14
	v_fma_mixlo_f16 v16, v14, s3, 0
	v_accvgpr_read_b32 v15, a7
	v_fma_mixlo_f16 v14, v14, s3, -v16 op_sel_hi:[0,0,1]
	ds_write_b16 v13, v16 offset:800
	ds_write_b16 v13, v14 offset:3360
	v_fma_f32 v14, s6, v15, v12
	v_accvgpr_read_b32 v11, a8
	v_max_f32_e32 v14, 0, v14
	v_fma_mixlo_f16 v15, v14, s3, 0
	v_fma_f32 v11, s6, v11, v12
	v_accvgpr_read_b32 v10, a9
	v_fma_mixlo_f16 v14, v14, s3, -v15 op_sel_hi:[0,0,1]
	v_max_f32_e32 v11, 0, v11
	ds_write_b16 v13, v15 offset:880
	ds_write_b16 v13, v14 offset:3440
	v_fma_mixlo_f16 v14, v11, s3, 0
	v_fma_f32 v10, s6, v10, v12
	v_accvgpr_read_b32 v9, a10
	v_fma_mixlo_f16 v11, v11, s3, -v14 op_sel_hi:[0,0,1]
	v_max_f32_e32 v10, 0, v10
	ds_write_b16 v13, v14 offset:1280
	ds_write_b16 v13, v11 offset:3840
	v_fma_mixlo_f16 v11, v10, s3, 0
	v_fma_f32 v9, s6, v9, v12
	v_accvgpr_read_b32 v8, a11
	v_fma_mixlo_f16 v10, v10, s3, -v11 op_sel_hi:[0,0,1]
	v_max_f32_e32 v9, 0, v9
	ds_write_b16 v13, v11 offset:1360
	ds_write_b16 v13, v10 offset:3920
	v_fma_mixlo_f16 v10, v9, s3, 0
	v_fma_f32 v8, s6, v8, v12
	v_accvgpr_read_b32 v7, a12
	v_fma_mixlo_f16 v9, v9, s3, -v10 op_sel_hi:[0,0,1]
	v_max_f32_e32 v8, 0, v8
	ds_write_b16 v13, v10 offset:1440
	ds_write_b16 v13, v9 offset:4000
	v_fma_mixlo_f16 v9, v8, s3, 0
	v_fma_f32 v7, s6, v7, v12
	v_accvgpr_read_b32 v6, a13
	v_fma_mixlo_f16 v8, v8, s3, -v9 op_sel_hi:[0,0,1]
	v_max_f32_e32 v7, 0, v7
	ds_write_b16 v13, v9 offset:1520
	ds_write_b16 v13, v8 offset:4080
	v_fma_mixlo_f16 v8, v7, s3, 0
	v_fma_f32 v6, s6, v6, v12
	v_accvgpr_read_b32 v5, a14
	v_fma_mixlo_f16 v7, v7, s3, -v8 op_sel_hi:[0,0,1]
	v_max_f32_e32 v6, 0, v6
	ds_write_b16 v13, v8 offset:1920
	ds_write_b16 v13, v7 offset:4480
	v_fma_mixlo_f16 v7, v6, s3, 0
	v_fma_f32 v5, s6, v5, v12
	v_accvgpr_read_b32 v4, a15
	v_fma_mixlo_f16 v6, v6, s3, -v7 op_sel_hi:[0,0,1]
	v_max_f32_e32 v5, 0, v5
	ds_write_b16 v13, v7 offset:2000
	ds_write_b16 v13, v6 offset:4560
	v_fma_mixlo_f16 v6, v5, s3, 0
	v_fmac_f32_e32 v12, s6, v4
	v_fma_mixlo_f16 v5, v5, s3, -v6 op_sel_hi:[0,0,1]
	v_max_f32_e32 v4, 0, v12
	ds_write_b16 v13, v6 offset:2080
	ds_write_b16 v13, v5 offset:4640
	v_fma_mixlo_f16 v5, v4, s3, 0
	v_and_b32_e32 v0, 63, v0
	v_fma_mixlo_f16 v4, v4, s3, -v5 op_sel_hi:[0,0,1]
	v_add_u32_e32 v3, s2, v3
	s_ashr_i32 s2, s7, 31
	ds_write_b16 v13, v5 offset:2160
	ds_write_b16 v13, v4 offset:4720
	v_lshrrev_b32_e32 v20, 2, v0
	v_ashrrev_i32_e32 v4, 31, v3
	v_or3_b32 v0, v1, v2, s7
	v_mov_b32_e32 v1, s2
	v_mul_lo_u32 v4, s0, v4
	v_mad_u64_u32 v[0:1], s[2:3], s0, v3, v[0:1]
	v_mul_lo_u32 v3, s1, v3
	v_add3_u32 v1, v3, v1, v4
	v_lshlrev_b64 v[0:1], 1, v[0:1]
	v_lshl_or_b32 v2, v2, 1, v23
	v_lshl_add_u64 v[12:13], s[8:9], 0, v[0:1]
	v_lshl_add_u64 v[14:15], s[10:11], 0, v[0:1]
	v_mul_u32_u24_e32 v0, 40, v20
	v_lshl_add_u32 v21, v0, 1, v2
	v_mad_u64_u32 v[8:9], s[2:3], s0, v20, 0
	ds_read_b128 v[0:3], v21
	ds_read_b128 v[4:7], v21 offset:2560
	v_mov_b32_e32 v10, v9
	v_mad_u64_u32 v[10:11], s[2:3], s1, v20, v[10:11]
	v_mov_b32_e32 v9, v10
	v_lshlrev_b64 v[16:17], 1, v[8:9]
	v_lshl_add_u64 v[18:19], v[12:13], 0, v[16:17]
	v_lshl_add_u64 v[16:17], v[14:15], 0, v[16:17]
	s_waitcnt lgkmcnt(0)
	global_store_dwordx4 v[16:17], v[4:7], off sc1
	ds_read_b128 v[8:11], v21 offset:1280
	global_store_dwordx4 v[18:19], v[0:3], off sc1
	v_or_b32_e32 v7, 16, v20
	v_mad_u64_u32 v[4:5], s[2:3], s0, v7, 0
	ds_read_b128 v[0:3], v21 offset:3840
	v_mov_b32_e32 v6, v5
	v_mad_u64_u32 v[6:7], s[0:1], s1, v7, v[6:7]
	v_mov_b32_e32 v5, v6
	v_lshlrev_b64 v[4:5], 1, v[4:5]
	v_lshl_add_u64 v[6:7], v[12:13], 0, v[4:5]
	v_lshl_add_u64 v[4:5], v[14:15], 0, v[4:5]
	s_waitcnt lgkmcnt(1)
	global_store_dwordx4 v[6:7], v[8:11], off sc1
	s_waitcnt lgkmcnt(0)
	global_store_dwordx4 v[4:5], v[0:3], off sc1
	s_endpgm
	s_endpgm
	s_endpgm
	s_endpgm
	s_endpgm
	s_endpgm
	s_endpgm
	s_endpgm
	s_endpgm
	s_endpgm
	s_endpgm
	.section	.rodata,"a",@progbits
	.p2align	6, 0x0

.LBB23_8:
	s_or_b64 exec, exec, s[18:19]
	s_mul_i32 s19, s22, s21
	s_sub_i32 s7, s7, s19
	s_xor_b32 s18, s23, s24
	s_add_i32 s19, s22, 1
	s_sub_i32 s23, s7, s21
	s_cmp_ge_u32 s7, s21
	s_cselect_b32 s19, s19, s22
	s_cselect_b32 s7, s23, s7
	s_add_i32 s22, s19, 1
	s_cmp_ge_u32 s7, s21
	s_cselect_b32 s7, s22, s19
	s_xor_b32 s7, s7, s18
	s_sub_i32 s7, s7, s18
	s_load_dwordx2 s[16:17], s[0:1], 0x10
	s_load_dword s25, s[0:1], 0x28
	s_mul_i32 s3, s7, s3
	v_lshlrev_b32_e32 v2, 3, v0
	s_mul_i32 s18, s7, s5
	s_sub_i32 s3, s20, s3
	v_lshrrev_b32_e32 v23, 2, v0
	v_and_b32_e32 v56, 24, v2
	s_ashr_i32 s19, s18, 31
	v_mov_b32_e32 v57, 0
	s_lshl_b32 s3, s3, 7
	v_lshl_add_u64 v[2:3], s[18:19], 0, v[56:57]
	v_add_u32_e32 v4, s2, v23
	s_add_i32 s18, s4, -1
	v_or_b32_e32 v6, s3, v23
	s_ashr_i32 s7, s3, 31
	v_min_i32_e32 v7, s18, v4
	v_add_u32_e32 v4, 64, v4
	v_min_i32_e32 v8, s18, v4
	s_waitcnt lgkmcnt(0)
	s_mul_i32 s7, s16, s7
	v_mad_u64_u32 v[4:5], s[18:19], s16, v6, v[2:3]
	v_mul_lo_u32 v6, s17, v6
	v_add3_u32 v5, v6, v5, s7
	v_lshlrev_b64 v[4:5], 1, v[4:5]
	v_mad_i64_i32 v[10:11], s[18:19], v7, s25, v[2:3]
	v_mad_i64_i32 v[14:15], s[18:19], v8, s25, v[2:3]
	v_lshl_add_u64 v[2:3], s[12:13], 0, v[4:5]
	global_load_dwordx4 v[24:27], v[2:3], off
	v_lshl_add_u64 v[4:5], s[14:15], 0, v[4:5]
	s_lshl_b64 s[12:13], s[16:17], 7
	global_load_dwordx4 v[28:31], v[4:5], off
	v_lshl_add_u64 v[6:7], v[2:3], 0, s[12:13]
	global_load_dwordx4 v[32:35], v[6:7], off
	v_lshl_add_u64 v[8:9], v[4:5], 0, s[12:13]
	v_lshlrev_b64 v[12:13], 1, v[10:11]
	global_load_dwordx4 v[36:39], v[8:9], off
	v_lshl_add_u64 v[10:11], s[8:9], 0, v[12:13]
	global_load_dwordx4 v[40:43], v[10:11], off
	v_lshl_add_u64 v[12:13], s[10:11], 0, v[12:13]
	v_lshlrev_b64 v[16:17], 1, v[14:15]
	global_load_dwordx4 v[44:47], v[12:13], off
	v_lshl_add_u64 v[14:15], s[8:9], 0, v[16:17]
	global_load_dwordx4 v[48:51], v[14:15], off
	v_lshl_add_u64 v[16:17], s[10:11], 0, v[16:17]
	global_load_dwordx4 v[52:55], v[16:17], off
	s_load_dwordx2 s[8:9], s[0:1], 0x38
	v_lshrrev_b32_e32 v21, 1, v0
	v_mul_u32_u24_e32 v23, 40, v23
	v_lshlrev_b32_e32 v56, 1, v56
	s_nop 7
	v_and_b32_e32 v21, 64, v21
	v_bfe_u32 v22, v0, 5, 1
	v_lshl_add_u32 v23, v23, 1, v56
	s_cmp_lt_i32 s5, 32
	v_accvgpr_write_b32 a48, 0
	v_accvgpr_write_b32 a49, 0
	v_accvgpr_write_b32 a50, 0
	v_accvgpr_write_b32 a51, 0
	v_accvgpr_write_b32 a52, 0
	v_accvgpr_write_b32 a53, 0
	v_accvgpr_write_b32 a54, 0
	v_accvgpr_write_b32 a55, 0
	v_accvgpr_write_b32 a56, 0
	v_accvgpr_write_b32 a57, 0
	v_accvgpr_write_b32 a58, 0
	v_accvgpr_write_b32 a59, 0
	v_accvgpr_write_b32 a60, 0
	v_accvgpr_write_b32 a61, 0
	v_accvgpr_write_b32 a62, 0
	v_accvgpr_write_b32 a63, 0
	v_accvgpr_write_b32 a32, 0
	v_accvgpr_write_b32 a33, 0
	v_accvgpr_write_b32 a34, 0
	v_accvgpr_write_b32 a35, 0
	v_accvgpr_write_b32 a36, 0
	v_accvgpr_write_b32 a37, 0
	v_accvgpr_write_b32 a38, 0
	v_accvgpr_write_b32 a39, 0
	v_accvgpr_write_b32 a40, 0
	v_accvgpr_write_b32 a41, 0
	v_accvgpr_write_b32 a42, 0
	v_accvgpr_write_b32 a43, 0
	v_accvgpr_write_b32 a44, 0
	v_accvgpr_write_b32 a45, 0
	v_accvgpr_write_b32 a46, 0
	v_accvgpr_write_b32 a47, 0
	v_accvgpr_write_b32 a16, 0
	v_accvgpr_write_b32 a17, 0
	v_accvgpr_write_b32 a18, 0
	v_accvgpr_write_b32 a19, 0
	v_accvgpr_write_b32 a20, 0
	v_accvgpr_write_b32 a21, 0
	v_accvgpr_write_b32 a22, 0
	v_accvgpr_write_b32 a23, 0
	v_accvgpr_write_b32 a24, 0
	v_accvgpr_write_b32 a25, 0
	v_accvgpr_write_b32 a26, 0
	v_accvgpr_write_b32 a27, 0
	v_accvgpr_write_b32 a28, 0
	v_accvgpr_write_b32 a29, 0
	v_accvgpr_write_b32 a30, 0
	v_accvgpr_write_b32 a31, 0
	v_accvgpr_write_b32 a0, 0
	v_accvgpr_write_b32 a1, 0
	v_accvgpr_write_b32 a2, 0
	v_accvgpr_write_b32 a3, 0
	v_accvgpr_write_b32 a4, 0
	v_accvgpr_write_b32 a5, 0
	v_accvgpr_write_b32 a6, 0
	v_accvgpr_write_b32 a7, 0
	v_accvgpr_write_b32 a8, 0
	v_accvgpr_write_b32 a9, 0
	v_accvgpr_write_b32 a10, 0
	v_accvgpr_write_b32 a11, 0
	v_accvgpr_write_b32 a12, 0
	v_accvgpr_write_b32 a13, 0
	v_accvgpr_write_b32 a14, 0
	v_accvgpr_write_b32 a15, 0
	s_waitcnt vmcnt(7)
	ds_write_b128 v23, v[24:27]
	s_waitcnt vmcnt(6)
	ds_write_b128 v23, v[28:31] offset:10240
	s_waitcnt vmcnt(5)
	ds_write_b128 v23, v[32:35] offset:5120
	s_waitcnt vmcnt(4)
	ds_write_b128 v23, v[36:39] offset:15360
	s_waitcnt vmcnt(3)
	ds_write_b128 v23, v[40:43] offset:20480
	s_waitcnt vmcnt(2)
	ds_write_b128 v23, v[44:47] offset:30720
	s_waitcnt vmcnt(1)
	ds_write_b128 v23, v[48:51] offset:25600
	s_waitcnt vmcnt(0)
	ds_write_b128 v23, v[52:55] offset:35840
	s_waitcnt lgkmcnt(0)
	s_barrier
	s_cbranch_scc1 .LBB23_11
	s_ashr_i32 s7, s5, 31
	s_lshr_b32 s7, s7, 27
	s_add_i32 s5, s5, s7
	s_ashr_i32 s5, s5, 5
	s_add_i32 s7, s5, -1
	s_min_i32 s10, s7, 2
	s_lshl_b32 s10, s10, 5
	s_ashr_i32 s11, s10, 31
	s_lshl_b64 s[10:11], s[10:11], 1
	v_lshl_add_u64 v[24:25], v[2:3], 0, s[10:11]
	global_load_dwordx4 v[30:33], v[2:3], off offset:64
	global_load_dwordx4 v[34:37], v[4:5], off offset:64
	global_load_dwordx4 v[42:45], v[6:7], off offset:64
	global_load_dwordx4 v[54:57], v[8:9], off offset:64
	global_load_dwordx4 v[46:49], v[10:11], off offset:64
	global_load_dwordx4 v[50:53], v[12:13], off offset:64
	global_load_dwordx4 v[58:61], v[14:15], off offset:64
	global_load_dwordx4 v[62:65], v[16:17], off offset:64
	global_load_dwordx4 v[38:41], v[24:25], off
	v_lshl_add_u64 v[24:25], v[4:5], 0, s[10:11]
	global_load_dwordx4 v[66:69], v[24:25], off
	v_lshl_add_u64 v[24:25], v[6:7], 0, s[10:11]
	global_load_dwordx4 v[70:73], v[24:25], off
	v_lshl_add_u64 v[24:25], v[8:9], 0, s[10:11]
	global_load_dwordx4 v[78:81], v[24:25], off
	v_lshl_add_u64 v[24:25], v[10:11], 0, s[10:11]
	global_load_dwordx4 v[74:77], v[24:25], off
	v_lshl_add_u64 v[24:25], v[12:13], 0, s[10:11]
	global_load_dwordx4 v[82:85], v[24:25], off
	v_lshl_add_u64 v[24:25], v[14:15], 0, s[10:11]
	global_load_dwordx4 v[86:89], v[24:25], off
	v_lshl_add_u64 v[24:25], v[16:17], 0, s[10:11]
	global_load_dwordx4 v[90:93], v[24:25], off
	v_and_b32_e32 v27, 0x5f, v0
	v_lshlrev_b32_e32 v28, 4, v22
	s_movk_i32 s10, 0x50
	v_or_b32_e32 v26, v21, v20
	v_mad_u32_u24 v24, v27, s10, v28
	v_mad_u32_u24 v25, v26, s10, v28
	ds_read_b128 v[98:101], v24 offset:23040
	ds_read_b128 v[102:105], v24 offset:30720
	ds_read_b128 v[118:121], v25 offset:2560
	ds_read_b128 v[110:113], v25
	ds_read_b128 v[106:109], v24 offset:33280
	ds_read_b128 v[94:97], v24 offset:20480
	ds_read_b128 v[122:125], v25 offset:12800
	ds_read_b128 v[114:117], v25 offset:10240
	v_mul_u32_u24_e32 v29, 0x50, v26
	v_add_u32_e32 v25, 0xa000, v23
	v_add_u32_e32 v26, 0xa000, v24
	v_add_u32_e32 v27, 0xa020, v24
	s_nop 7
	s_mov_b32 s10, 0
	v_add_u32_e32 v28, v28, v29

.LBB23_13:
	s_endpgm
	s_endpgm
	s_endpgm
	s_endpgm
	s_endpgm
	s_endpgm
	s_endpgm
	s_endpgm
	s_endpgm
	s_endpgm
	s_endpgm
	s_endpgm
	s_endpgm
	s_endpgm
	s_endpgm
	s_endpgm
	s_endpgm
	s_endpgm
	s_endpgm
	s_endpgm
	s_endpgm
	s_endpgm
	s_endpgm
	s_endpgm
	s_endpgm
	s_endpgm
	s_endpgm
	s_endpgm
	s_endpgm
	s_endpgm
	s_endpgm
	.section	.rodata,"a",@progbits
	.p2align	6, 0x0
